# combo3 plus non-temporal stores for the residual stream XRES written in P7 and P11
# speedup vs baseline: 1.0150x; 1.0049x over previous
.LBB0_1194:
	s_lshl_b32 s56, s55, 4
	v_add_u32_e32 v128, s56, v217
	v_ashrrev_i32_e32 v129, 31, v128
	v_lshlrev_b64 v[132:133], 12, v[128:129]
	v_lshl_add_u64 v[0:1], v[114:115], 0, v[132:133]
	global_load_dwordx4 v[138:141], v[0:1], off
	v_or_b32_e32 v126, 1, v128
	v_ashrrev_i32_e32 v127, 31, v126
	v_lshrrev_b32_e32 v6, 20, v129
	v_lshlrev_b64 v[130:131], 12, v[126:127]
	v_add_u32_e32 v10, v128, v6
	v_lshl_add_u64 v[4:5], v[114:115], 0, v[130:131]
	v_lshlrev_b64 v[2:3], 13, v[128:129]
	v_lshlrev_b64 v[8:9], 13, v[126:127]
	v_ashrrev_i32_e32 v10, 12, v10
	global_load_dwordx4 v[146:149], v[4:5], off
	v_lshl_add_u64 v[6:7], v[116:117], 0, v[2:3]
	global_load_dwordx4 v[162:165], v[0:1], off offset:1024
	global_load_dwordx4 v[170:173], v[0:1], off offset:2048
	global_load_dwordx4 v[104:107], v[0:1], off offset:3072
	global_load_dwordx4 v[92:95], v[6:7], off offset:16
	global_load_dwordx4 v[96:99], v[6:7], off
	s_nop 0
	global_load_dwordx4 v[0:3], v[6:7], off offset:2064
	global_load_dwordx4 v[88:91], v[6:7], off offset:2048
	v_lshl_add_u64 v[16:17], v[116:117], 0, v[8:9]
	global_load_dwordx4 v[166:169], v[4:5], off offset:1024
	v_mul_i32_i24_e32 v36, 6, v10
	global_load_dwordx4 v[100:103], v[4:5], off offset:2048
	global_load_dwordx4 v[72:75], v[4:5], off offset:3072
	global_load_dwordx4 v[24:27], v[16:17], off offset:16
	global_load_dwordx4 v[32:35], v[16:17], off
	global_load_dwordx4 v[8:11], v[16:17], off offset:2064
	global_load_dwordx4 v[20:23], v[16:17], off offset:2048
	v_lshl_add_u64 v[12:13], v[6:7], 0, s[34:35]
	v_lshl_add_u64 v[14:15], v[6:7], 0, s[36:37]
	v_add_co_u32_e32 v6, vcc, s17, v6
	v_ashrrev_i32_e32 v37, 31, v36
	s_nop 0
	v_addc_co_u32_e32 v7, vcc, 0, v7, vcc
	v_lshlrev_b64 v[36:37], 13, v[36:37]
	global_load_dwordx4 v[80:83], v[12:13], off offset:16
	global_load_dwordx4 v[84:87], v[6:7], off
	global_load_dwordx4 v[52:55], v[14:15], off offset:16
	global_load_dwordx4 v[76:79], v[6:7], off offset:2048
	v_add_co_u32_e32 v12, vcc, s17, v16
	v_lshl_add_u64 v[36:37], s[24:25], 0, v[36:37]
	s_nop 0
	v_addc_co_u32_e32 v13, vcc, 0, v17, vcc
	v_lshl_add_u64 v[134:135], v[36:37], 0, v[124:125]
	v_add_co_u32_e32 v46, vcc, s17, v134
	v_lshl_add_u64 v[4:5], v[16:17], 0, s[34:35]
	s_nop 0
	v_addc_co_u32_e32 v47, vcc, 0, v135, vcc
	v_lshl_add_u64 v[38:39], v[16:17], 0, s[36:37]
	v_lshl_add_u64 v[44:45], v[134:135], 0, s[34:35]
	v_lshl_add_u64 v[36:37], v[134:135], 0, s[36:37]
	v_add_co_u32_e32 v136, vcc, s16, v134
	global_load_dwordx4 v[16:19], v[4:5], off offset:16
	global_load_dwordx4 v[28:31], v[12:13], off
	s_nop 0
	global_load_dwordx4 v[4:7], v[38:39], off offset:16
	s_nop 0
	global_load_dwordx4 v[12:15], v[12:13], off offset:2048
	s_nop 0
	global_load_dwordx4 v[56:59], v[134:135], off offset:16
	global_load_dwordx4 v[68:71], v[134:135], off
	global_load_dwordx4 v[40:43], v[134:135], off offset:2064
	global_load_dwordx4 v[48:51], v[134:135], off offset:2048
	v_addc_co_u32_e32 v137, vcc, 0, v135, vcc
	global_load_dwordx4 v[36:39], v[36:37], off offset:16
	s_nop 0
	global_load_dwordx4 v[64:67], v[136:137], off offset:-4096
	global_load_dwordx4 v[60:63], v[44:45], off offset:16
	s_nop 0
	global_load_dwordx4 v[44:47], v[46:47], off offset:2048
	s_mov_b32 s28, 0
	s_waitcnt vmcnt(31)
	v_lshlrev_b32_e32 v196, 16, v141
	v_and_b32_e32 v197, 0xffff0000, v141
	v_lshlrev_b32_e32 v190, 16, v139
	v_and_b32_e32 v191, 0xffff0000, v139
	v_lshlrev_b32_e32 v188, 16, v138
	v_and_b32_e32 v189, 0xffff0000, v138
	v_lshlrev_b32_e32 v194, 16, v140
	v_and_b32_e32 v195, 0xffff0000, v140
	v_pk_mul_f32 v[198:199], v[196:197], v[196:197]
	v_pk_mul_f32 v[202:203], v[190:191], v[190:191]
	v_pk_mul_f32 v[204:205], v[188:189], v[188:189]
	v_pk_mul_f32 v[200:201], v[194:195], v[194:195]
	s_waitcnt vmcnt(21)
	v_lshlrev_b32_e32 v182, 16, v101
	v_and_b32_e32 v183, 0xffff0000, v101
	v_add_f32_e32 v101, v198, v199
	v_add_f32_e32 v112, v202, v203
	v_add_f32_e32 v198, v204, v205
	v_lshlrev_b32_e32 v244, 16, v162
	v_and_b32_e32 v245, 0xffff0000, v162
	v_add_f32_e32 v112, v198, v112
	v_add_f32_e32 v198, v200, v201
	v_lshlrev_b32_e32 v240, 16, v163
	v_and_b32_e32 v241, 0xffff0000, v163
	v_pk_mul_f32 v[246:247], v[244:245], v[244:245]
	v_add_f32_e32 v112, v198, v112
	v_lshlrev_b32_e32 v238, 16, v164
	v_and_b32_e32 v239, 0xffff0000, v164
	v_pk_mul_f32 v[242:243], v[240:241], v[240:241]
	v_add_f32_e32 v101, v101, v112
	v_add_f32_e32 v112, v246, v247
	v_lshlrev_b32_e32 v236, 16, v165
	v_and_b32_e32 v237, 0xffff0000, v165
	v_pk_mul_f32 v[214:215], v[238:239], v[238:239]
	v_add_f32_e32 v101, v112, v101
	v_add_f32_e32 v112, v242, v243
	v_pk_mul_f32 v[206:207], v[236:237], v[236:237]
	v_lshlrev_b32_e32 v224, 16, v170
	v_and_b32_e32 v225, 0xffff0000, v170
	v_add_f32_e32 v101, v112, v101
	v_add_f32_e32 v112, v214, v215
	v_lshlrev_b32_e32 v138, 16, v149
	v_and_b32_e32 v139, 0xffff0000, v149
	v_lshlrev_b32_e32 v140, 16, v148
	v_and_b32_e32 v141, 0xffff0000, v148
	v_lshlrev_b32_e32 v142, 16, v147
	v_and_b32_e32 v143, 0xffff0000, v147
	v_lshlrev_b32_e32 v144, 16, v146
	v_and_b32_e32 v145, 0xffff0000, v146
	v_lshlrev_b32_e32 v146, 16, v169
	v_and_b32_e32 v147, 0xffff0000, v169
	v_lshlrev_b32_e32 v148, 16, v168
	v_and_b32_e32 v149, 0xffff0000, v168
	v_lshlrev_b32_e32 v164, 16, v173
	v_and_b32_e32 v165, 0xffff0000, v173
	v_lshlrev_b32_e32 v168, 16, v172
	v_and_b32_e32 v169, 0xffff0000, v172
	v_lshlrev_b32_e32 v172, 16, v171
	v_and_b32_e32 v173, 0xffff0000, v171
	v_pk_mul_f32 v[170:171], v[224:225], v[224:225]
	v_and_b32_e32 v185, 0xffff0000, v107
	v_and_b32_e32 v209, 0xffff0000, v106
	v_add_f32_e32 v101, v112, v101
	v_add_f32_e32 v112, v206, v207
	v_pk_mul_f32 v[252:253], v[172:173], v[172:173]
	v_lshlrev_b32_e32 v184, 16, v107
	v_lshlrev_b32_e32 v208, 16, v106
	v_mov_b32_e32 v106, v185
	v_mov_b32_e32 v107, v209
	v_add_f32_e32 v101, v112, v101
	v_add_f32_e32 v112, v170, v171
	v_lshlrev_b32_e32 v150, 16, v167
	v_and_b32_e32 v151, 0xffff0000, v167
	v_lshlrev_b32_e32 v156, 16, v166
	v_and_b32_e32 v157, 0xffff0000, v166
	v_pk_mul_f32 v[250:251], v[168:169], v[168:169]
	v_lshlrev_b32_e32 v162, 16, v103
	v_and_b32_e32 v163, 0xffff0000, v103
	v_lshlrev_b32_e32 v166, 16, v102
	v_and_b32_e32 v167, 0xffff0000, v102
	v_mov_b32_e32 v102, v184
	v_mov_b32_e32 v103, v208
	v_pk_mul_f32 v[106:107], v[106:107], v[106:107]
	v_and_b32_e32 v211, 0xffff0000, v105
	v_and_b32_e32 v213, 0xffff0000, v104
	v_add_f32_e32 v101, v112, v101
	v_add_f32_e32 v112, v252, v253
	v_pk_mul_f32 v[248:249], v[164:165], v[164:165]
	v_pk_fma_f32 v[102:103], v[102:103], v[102:103], v[106:107]
	v_lshlrev_b32_e32 v210, 16, v105
	v_lshlrev_b32_e32 v212, 16, v104
	v_mov_b32_e32 v106, v211
	v_mov_b32_e32 v107, v213
	v_add_f32_e32 v101, v112, v101
	v_add_f32_e32 v112, v250, v251
	v_mov_b32_e32 v104, v210
	v_mov_b32_e32 v105, v212
	v_pk_mul_f32 v[106:107], v[106:107], v[106:107]
	v_add_f32_e32 v101, v112, v101
	v_add_f32_e32 v112, v248, v249
	v_pk_fma_f32 v[106:107], v[104:105], v[104:105], v[106:107]
	v_add_f32_e32 v101, v112, v101
	v_add_f32_e32 v101, v107, v101
	v_add_f32_e32 v101, v106, v101
	v_add_f32_e32 v101, v103, v101
	v_add_f32_e32 v101, v102, v101
	v_mov_b32_e32 v102, 0
	v_lshlrev_b32_e32 v206, 16, v100
	v_add_f32_dpp v101, v101, v101 quad_perm:[1,0,3,2] row_mask:0xf bank_mask:0xf bound_ctrl:1
	v_and_b32_e32 v207, 0xffff0000, v100
	s_waitcnt vmcnt(20)
	v_and_b32_e32 v243, 0xffff0000, v74
	v_add_f32_dpp v101, v101, v101 quad_perm:[2,3,0,1] row_mask:0xf bank_mask:0xf bound_ctrl:1
	v_lshlrev_b32_e32 v242, 16, v74
	v_and_b32_e32 v247, 0xffff0000, v72
	v_add_f32_dpp v101, v101, v101 row_half_mirror row_mask:0xf bank_mask:0xf bound_ctrl:1
	v_lshlrev_b32_e32 v246, 16, v72
	v_pk_mul_f32 v[158:159], v[142:143], v[142:143]
	v_add_f32_dpp v101, v101, v101 row_mirror row_mask:0xf bank_mask:0xf bound_ctrl:1
	v_pk_mul_f32 v[160:161], v[144:145], v[144:145]
	v_pk_mul_f32 v[154:155], v[140:141], v[140:141]
	v_mov_b32_dpp v102, v101 row_bcast:15 row_mask:0xa bank_mask:0xf
	v_add_f32_e32 v101, v101, v102
	v_mov_b32_e32 v102, 0
	v_pk_mul_f32 v[152:153], v[138:139], v[138:139]
	v_pk_mul_f32 v[180:181], v[156:157], v[156:157]
	v_mov_b32_dpp v102, v101 row_bcast:31 row_mask:0xc bank_mask:0xf
	v_add_f32_e32 v101, v101, v102
	v_pk_mul_f32 v[178:179], v[150:151], v[150:151]
	v_readlane_b32 s18, v101, 63
	v_pk_mul_f32 v[176:177], v[148:149], v[148:149]
	v_pk_mul_f32 v[174:175], v[146:147], v[146:147]
	v_fma_f32 v101, s18, v232, v229
	v_mul_f32_e32 v102, 0x4b800000, v101
	v_cmp_gt_f32_e32 vcc, s33, v101
	v_pk_mul_f32 v[214:215], v[206:207], v[206:207]
	v_pk_mul_f32 v[104:105], v[182:183], v[182:183]
	v_cndmask_b32_e32 v101, v101, v102, vcc
	v_rsq_f32_e32 v101, v101
	v_pk_mul_f32 v[192:193], v[166:167], v[166:167]
	v_pk_mul_f32 v[186:187], v[162:163], v[162:163]
	v_mul_f32_e32 v100, 0x45800000, v101
	v_cndmask_b32_e32 v106, v101, v100, vcc
	v_pk_mul_f32 v[170:171], v[106:107], v[224:225] op_sel_hi:[0,1]
	s_waitcnt vmcnt(2)
	v_pk_fma_f32 v[170:171], v[64:65], v[170:171], v[84:85]
	v_pk_mul_f32 v[84:85], v[106:107], v[172:173] op_sel_hi:[0,1]
	v_pk_fma_f32 v[172:173], v[66:67], v[84:85], v[86:87]
	v_pk_mul_f32 v[84:85], v[106:107], v[168:169] op_sel_hi:[0,1]
	v_pk_mul_f32 v[100:101], v[106:107], v[188:189] op_sel_hi:[0,1]
	s_waitcnt vmcnt(1)
	v_pk_fma_f32 v[168:169], v[60:61], v[84:85], v[80:81]
	v_pk_mul_f32 v[80:81], v[106:107], v[164:165] op_sel_hi:[0,1]
	v_pk_fma_f32 v[100:101], v[68:69], v[100:101], v[96:97]
	v_pk_mul_f32 v[96:97], v[106:107], v[190:191] op_sel_hi:[0,1]
	v_pk_fma_f32 v[164:165], v[62:63], v[80:81], v[82:83]
	v_pk_mul_f32 v[82:83], v[106:107], v[208:209] op_sel_hi:[0,1]
	v_pk_fma_f32 v[102:103], v[70:71], v[96:97], v[98:99]
	v_pk_mul_f32 v[96:97], v[106:107], v[194:195] op_sel_hi:[0,1]
	v_pk_fma_f32 v[82:83], v[36:37], v[82:83], v[52:53]
	v_and_b32_e32 v53, 0xffff0000, v75
	v_pk_fma_f32 v[98:99], v[56:57], v[96:97], v[92:93]
	v_pk_mul_f32 v[92:93], v[106:107], v[196:197] op_sel_hi:[0,1]
	v_lshlrev_b32_e32 v52, 16, v75
	v_mov_b32_e32 v86, v53
	v_mov_b32_e32 v87, v243
	v_pk_fma_f32 v[96:97], v[58:59], v[92:93], v[94:95]
	v_pk_mul_f32 v[92:93], v[106:107], v[244:245] op_sel_hi:[0,1]
	v_mov_b32_e32 v74, v52
	v_mov_b32_e32 v75, v242
	v_pk_mul_f32 v[86:87], v[86:87], v[86:87]
	v_and_b32_e32 v245, 0xffff0000, v73
	v_pk_fma_f32 v[92:93], v[48:49], v[92:93], v[88:89]
	v_pk_mul_f32 v[88:89], v[106:107], v[240:241] op_sel_hi:[0,1]
	v_pk_fma_f32 v[74:75], v[74:75], v[74:75], v[86:87]
	v_lshlrev_b32_e32 v244, 16, v73
	v_mov_b32_e32 v86, v245
	v_mov_b32_e32 v87, v247
	v_pk_fma_f32 v[94:95], v[50:51], v[88:89], v[90:91]
	v_pk_mul_f32 v[88:89], v[106:107], v[238:239] op_sel_hi:[0,1]
	v_pk_mul_f32 v[80:81], v[106:107], v[212:213] op_sel_hi:[0,1]
	v_mov_b32_e32 v72, v244
	v_mov_b32_e32 v73, v246
	v_pk_mul_f32 v[86:87], v[86:87], v[86:87]
	v_pk_fma_f32 v[90:91], v[40:41], v[88:89], v[0:1]
	v_pk_mul_f32 v[0:1], v[106:107], v[236:237] op_sel_hi:[0,1]
	s_waitcnt vmcnt(0)
	v_pk_fma_f32 v[80:81], v[44:45], v[80:81], v[76:77]
	v_pk_mul_f32 v[76:77], v[106:107], v[210:211] op_sel_hi:[0,1]
	v_pk_fma_f32 v[72:73], v[72:73], v[72:73], v[86:87]
	v_add_f32_e32 v87, v158, v159
	v_add_f32_e32 v107, v160, v161
	v_add_f32_e32 v87, v107, v87
	v_add_f32_e32 v107, v154, v155
	v_add_f32_e32 v86, v152, v153
	v_add_f32_e32 v87, v107, v87
	v_add_f32_e32 v86, v86, v87
	v_add_f32_e32 v87, v180, v181
	v_add_f32_e32 v86, v87, v86
	v_add_f32_e32 v87, v178, v179
	v_add_f32_e32 v86, v87, v86
	v_add_f32_e32 v87, v176, v177
	v_add_f32_e32 v86, v87, v86
	v_add_f32_e32 v87, v174, v175
	v_add_f32_e32 v86, v87, v86
	v_add_f32_e32 v87, v214, v215
	v_add_f32_e32 v86, v87, v86
	v_add_f32_e32 v87, v104, v105
	v_add_f32_e32 v86, v87, v86
	v_add_f32_e32 v87, v192, v193
	v_add_f32_e32 v86, v87, v86
	v_add_f32_e32 v87, v186, v187
	v_add_f32_e32 v86, v87, v86
	v_add_f32_e32 v73, v73, v86
	v_add_f32_e32 v72, v72, v73
	v_add_f32_e32 v72, v75, v72
	v_add_f32_e32 v72, v74, v72
	v_mov_b32_e32 v73, 0
	v_pk_fma_f32 v[88:89], v[42:43], v[0:1], v[2:3]
	v_add_f32_dpp v72, v72, v72 quad_perm:[1,0,3,2] row_mask:0xf bank_mask:0xf bound_ctrl:1
	v_lshl_add_u64 v[0:1], v[134:135], 0, s[48:49]
	v_lshl_add_u64 v[208:209], v[134:135], 0, s[38:39]
	v_add_f32_dpp v72, v72, v72 quad_perm:[2,3,0,1] row_mask:0xf bank_mask:0xf bound_ctrl:1
	global_load_dwordx4 v[0:3], v[0:1], off offset:16
	v_pk_fma_f32 v[84:85], v[46:47], v[76:77], v[78:79]
	v_add_f32_dpp v72, v72, v72 row_half_mirror row_mask:0xf bank_mask:0xf bound_ctrl:1
	global_load_dwordx4 v[76:79], v[208:209], off offset:16
	v_pk_mul_f32 v[188:189], v[100:101], v[100:101]
	v_add_f32_dpp v72, v72, v72 row_mirror row_mask:0xf bank_mask:0xf bound_ctrl:1
	v_pk_mul_f32 v[190:191], v[102:103], v[102:103]
	v_add_f32_e32 v112, v188, v189
	v_mov_b32_dpp v73, v72 row_bcast:15 row_mask:0xa bank_mask:0xf
	v_add_f32_e32 v72, v72, v73
	v_mov_b32_e32 v73, 0
	v_add_f32_e32 v112, v190, v112
	v_pk_mul_f32 v[194:195], v[98:99], v[98:99]
	v_mov_b32_dpp v73, v72 row_bcast:31 row_mask:0xc bank_mask:0xf
	v_add_f32_e32 v72, v72, v73
	v_add_f32_e32 v112, v191, v112
	v_readlane_b32 s18, v72, 63
	v_add_f32_e32 v112, v194, v112
	v_pk_mul_f32 v[196:197], v[96:97], v[96:97]
	v_fma_f32 v72, s18, v232, v229
	v_mul_f32_e32 v73, 0x4b800000, v72
	v_cmp_gt_f32_e32 vcc, s33, v72
	v_add_f32_e32 v112, v195, v112
	v_add_f32_e32 v112, v196, v112
	v_cndmask_b32_e32 v72, v72, v73, vcc
	v_rsq_f32_e32 v74, v72
	v_pk_mul_f32 v[72:73], v[106:107], v[184:185] op_sel_hi:[0,1]
	v_pk_fma_f32 v[154:155], v[38:39], v[72:73], v[54:55]
	v_pk_mul_f32 v[198:199], v[92:93], v[92:93]
	v_mul_f32_e32 v54, 0x45800000, v74
	v_cndmask_b32_e32 v54, v74, v54, vcc
	v_pk_mul_f32 v[72:73], v[54:55], v[144:145] op_sel_hi:[0,1]
	v_pk_fma_f32 v[144:145], v[68:69], v[72:73], v[32:33]
	v_pk_mul_f32 v[32:33], v[54:55], v[142:143] op_sel_hi:[0,1]
	v_pk_fma_f32 v[142:143], v[70:71], v[32:33], v[34:35]
	v_pk_mul_f32 v[32:33], v[54:55], v[140:141] op_sel_hi:[0,1]
	v_pk_fma_f32 v[152:153], v[56:57], v[32:33], v[24:25]
	v_pk_mul_f32 v[24:25], v[54:55], v[138:139] op_sel_hi:[0,1]
	v_pk_fma_f32 v[140:141], v[58:59], v[24:25], v[26:27]
	v_pk_mul_f32 v[24:25], v[54:55], v[156:157] op_sel_hi:[0,1]
	v_pk_fma_f32 v[104:105], v[48:49], v[24:25], v[20:21]
	v_pk_mul_f32 v[20:21], v[54:55], v[150:151] op_sel_hi:[0,1]
	v_pk_fma_f32 v[106:107], v[50:51], v[20:21], v[22:23]
	v_pk_mul_f32 v[20:21], v[54:55], v[148:149] op_sel_hi:[0,1]
	v_pk_fma_f32 v[138:139], v[40:41], v[20:21], v[8:9]
	v_pk_mul_f32 v[8:9], v[54:55], v[146:147] op_sel_hi:[0,1]
	v_pk_fma_f32 v[86:87], v[42:43], v[8:9], v[10:11]
	v_pk_mul_f32 v[8:9], v[54:55], v[206:207] op_sel_hi:[0,1]
	v_pk_fma_f32 v[70:71], v[64:65], v[8:9], v[28:29]
	v_pk_mul_f32 v[8:9], v[54:55], v[182:183] op_sel_hi:[0,1]
	v_pk_fma_f32 v[72:73], v[66:67], v[8:9], v[30:31]
	v_pk_mul_f32 v[8:9], v[54:55], v[166:167] op_sel_hi:[0,1]
	v_pk_fma_f32 v[74:75], v[60:61], v[8:9], v[16:17]
	v_pk_mul_f32 v[8:9], v[54:55], v[162:163] op_sel_hi:[0,1]
	v_pk_fma_f32 v[68:69], v[62:63], v[8:9], v[18:19]
	v_pk_mul_f32 v[8:9], v[54:55], v[246:247] op_sel_hi:[0,1]
	v_pk_fma_f32 v[62:63], v[44:45], v[8:9], v[12:13]
	v_pk_mul_f32 v[8:9], v[54:55], v[244:245] op_sel_hi:[0,1]
	v_pk_fma_f32 v[64:65], v[46:47], v[8:9], v[14:15]
	v_pk_mul_f32 v[8:9], v[54:55], v[242:243] op_sel_hi:[0,1]
	v_pk_fma_f32 v[66:67], v[36:37], v[8:9], v[4:5]
	v_pk_mul_f32 v[4:5], v[54:55], v[52:53] op_sel_hi:[0,1]
	v_add_co_u32_e32 v12, vcc, s51, v134
	v_pk_fma_f32 v[60:61], v[38:39], v[4:5], v[6:7]
	v_lshl_add_u64 v[4:5], v[134:135], 0, s[40:41]
	v_addc_co_u32_e32 v13, vcc, 0, v135, vcc
	global_load_dwordx4 v[52:55], v[136:137], off
	global_load_dwordx4 v[56:59], v[12:13], off offset:-4096
	global_load_dwordx4 v[32:35], v[208:209], off offset:2064
	global_load_dwordx4 v[40:43], v[208:209], off offset:2048
	global_load_dwordx4 v[48:51], v[4:5], off offset:16
	global_load_dwordx4 v[44:47], v[4:5], off offset:2048
	v_lshl_add_u64 v[6:7], v[134:135], 0, s[42:43]
	global_load_dwordx4 v[36:39], v[4:5], off offset:2064
	global_load_dwordx4 v[16:19], v[6:7], off offset:16
	v_add_co_u32_e32 v8, vcc, s50, v134
	v_lshl_add_u64 v[4:5], v[134:135], 0, s[44:45]
	s_nop 0
	v_addc_co_u32_e32 v9, vcc, 0, v135, vcc
	v_lshl_add_u64 v[6:7], v[134:135], 0, s[46:47]
	global_load_dwordx4 v[24:27], v[8:9], off
	s_nop 0
	global_load_dwordx4 v[8:11], v[8:9], off offset:2048
	s_nop 0
	global_load_dwordx4 v[20:23], v[4:5], off offset:16
	s_nop 0
	global_load_dwordx4 v[4:7], v[6:7], off offset:16
	s_nop 0
	global_load_dwordx4 v[28:31], v[12:13], off
	s_nop 0
	global_load_dwordx4 v[12:15], v[12:13], off offset:2048
	v_lshl_add_u64 v[136:137], v[118:119], 0, v[132:133]
	v_cvt_pk_bf16_f32 v132, v100, v101
	v_cvt_pk_bf16_f32 v133, v102, v103
	v_cvt_pk_bf16_f32 v134, v98, v99
	v_cvt_pk_bf16_f32 v135, v96, v97
	global_store_dwordx4 v[136:137], v[132:135], off nt
	v_add_f32_e32 v112, v197, v112
	v_pk_mul_f32 v[160:161], v[144:145], v[144:145]
	v_cvt_pk_bf16_f32 v132, v92, v93
	v_cvt_pk_bf16_f32 v133, v94, v95
	v_cvt_pk_bf16_f32 v134, v90, v91
	v_cvt_pk_bf16_f32 v135, v88, v89
	global_store_dwordx4 v[136:137], v[132:135], off offset:1024 nt
	v_add_f32_e32 v112, v198, v112
	v_pk_mul_f32 v[200:201], v[94:95], v[94:95]
	v_cvt_pk_bf16_f32 v132, v170, v171
	v_cvt_pk_bf16_f32 v133, v172, v173
	v_cvt_pk_bf16_f32 v134, v168, v169
	v_cvt_pk_bf16_f32 v135, v164, v165
	global_store_dwordx4 v[136:137], v[132:135], off offset:2048 nt
	v_pk_mul_f32 v[174:175], v[142:143], v[142:143]
	v_add_f32_e32 v112, v199, v112
	v_cvt_pk_bf16_f32 v132, v80, v81
	v_cvt_pk_bf16_f32 v133, v84, v85
	v_cvt_pk_bf16_f32 v134, v82, v83
	v_cvt_pk_bf16_f32 v135, v154, v155
	global_store_dwordx4 v[136:137], v[132:135], off offset:3072 nt
	v_add_f32_e32 v136, v160, v161
	v_add_f32_e32 v112, v200, v112
	v_add_f32_e32 v136, v174, v136
	v_pk_mul_f32 v[202:203], v[90:91], v[90:91]
	v_pk_mul_f32 v[176:177], v[152:153], v[152:153]
	v_add_f32_e32 v112, v201, v112
	v_add_f32_e32 v136, v175, v136
	v_add_f32_e32 v112, v202, v112
	v_add_f32_e32 v136, v176, v136
	v_pk_mul_f32 v[204:205], v[88:89], v[88:89]
	v_pk_mul_f32 v[178:179], v[140:141], v[140:141]
	v_add_f32_e32 v112, v203, v112
	v_add_f32_e32 v136, v177, v136
	v_add_f32_e32 v112, v204, v112
	v_add_f32_e32 v136, v178, v136
	v_pk_mul_f32 v[224:225], v[170:171], v[170:171]
	v_pk_mul_f32 v[156:157], v[104:105], v[104:105]
	v_add_f32_e32 v112, v205, v112
	v_add_f32_e32 v136, v179, v136
	v_add_f32_e32 v112, v224, v112
	v_add_f32_e32 v136, v156, v136
	v_pk_mul_f32 v[236:237], v[172:173], v[172:173]
	v_pk_mul_f32 v[150:151], v[106:107], v[106:107]
	v_add_f32_e32 v112, v225, v112
	v_add_f32_e32 v136, v157, v136
	v_add_f32_e32 v112, v236, v112
	v_add_f32_e32 v136, v150, v136
	v_pk_mul_f32 v[238:239], v[168:169], v[168:169]
	v_pk_mul_f32 v[148:149], v[138:139], v[138:139]
	v_add_f32_e32 v112, v237, v112
	v_add_f32_e32 v136, v151, v136
	v_add_f32_e32 v112, v238, v112
	v_add_f32_e32 v136, v148, v136
	v_pk_mul_f32 v[240:241], v[164:165], v[164:165]
	v_pk_mul_f32 v[146:147], v[86:87], v[86:87]
	v_add_f32_e32 v112, v239, v112
	v_add_f32_e32 v136, v149, v136
	v_add_f32_e32 v112, v240, v112
	v_add_f32_e32 v136, v146, v136
	v_pk_mul_f32 v[212:213], v[80:81], v[80:81]
	v_pk_mul_f32 v[180:181], v[70:71], v[70:71]
	v_add_f32_e32 v112, v241, v112
	v_add_f32_e32 v136, v147, v136
	v_add_f32_e32 v112, v212, v112
	v_add_f32_e32 v136, v180, v136
	v_pk_mul_f32 v[210:211], v[84:85], v[84:85]
	v_pk_mul_f32 v[182:183], v[72:73], v[72:73]
	v_add_f32_e32 v112, v213, v112
	v_add_f32_e32 v136, v181, v136
	v_add_f32_e32 v112, v210, v112
	v_add_f32_e32 v136, v182, v136
	v_pk_mul_f32 v[158:159], v[82:83], v[82:83]
	v_pk_mul_f32 v[166:167], v[74:75], v[74:75]
	v_add_f32_e32 v112, v211, v112
	v_add_f32_e32 v136, v183, v136
	v_add_f32_e32 v112, v158, v112
	v_add_f32_e32 v136, v166, v136
	v_pk_mul_f32 v[162:163], v[68:69], v[68:69]
	v_pk_mul_f32 v[206:207], v[154:155], v[154:155]
	v_add_f32_e32 v112, v159, v112
	v_add_f32_e32 v136, v167, v136
	v_add_f32_e32 v112, v206, v112
	v_add_f32_e32 v136, v162, v136
	v_pk_mul_f32 v[184:185], v[62:63], v[62:63]
	v_add_f32_e32 v112, v207, v112
	v_add_f32_e32 v136, v163, v136
	v_add_f32_e32 v136, v184, v136
	v_add_f32_dpp v112, v112, v112 quad_perm:[1,0,3,2] row_mask:0xf bank_mask:0xf bound_ctrl:1
	v_pk_mul_f32 v[186:187], v[64:65], v[64:65]
	v_add_f32_e32 v136, v185, v136
	v_add_f32_dpp v112, v112, v112 quad_perm:[2,3,0,1] row_mask:0xf bank_mask:0xf bound_ctrl:1
	v_add_f32_e32 v136, v186, v136
	v_pk_mul_f32 v[192:193], v[66:67], v[66:67]
	v_add_f32_dpp v112, v112, v112 row_half_mirror row_mask:0xf bank_mask:0xf bound_ctrl:1
	v_add_f32_e32 v136, v187, v136
	v_mov_b32_e32 v137, 0
	v_add_f32_dpp v112, v112, v112 row_mirror row_mask:0xf bank_mask:0xf bound_ctrl:1
	v_add_f32_e32 v136, v192, v136
	v_pk_mul_f32 v[214:215], v[60:61], v[60:61]
	v_mov_b32_dpp v137, v112 row_bcast:15 row_mask:0xa bank_mask:0xf
	v_add_f32_e32 v136, v193, v136
	v_add_f32_e32 v112, v112, v137
	v_mov_b32_e32 v137, 0
	v_add_f32_e32 v136, v214, v136
	v_add_f32_e32 v136, v215, v136
	v_mov_b32_dpp v137, v112 row_bcast:31 row_mask:0xc bank_mask:0xf
	v_add_f32_e32 v112, v112, v137
	v_lshl_add_u64 v[134:135], v[118:119], 0, v[130:131]
	v_readlane_b32 s18, v112, 63
	v_add_f32_dpp v112, v136, v136 quad_perm:[1,0,3,2] row_mask:0xf bank_mask:0xf bound_ctrl:1
	v_mov_b32_e32 v136, 0
	v_cvt_pk_bf16_f32 v130, v144, v145
	v_add_f32_dpp v112, v112, v112 quad_perm:[2,3,0,1] row_mask:0xf bank_mask:0xf bound_ctrl:1
	v_cvt_pk_bf16_f32 v131, v142, v143
	v_cvt_pk_bf16_f32 v132, v152, v153
	v_add_f32_dpp v112, v112, v112 row_half_mirror row_mask:0xf bank_mask:0xf bound_ctrl:1
	v_cvt_pk_bf16_f32 v133, v140, v141
	global_store_dwordx4 v[134:135], v[130:133], off nt
	v_add_f32_dpp v112, v112, v112 row_mirror row_mask:0xf bank_mask:0xf bound_ctrl:1
	s_nop 0
	v_cvt_pk_bf16_f32 v130, v104, v105
	v_mov_b32_dpp v136, v112 row_bcast:15 row_mask:0xa bank_mask:0xf
	v_add_f32_e32 v112, v112, v136
	v_mov_b32_e32 v136, 0
	v_cvt_pk_bf16_f32 v131, v106, v107
	v_cvt_pk_bf16_f32 v132, v138, v139
	v_mov_b32_dpp v136, v112 row_bcast:31 row_mask:0xc bank_mask:0xf
	v_add_f32_e32 v112, v112, v136
	v_cvt_pk_bf16_f32 v133, v86, v87
	v_readlane_b32 s19, v112, 63
	v_fma_f32 v112, s18, v232, v229
	v_mul_f32_e32 v136, 0x4b800000, v112
	v_cmp_gt_f32_e32 vcc, s33, v112
	global_store_dwordx4 v[134:135], v[130:133], off offset:1024 nt
	s_nop 0
	v_cndmask_b32_e32 v112, v112, v136, vcc
	v_fma_f32 v136, s19, v232, v229
	v_rsq_f32_e32 v112, v112
	v_mul_f32_e32 v137, 0x4b800000, v136
	v_cmp_gt_f32_e64 s[18:19], s33, v136
	v_cvt_pk_bf16_f32 v130, v70, v71
	v_cvt_pk_bf16_f32 v131, v72, v73
	v_cndmask_b32_e64 v136, v136, v137, s[18:19]
	v_cvt_pk_bf16_f32 v132, v74, v75
	v_cvt_pk_bf16_f32 v133, v68, v69
	v_rsq_f32_e32 v136, v136
	global_store_dwordx4 v[134:135], v[130:133], off offset:2048 nt
	v_mov_b32_e32 v137, 0
	s_nop 0
	v_cvt_pk_bf16_f32 v130, v62, v63
	v_cvt_pk_bf16_f32 v131, v64, v65
	v_cvt_pk_bf16_f32 v132, v66, v67
	v_cvt_pk_bf16_f32 v133, v60, v61
	global_store_dwordx4 v[134:135], v[130:133], off offset:3072 nt
	v_lshlrev_b64 v[134:135], 11, v[128:129]
	v_lshl_add_u64 v[134:135], v[122:123], 0, v[134:135]
	v_mul_f32_e32 v130, 0x45800000, v112
	v_cndmask_b32_e32 v132, v112, v130, vcc
	v_mul_f32_e32 v112, 0x45800000, v136
	v_pk_mul_f32 v[100:101], v[100:101], v[132:133] op_sel_hi:[1,0]
	v_pk_mul_f32 v[98:99], v[98:99], v[132:133] op_sel_hi:[1,0]
	v_pk_mul_f32 v[96:97], v[96:97], v[132:133] op_sel_hi:[1,0]
	v_pk_mul_f32 v[92:93], v[92:93], v[132:133] op_sel_hi:[1,0]
	v_pk_mul_f32 v[90:91], v[90:91], v[132:133] op_sel_hi:[1,0]
	v_cndmask_b32_e64 v112, v136, v112, s[18:19]
	s_waitcnt vmcnt(20)
	v_pk_fma_f32 v[100:101], v[52:53], v[100:101], v[56:57]
	s_waitcnt vmcnt(17)
	v_pk_fma_f32 v[128:129], v[76:77], v[98:99], v[48:49]
	v_mov_b32_e32 v136, 0
	v_pk_fma_f32 v[130:131], v[78:79], v[96:97], v[50:51]
	s_waitcnt vmcnt(16)
	v_pk_fma_f32 v[92:93], v[40:41], v[92:93], v[44:45]
	s_waitcnt vmcnt(15)
	v_pk_fma_f32 v[96:97], v[32:33], v[90:91], v[36:37]
	v_mov_b32_e32 v90, 0
	v_mov_b32_e32 v91, 0
	v_cvt_pk_fp8_f32 v136, v100, v101
	v_cvt_pk_fp8_f32 v137, v128, v129
	v_cvt_pk_fp8_f32 v90, v92, v93
	v_cvt_pk_fp8_f32 v91, v96, v97
	v_pk_mul_f32 v[102:103], v[102:103], v[132:133] op_sel_hi:[1,0]
	v_pk_mul_f32 v[94:95], v[94:95], v[132:133] op_sel_hi:[1,0]
	v_pk_mul_f32 v[88:89], v[88:89], v[132:133] op_sel_hi:[1,0]
	v_pk_fma_f32 v[102:103], v[54:55], v[102:103], v[58:59]
	v_pk_fma_f32 v[94:95], v[42:43], v[94:95], v[46:47]
	v_pk_fma_f32 v[98:99], v[34:35], v[88:89], v[38:39]
	v_cvt_pk_fp8_f32 v136, v102, v103 op_sel:[0,0,1]
	v_cvt_pk_fp8_f32 v137, v130, v131 op_sel:[0,0,1]
	v_cvt_pk_fp8_f32 v90, v94, v95 op_sel:[0,0,1]
	v_cvt_pk_fp8_f32 v91, v98, v99 op_sel:[0,0,1]
	v_pk_mul_f32 v[80:81], v[80:81], v[132:133] op_sel_hi:[1,0]
	global_store_dwordx2 v[134:135], v[136:137], off
	ds_write_b128 v222, v[100:103]
	ds_write_b128 v222, v[128:131] offset:16
	global_store_dwordx2 v[134:135], v[90:91], off offset:512
	ds_write_b128 v222, v[92:95] offset:2048
	ds_write_b128 v222, v[96:99] offset:2064
	s_waitcnt vmcnt(10)
	v_pk_fma_f32 v[96:97], v[8:9], v[80:81], v[12:13]
	v_pk_mul_f32 v[80:81], v[84:85], v[132:133] op_sel_hi:[1,0]
	v_pk_mul_f32 v[88:89], v[170:171], v[132:133] op_sel_hi:[1,0]
	v_pk_mul_f32 v[92:93], v[168:169], v[132:133] op_sel_hi:[1,0]
	v_pk_fma_f32 v[98:99], v[10:11], v[80:81], v[14:15]
	v_pk_mul_f32 v[80:81], v[82:83], v[132:133] op_sel_hi:[1,0]
	v_pk_fma_f32 v[88:89], v[24:25], v[88:89], v[28:29]
	v_pk_fma_f32 v[92:93], v[16:17], v[92:93], v[20:21]
	v_mov_b32_e32 v100, 0
	v_mov_b32_e32 v101, 0
	v_pk_fma_f32 v[80:81], v[4:5], v[80:81], v[0:1]
	v_mov_b32_e32 v84, 0
	v_mov_b32_e32 v85, 0
	v_cvt_pk_fp8_f32 v100, v88, v89
	v_cvt_pk_fp8_f32 v101, v92, v93
	v_cvt_pk_fp8_f32 v84, v96, v97
	v_cvt_pk_fp8_f32 v85, v80, v81
	v_pk_mul_f32 v[90:91], v[172:173], v[132:133] op_sel_hi:[1,0]
	v_pk_mul_f32 v[94:95], v[164:165], v[132:133] op_sel_hi:[1,0]
	v_pk_mul_f32 v[82:83], v[154:155], v[132:133] op_sel_hi:[1,0]
	v_pk_fma_f32 v[90:91], v[26:27], v[90:91], v[30:31]
	v_pk_fma_f32 v[94:95], v[18:19], v[94:95], v[22:23]
	v_pk_fma_f32 v[82:83], v[6:7], v[82:83], v[2:3]
	v_cvt_pk_fp8_f32 v100, v90, v91 op_sel:[0,0,1]
	v_cvt_pk_fp8_f32 v101, v94, v95 op_sel:[0,0,1]
	v_cvt_pk_fp8_f32 v84, v98, v99 op_sel:[0,0,1]
	v_cvt_pk_fp8_f32 v85, v82, v83 op_sel:[0,0,1]
	v_readfirstlane_b32 s18, v109
	global_store_dwordx2 v[134:135], v[100:101], off offset:1024
	ds_write_b128 v222, v[88:91] offset:4096
	ds_write_b128 v222, v[92:95] offset:4112
	global_store_dwordx2 v[134:135], v[84:85], off offset:1536
	ds_write_b128 v222, v[96:99] offset:6144
	ds_write_b128 v222, v[80:83] offset:6160
	v_pk_mul_f32 v[82:83], v[144:145], v[112:113] op_sel_hi:[1,0]
	v_lshlrev_b64 v[80:81], 11, v[126:127]
	v_pk_fma_f32 v[52:53], v[52:53], v[82:83], v[56:57]
	v_pk_mul_f32 v[56:57], v[142:143], v[112:113] op_sel_hi:[1,0]
	s_ashr_i32 s19, s18, 31
	v_pk_fma_f32 v[54:55], v[54:55], v[56:57], v[58:59]
	v_pk_mul_f32 v[56:57], v[152:153], v[112:113] op_sel_hi:[1,0]
	v_pk_mul_f32 v[58:59], v[140:141], v[112:113] op_sel_hi:[1,0]
	v_pk_fma_f32 v[48:49], v[76:77], v[56:57], v[48:49]
	v_pk_mul_f32 v[76:77], v[104:105], v[112:113] op_sel_hi:[1,0]
	v_mov_b32_e32 v56, 0
	v_pk_fma_f32 v[40:41], v[40:41], v[76:77], v[44:45]
	v_pk_mul_f32 v[44:45], v[106:107], v[112:113] op_sel_hi:[1,0]
	v_mov_b32_e32 v57, 0
	v_pk_fma_f32 v[42:43], v[42:43], v[44:45], v[46:47]
	v_pk_mul_f32 v[44:45], v[138:139], v[112:113] op_sel_hi:[1,0]
	v_cvt_pk_fp8_f32 v56, v52, v53
	v_pk_fma_f32 v[32:33], v[32:33], v[44:45], v[36:37]
	v_mov_b32_e32 v36, 0
	v_mov_b32_e32 v37, 0
	v_cvt_pk_fp8_f32 v57, v48, v49
	v_cvt_pk_fp8_f32 v36, v40, v41
	v_cvt_pk_fp8_f32 v37, v32, v33
	v_pk_mul_f32 v[44:45], v[86:87], v[112:113] op_sel_hi:[1,0]
	v_pk_fma_f32 v[50:51], v[78:79], v[58:59], v[50:51]
	v_pk_fma_f32 v[34:35], v[34:35], v[44:45], v[38:39]
	v_cvt_pk_fp8_f32 v56, v54, v55 op_sel:[0,0,1]
	v_cvt_pk_fp8_f32 v57, v50, v51 op_sel:[0,0,1]
	v_cvt_pk_fp8_f32 v36, v42, v43 op_sel:[0,0,1]
	v_cvt_pk_fp8_f32 v37, v34, v35 op_sel:[0,0,1]
	v_lshl_add_u64 v[58:59], v[122:123], 0, v[80:81]
	global_store_dwordx2 v[58:59], v[56:57], off
	ds_write_b128 v222, v[52:55] offset:8208
	ds_write_b128 v222, v[48:51] offset:8224
	global_store_dwordx2 v[58:59], v[36:37], off offset:512
	ds_write_b128 v222, v[40:43] offset:10256
	ds_write_b128 v222, v[32:35] offset:10272
	v_pk_mul_f32 v[32:33], v[70:71], v[112:113] op_sel_hi:[1,0]
	s_lshl_b64 s[18:19], s[18:19], 16
	v_pk_fma_f32 v[24:25], v[24:25], v[32:33], v[28:29]
	v_pk_mul_f32 v[28:29], v[72:73], v[112:113] op_sel_hi:[1,0]
	s_add_u32 s18, s22, s18
	v_pk_fma_f32 v[26:27], v[26:27], v[28:29], v[30:31]
	v_pk_mul_f32 v[28:29], v[74:75], v[112:113] op_sel_hi:[1,0]
	s_addc_u32 s19, s23, s19
	v_pk_fma_f32 v[16:17], v[16:17], v[28:29], v[20:21]
	v_pk_mul_f32 v[28:29], v[68:69], v[112:113] op_sel_hi:[1,0]
	v_mov_b32_e32 v20, 0
	v_pk_fma_f32 v[18:19], v[18:19], v[28:29], v[22:23]
	v_pk_mul_f32 v[22:23], v[62:63], v[112:113] op_sel_hi:[1,0]
	v_mov_b32_e32 v21, 0
	v_pk_fma_f32 v[8:9], v[8:9], v[22:23], v[12:13]
	v_pk_mul_f32 v[12:13], v[64:65], v[112:113] op_sel_hi:[1,0]
	v_cvt_pk_fp8_f32 v20, v24, v25
	v_pk_fma_f32 v[10:11], v[10:11], v[12:13], v[14:15]
	v_pk_mul_f32 v[12:13], v[66:67], v[112:113] op_sel_hi:[1,0]
	v_cvt_pk_fp8_f32 v21, v16, v17
	v_pk_fma_f32 v[0:1], v[4:5], v[12:13], v[0:1]
	v_mov_b32_e32 v4, 0
	v_mov_b32_e32 v5, 0
	v_cvt_pk_fp8_f32 v4, v8, v9
	v_cvt_pk_fp8_f32 v5, v0, v1
	v_pk_mul_f32 v[12:13], v[60:61], v[112:113] op_sel_hi:[1,0]
	v_cvt_pk_fp8_f32 v20, v26, v27 op_sel:[0,0,1]
	v_pk_fma_f32 v[2:3], v[6:7], v[12:13], v[2:3]
	v_cvt_pk_fp8_f32 v21, v18, v19 op_sel:[0,0,1]
	v_cvt_pk_fp8_f32 v4, v10, v11 op_sel:[0,0,1]
	v_cvt_pk_fp8_f32 v5, v2, v3 op_sel:[0,0,1]
	v_mov_b32_e32 v112, v218
	global_store_dwordx2 v[58:59], v[20:21], off offset:1024
	ds_write_b128 v222, v[24:27] offset:12304
	ds_write_b128 v222, v[16:19] offset:12320
	global_store_dwordx2 v[58:59], v[4:5], off offset:1536
	ds_write_b128 v222, v[8:11] offset:14352
	ds_write_b128 v222, v[0:3] offset:14368
	global_load_dwordx4 v[0:3], v112, s[18:19]
	global_load_dwordx4 v[4:7], v112, s[18:19] offset:1024
	global_load_dwordx4 v[8:11], v112, s[18:19] offset:2048
	global_load_dwordx4 v[12:15], v112, s[18:19] offset:3072
	v_lshl_add_u64 v[16:17], s[18:19], 0, v[112:113]
	v_add_co_u32_e32 v28, vcc, s17, v16
	v_mov_b32_e32 v112, v219
	s_nop 0
	v_addc_co_u32_e32 v29, vcc, 0, v17, vcc
	global_load_dwordx4 v[16:19], v[28:29], off
	global_load_dwordx4 v[20:23], v[28:29], off offset:1024
	global_load_dwordx4 v[24:27], v[28:29], off offset:2048
	s_nop 0
	global_load_dwordx4 v[28:31], v[28:29], off offset:3072
	s_waitcnt lgkmcnt(0)
	s_barrier
	ds_read2_b32 v[44:45], v220 offset1:4
	s_waitcnt vmcnt(7) lgkmcnt(0)
	v_mfma_f32_16x16x4_f32 v[32:35], v44, v0, 0
	ds_read2_b32 v[52:53], v220 offset0:24 offset1:28
	v_mfma_f32_16x16x4_f32 v[36:39], v44, v1, 0
	v_mfma_f32_16x16x4_f32 v[40:43], v44, v2, 0
	v_mfma_f32_16x16x4_f32 v[0:3], v44, v3, 0
	s_waitcnt vmcnt(6)
	v_mfma_f32_16x16x4_f32 v[32:35], v45, v4, v[32:35]
	v_mfma_f32_16x16x4_f32 v[36:39], v45, v5, v[36:39]
	v_mfma_f32_16x16x4_f32 v[40:43], v45, v6, v[40:43]
	v_mfma_f32_16x16x4_f32 v[0:3], v45, v7, v[0:3]
	ds_read2_b32 v[44:45], v220 offset0:8 offset1:12
	s_waitcnt vmcnt(5) lgkmcnt(0)
	v_mfma_f32_16x16x4_f32 v[4:7], v44, v8, v[32:35]
	v_mfma_f32_16x16x4_f32 v[32:35], v44, v9, v[36:39]
	v_mfma_f32_16x16x4_f32 v[36:39], v44, v10, v[40:43]
	v_mfma_f32_16x16x4_f32 v[0:3], v44, v11, v[0:3]
	s_waitcnt vmcnt(4)
	v_mfma_f32_16x16x4_f32 v[8:11], v45, v13, v[32:35]
	v_mfma_f32_16x16x4_f32 v[32:35], v45, v14, v[36:39]
	s_nop 5
	ds_read2_b32 v[36:37], v220 offset0:16 offset1:20
	v_mfma_f32_16x16x4_f32 v[4:7], v45, v12, v[4:7]
	v_mfma_f32_16x16x4_f32 v[0:3], v45, v15, v[0:3]
	s_waitcnt vmcnt(3) lgkmcnt(0)
	v_mfma_f32_16x16x4_f32 v[4:7], v36, v16, v[4:7]
	v_mfma_f32_16x16x4_f32 v[8:11], v36, v17, v[8:11]
	v_mfma_f32_16x16x4_f32 v[12:15], v36, v18, v[32:35]
	v_mfma_f32_16x16x4_f32 v[0:3], v36, v19, v[0:3]
	global_load_dwordx4 v[16:19], v112, s[18:19]
	s_waitcnt vmcnt(3)
	v_mfma_f32_16x16x4_f32 v[4:7], v37, v20, v[4:7]
	v_mfma_f32_16x16x4_f32 v[8:11], v37, v21, v[8:11]
	v_mfma_f32_16x16x4_f32 v[12:15], v37, v22, v[12:15]
	v_mfma_f32_16x16x4_f32 v[0:3], v37, v23, v[0:3]
	global_load_dwordx4 v[20:23], v112, s[18:19] offset:1024
	s_waitcnt vmcnt(3)
	v_mfma_f32_16x16x4_f32 v[4:7], v52, v24, v[4:7]
	v_mfma_f32_16x16x4_f32 v[8:11], v52, v25, v[8:11]
	v_mfma_f32_16x16x4_f32 v[12:15], v52, v26, v[12:15]
	v_mfma_f32_16x16x4_f32 v[0:3], v52, v27, v[0:3]
	global_load_dwordx4 v[24:27], v112, s[18:19] offset:2048
	global_load_dwordx4 v[32:35], v112, s[18:19] offset:3072
	s_waitcnt vmcnt(4)
	v_mfma_f32_16x16x4_f32 v[4:7], v53, v28, v[4:7]
	v_mfma_f32_16x16x4_f32 v[8:11], v53, v29, v[8:11]
	v_lshl_add_u64 v[28:29], s[18:19], 0, v[112:113]
	v_add_co_u32_e32 v28, vcc, s17, v28
	v_mov_b32_e32 v112, v223
	s_nop 0
	v_addc_co_u32_e32 v29, vcc, 0, v29, vcc
	global_load_dwordx4 v[36:39], v[28:29], off
	global_load_dwordx4 v[40:43], v[28:29], off offset:1024
	global_load_dwordx4 v[44:47], v[28:29], off offset:2048
	global_load_dwordx4 v[48:51], v[28:29], off offset:3072
	ds_read2_b32 v[28:29], v220 offset0:32 offset1:36
	v_mfma_f32_16x16x4_f32 v[12:15], v53, v30, v[12:15]
	v_mfma_f32_16x16x4_f32 v[0:3], v53, v31, v[0:3]
	ds_read2_b32 v[52:53], v220 offset0:56 offset1:60
	s_waitcnt vmcnt(7) lgkmcnt(1)
	v_mfma_f32_16x16x4_f32 v[4:7], v28, v16, v[4:7]
	v_mfma_f32_16x16x4_f32 v[8:11], v28, v17, v[8:11]
	ds_read2_b32 v[16:17], v220 offset0:40 offset1:44
	v_mfma_f32_16x16x4_f32 v[12:15], v28, v18, v[12:15]
	v_mfma_f32_16x16x4_f32 v[0:3], v28, v19, v[0:3]
	s_waitcnt vmcnt(6)
	v_mfma_f32_16x16x4_f32 v[4:7], v29, v20, v[4:7]
	v_mfma_f32_16x16x4_f32 v[8:11], v29, v21, v[8:11]
	v_mfma_f32_16x16x4_f32 v[12:15], v29, v22, v[12:15]
	v_mfma_f32_16x16x4_f32 v[0:3], v29, v23, v[0:3]
	global_load_dwordx4 v[20:23], v112, s[18:19] offset:1024
	s_waitcnt vmcnt(6) lgkmcnt(0)
	v_mfma_f32_16x16x4_f32 v[4:7], v16, v24, v[4:7]
	v_mfma_f32_16x16x4_f32 v[8:11], v16, v25, v[8:11]
	v_mfma_f32_16x16x4_f32 v[12:15], v16, v26, v[12:15]
	v_mfma_f32_16x16x4_f32 v[0:3], v16, v27, v[0:3]
	s_waitcnt vmcnt(5)
	v_mfma_f32_16x16x4_f32 v[4:7], v17, v32, v[4:7]
	v_mfma_f32_16x16x4_f32 v[8:11], v17, v33, v[8:11]
	v_lshl_add_u64 v[32:33], s[18:19], 0, v[112:113]
	v_mfma_f32_16x16x4_f32 v[12:15], v17, v34, v[12:15]
	v_mfma_f32_16x16x4_f32 v[0:3], v17, v35, v[0:3]
	ds_read2_b32 v[16:17], v220 offset0:48 offset1:52
	s_waitcnt vmcnt(4) lgkmcnt(0)
	v_mfma_f32_16x16x4_f32 v[4:7], v16, v36, v[4:7]
	v_mfma_f32_16x16x4_f32 v[8:11], v16, v37, v[8:11]
	v_mfma_f32_16x16x4_f32 v[12:15], v16, v38, v[12:15]
	v_mfma_f32_16x16x4_f32 v[0:3], v16, v39, v[0:3]
	s_waitcnt vmcnt(3)
	v_mfma_f32_16x16x4_f32 v[4:7], v17, v40, v[4:7]
	v_mfma_f32_16x16x4_f32 v[8:11], v17, v41, v[8:11]
	v_mfma_f32_16x16x4_f32 v[12:15], v17, v42, v[12:15]
	v_mfma_f32_16x16x4_f32 v[0:3], v17, v43, v[0:3]
	global_load_dwordx4 v[16:19], v112, s[18:19]
	global_load_dwordx4 v[24:27], v112, s[18:19] offset:2048
	global_load_dwordx4 v[28:31], v112, s[18:19] offset:3072
	v_mov_b32_e32 v112, v216
	s_waitcnt vmcnt(5)
	v_mfma_f32_16x16x4_f32 v[4:7], v52, v44, v[4:7]
	v_add_co_u32_e32 v44, vcc, s17, v32
	v_mfma_f32_16x16x4_f32 v[8:11], v52, v45, v[8:11]
	s_nop 0
	v_addc_co_u32_e32 v45, vcc, 0, v33, vcc
	v_mfma_f32_16x16x4_f32 v[12:15], v52, v46, v[12:15]
	v_mfma_f32_16x16x4_f32 v[0:3], v52, v47, v[0:3]
	global_load_dwordx4 v[32:35], v[44:45], off
	global_load_dwordx4 v[36:39], v[44:45], off offset:1024
	global_load_dwordx4 v[40:43], v[44:45], off offset:2048
	s_nop 0
	global_load_dwordx4 v[44:47], v[44:45], off offset:3072
	s_waitcnt vmcnt(8)
	v_mfma_f32_16x16x4_f32 v[4:7], v53, v48, v[4:7]
	v_mfma_f32_16x16x4_f32 v[8:11], v53, v49, v[8:11]
	ds_read2_b32 v[48:49], v220 offset0:64 offset1:68
	v_mfma_f32_16x16x4_f32 v[12:15], v53, v50, v[12:15]
	v_mfma_f32_16x16x4_f32 v[0:3], v53, v51, v[0:3]
	ds_read2_b32 v[52:53], v220 offset0:88 offset1:92
	s_waitcnt vmcnt(6) lgkmcnt(1)
	v_mfma_f32_16x16x4_f32 v[4:7], v48, v16, v[4:7]
	v_mfma_f32_16x16x4_f32 v[8:11], v48, v17, v[8:11]
	ds_read2_b32 v[16:17], v220 offset0:72 offset1:76
	v_mfma_f32_16x16x4_f32 v[12:15], v48, v18, v[12:15]
	v_mfma_f32_16x16x4_f32 v[0:3], v48, v19, v[0:3]
	v_mfma_f32_16x16x4_f32 v[4:7], v49, v20, v[4:7]
	v_mfma_f32_16x16x4_f32 v[8:11], v49, v21, v[8:11]
	v_mfma_f32_16x16x4_f32 v[12:15], v49, v22, v[12:15]
	v_mfma_f32_16x16x4_f32 v[0:3], v49, v23, v[0:3]
	global_load_dwordx4 v[20:23], v112, s[18:19] offset:1024
	s_waitcnt vmcnt(6) lgkmcnt(0)
	v_mfma_f32_16x16x4_f32 v[4:7], v16, v24, v[4:7]
	v_mfma_f32_16x16x4_f32 v[8:11], v16, v25, v[8:11]
	v_mfma_f32_16x16x4_f32 v[12:15], v16, v26, v[12:15]
	v_mfma_f32_16x16x4_f32 v[0:3], v16, v27, v[0:3]
	s_waitcnt vmcnt(5)
	v_mfma_f32_16x16x4_f32 v[4:7], v17, v28, v[4:7]
	v_mfma_f32_16x16x4_f32 v[8:11], v17, v29, v[8:11]
	v_mfma_f32_16x16x4_f32 v[12:15], v17, v30, v[12:15]
	v_mfma_f32_16x16x4_f32 v[0:3], v17, v31, v[0:3]
	ds_read2_b32 v[16:17], v220 offset0:80 offset1:84
	s_waitcnt vmcnt(4) lgkmcnt(0)
	v_mfma_f32_16x16x4_f32 v[4:7], v16, v32, v[4:7]
	v_mfma_f32_16x16x4_f32 v[8:11], v16, v33, v[8:11]
	v_lshl_add_u64 v[32:33], s[18:19], 0, v[112:113]
	v_mfma_f32_16x16x4_f32 v[12:15], v16, v34, v[12:15]
	v_mfma_f32_16x16x4_f32 v[0:3], v16, v35, v[0:3]
	s_waitcnt vmcnt(3)
	v_mfma_f32_16x16x4_f32 v[4:7], v17, v36, v[4:7]
	v_mfma_f32_16x16x4_f32 v[8:11], v17, v37, v[8:11]
	v_mfma_f32_16x16x4_f32 v[12:15], v17, v38, v[12:15]
	v_mfma_f32_16x16x4_f32 v[0:3], v17, v39, v[0:3]
	global_load_dwordx4 v[16:19], v112, s[18:19]
	global_load_dwordx4 v[24:27], v112, s[18:19] offset:2048
	global_load_dwordx4 v[28:31], v112, s[18:19] offset:3072
	v_mov_b32_e32 v112, v235
	s_waitcnt vmcnt(5)
	v_mfma_f32_16x16x4_f32 v[4:7], v52, v40, v[4:7]
	v_mfma_f32_16x16x4_f32 v[8:11], v52, v41, v[8:11]
	s_waitcnt vmcnt(4)
	v_mfma_f32_16x16x4_f32 v[4:7], v53, v44, v[4:7]
	v_add_co_u32_e32 v44, vcc, s17, v32
	v_mfma_f32_16x16x4_f32 v[8:11], v53, v45, v[8:11]
	s_nop 0
	v_addc_co_u32_e32 v45, vcc, 0, v33, vcc
	v_mfma_f32_16x16x4_f32 v[12:15], v52, v42, v[12:15]
	v_mfma_f32_16x16x4_f32 v[0:3], v52, v43, v[0:3]
	global_load_dwordx4 v[32:35], v[44:45], off
	global_load_dwordx4 v[36:39], v[44:45], off offset:1024
	global_load_dwordx4 v[40:43], v[44:45], off offset:2048
	global_load_dwordx4 v[48:51], v[44:45], off offset:3072
	ds_read2_b32 v[44:45], v220 offset0:96 offset1:100
	v_mfma_f32_16x16x4_f32 v[12:15], v53, v46, v[12:15]
	v_mfma_f32_16x16x4_f32 v[0:3], v53, v47, v[0:3]
	ds_read2_b32 v[52:53], v220 offset0:120 offset1:124
	s_waitcnt vmcnt(6) lgkmcnt(1)
	v_mfma_f32_16x16x4_f32 v[4:7], v44, v16, v[4:7]
	v_mfma_f32_16x16x4_f32 v[8:11], v44, v17, v[8:11]
	ds_read2_b32 v[16:17], v220 offset0:104 offset1:108
	v_mfma_f32_16x16x4_f32 v[12:15], v44, v18, v[12:15]
	v_mfma_f32_16x16x4_f32 v[0:3], v44, v19, v[0:3]
	v_mfma_f32_16x16x4_f32 v[4:7], v45, v20, v[4:7]
	v_mfma_f32_16x16x4_f32 v[8:11], v45, v21, v[8:11]
	v_mfma_f32_16x16x4_f32 v[12:15], v45, v22, v[12:15]
	v_mfma_f32_16x16x4_f32 v[0:3], v45, v23, v[0:3]
	global_load_dwordx4 v[20:23], v112, s[18:19] offset:1024
	s_waitcnt vmcnt(6) lgkmcnt(0)
	v_mfma_f32_16x16x4_f32 v[4:7], v16, v24, v[4:7]
	v_mfma_f32_16x16x4_f32 v[8:11], v16, v25, v[8:11]
	v_mfma_f32_16x16x4_f32 v[12:15], v16, v26, v[12:15]
	v_mfma_f32_16x16x4_f32 v[0:3], v16, v27, v[0:3]
	s_waitcnt vmcnt(5)
	v_mfma_f32_16x16x4_f32 v[4:7], v17, v28, v[4:7]
	v_mfma_f32_16x16x4_f32 v[8:11], v17, v29, v[8:11]
	v_mfma_f32_16x16x4_f32 v[12:15], v17, v30, v[12:15]
	v_mfma_f32_16x16x4_f32 v[0:3], v17, v31, v[0:3]
	ds_read2_b32 v[16:17], v220 offset0:112 offset1:116
	s_waitcnt vmcnt(4) lgkmcnt(0)
	v_mfma_f32_16x16x4_f32 v[4:7], v16, v32, v[4:7]
	v_mfma_f32_16x16x4_f32 v[8:11], v16, v33, v[8:11]
	v_lshl_add_u64 v[32:33], s[18:19], 0, v[112:113]
	v_add_co_u32_e32 v44, vcc, s17, v32
	s_nop 1
	v_addc_co_u32_e32 v45, vcc, 0, v33, vcc
	v_mfma_f32_16x16x4_f32 v[12:15], v16, v34, v[12:15]
	v_mfma_f32_16x16x4_f32 v[0:3], v16, v35, v[0:3]
	s_waitcnt vmcnt(3)
	v_mfma_f32_16x16x4_f32 v[4:7], v17, v36, v[4:7]
	v_mfma_f32_16x16x4_f32 v[8:11], v17, v37, v[8:11]
	v_mfma_f32_16x16x4_f32 v[12:15], v17, v38, v[12:15]
	v_mfma_f32_16x16x4_f32 v[0:3], v17, v39, v[0:3]
	global_load_dwordx4 v[16:19], v112, s[18:19]
	global_load_dwordx4 v[24:27], v112, s[18:19] offset:2048
	global_load_dwordx4 v[28:31], v112, s[18:19] offset:3072
	v_mov_b32_e32 v112, v226
	s_waitcnt vmcnt(5)
	v_mfma_f32_16x16x4_f32 v[4:7], v52, v40, v[4:7]
	v_mfma_f32_16x16x4_f32 v[8:11], v52, v41, v[8:11]
	v_mfma_f32_16x16x4_f32 v[12:15], v52, v42, v[12:15]
	v_mfma_f32_16x16x4_f32 v[0:3], v52, v43, v[0:3]
	global_load_dwordx4 v[32:35], v[44:45], off
	global_load_dwordx4 v[36:39], v[44:45], off offset:1024
	global_load_dwordx4 v[40:43], v[44:45], off offset:2048
	s_nop 0
	global_load_dwordx4 v[44:47], v[44:45], off offset:3072
	s_waitcnt vmcnt(8)
	v_mfma_f32_16x16x4_f32 v[4:7], v53, v48, v[4:7]
	v_mfma_f32_16x16x4_f32 v[8:11], v53, v49, v[8:11]
	ds_read2_b32 v[48:49], v220 offset0:128 offset1:132
	v_mfma_f32_16x16x4_f32 v[12:15], v53, v50, v[12:15]
	v_mfma_f32_16x16x4_f32 v[0:3], v53, v51, v[0:3]
	ds_read2_b32 v[52:53], v220 offset0:152 offset1:156
	s_waitcnt vmcnt(6) lgkmcnt(1)
	v_mfma_f32_16x16x4_f32 v[4:7], v48, v16, v[4:7]
	v_mfma_f32_16x16x4_f32 v[8:11], v48, v17, v[8:11]
	ds_read2_b32 v[16:17], v220 offset0:136 offset1:140
	v_mfma_f32_16x16x4_f32 v[12:15], v48, v18, v[12:15]
	v_mfma_f32_16x16x4_f32 v[0:3], v48, v19, v[0:3]
	v_mfma_f32_16x16x4_f32 v[4:7], v49, v20, v[4:7]
	v_mfma_f32_16x16x4_f32 v[8:11], v49, v21, v[8:11]
	v_mfma_f32_16x16x4_f32 v[12:15], v49, v22, v[12:15]
	v_mfma_f32_16x16x4_f32 v[0:3], v49, v23, v[0:3]
	global_load_dwordx4 v[20:23], v112, s[18:19] offset:1024
	s_waitcnt vmcnt(6) lgkmcnt(0)
	v_mfma_f32_16x16x4_f32 v[4:7], v16, v24, v[4:7]
	v_mfma_f32_16x16x4_f32 v[8:11], v16, v25, v[8:11]
	v_mfma_f32_16x16x4_f32 v[12:15], v16, v26, v[12:15]
	v_mfma_f32_16x16x4_f32 v[0:3], v16, v27, v[0:3]
	s_waitcnt vmcnt(5)
	v_mfma_f32_16x16x4_f32 v[4:7], v17, v28, v[4:7]
	v_mfma_f32_16x16x4_f32 v[8:11], v17, v29, v[8:11]
	v_mfma_f32_16x16x4_f32 v[12:15], v17, v30, v[12:15]
	v_mfma_f32_16x16x4_f32 v[0:3], v17, v31, v[0:3]
	ds_read2_b32 v[16:17], v220 offset0:144 offset1:148
	s_waitcnt vmcnt(4) lgkmcnt(0)
	v_mfma_f32_16x16x4_f32 v[4:7], v16, v32, v[4:7]
	v_mfma_f32_16x16x4_f32 v[8:11], v16, v33, v[8:11]
	v_lshl_add_u64 v[32:33], s[18:19], 0, v[112:113]
	v_mfma_f32_16x16x4_f32 v[12:15], v16, v34, v[12:15]
	v_mfma_f32_16x16x4_f32 v[0:3], v16, v35, v[0:3]
	s_waitcnt vmcnt(3)
	v_mfma_f32_16x16x4_f32 v[4:7], v17, v36, v[4:7]
	v_mfma_f32_16x16x4_f32 v[8:11], v17, v37, v[8:11]
	v_mfma_f32_16x16x4_f32 v[12:15], v17, v38, v[12:15]
	v_mfma_f32_16x16x4_f32 v[0:3], v17, v39, v[0:3]
	global_load_dwordx4 v[16:19], v112, s[18:19]
	global_load_dwordx4 v[24:27], v112, s[18:19] offset:2048
	global_load_dwordx4 v[28:31], v112, s[18:19] offset:3072
	v_mov_b32_e32 v112, v227
	s_waitcnt vmcnt(5)
	v_mfma_f32_16x16x4_f32 v[4:7], v52, v40, v[4:7]
	v_mfma_f32_16x16x4_f32 v[8:11], v52, v41, v[8:11]
	s_waitcnt vmcnt(4)
	v_mfma_f32_16x16x4_f32 v[4:7], v53, v44, v[4:7]
	v_add_co_u32_e32 v44, vcc, s17, v32
	v_mfma_f32_16x16x4_f32 v[8:11], v53, v45, v[8:11]
	s_nop 0
	v_addc_co_u32_e32 v45, vcc, 0, v33, vcc
	v_mfma_f32_16x16x4_f32 v[12:15], v52, v42, v[12:15]
	v_mfma_f32_16x16x4_f32 v[0:3], v52, v43, v[0:3]
	global_load_dwordx4 v[32:35], v[44:45], off
	global_load_dwordx4 v[36:39], v[44:45], off offset:1024
	global_load_dwordx4 v[40:43], v[44:45], off offset:2048
	global_load_dwordx4 v[48:51], v[44:45], off offset:3072
	ds_read2_b32 v[44:45], v220 offset0:160 offset1:164
	v_mfma_f32_16x16x4_f32 v[12:15], v53, v46, v[12:15]
	v_mfma_f32_16x16x4_f32 v[0:3], v53, v47, v[0:3]
	ds_read2_b32 v[52:53], v220 offset0:184 offset1:188
	s_waitcnt vmcnt(6) lgkmcnt(1)
	v_mfma_f32_16x16x4_f32 v[4:7], v44, v16, v[4:7]
	v_mfma_f32_16x16x4_f32 v[8:11], v44, v17, v[8:11]
	ds_read2_b32 v[16:17], v220 offset0:168 offset1:172
	v_mfma_f32_16x16x4_f32 v[12:15], v44, v18, v[12:15]
	v_mfma_f32_16x16x4_f32 v[0:3], v44, v19, v[0:3]
	v_mfma_f32_16x16x4_f32 v[4:7], v45, v20, v[4:7]
	v_mfma_f32_16x16x4_f32 v[8:11], v45, v21, v[8:11]
	v_mfma_f32_16x16x4_f32 v[12:15], v45, v22, v[12:15]
	v_mfma_f32_16x16x4_f32 v[0:3], v45, v23, v[0:3]
	global_load_dwordx4 v[20:23], v112, s[18:19] offset:1024
	s_waitcnt vmcnt(6) lgkmcnt(0)
	v_mfma_f32_16x16x4_f32 v[4:7], v16, v24, v[4:7]
	v_mfma_f32_16x16x4_f32 v[8:11], v16, v25, v[8:11]
	v_mfma_f32_16x16x4_f32 v[12:15], v16, v26, v[12:15]
	v_mfma_f32_16x16x4_f32 v[0:3], v16, v27, v[0:3]
	s_waitcnt vmcnt(5)
	v_mfma_f32_16x16x4_f32 v[4:7], v17, v28, v[4:7]
	v_mfma_f32_16x16x4_f32 v[8:11], v17, v29, v[8:11]
	v_mfma_f32_16x16x4_f32 v[12:15], v17, v30, v[12:15]
	v_mfma_f32_16x16x4_f32 v[0:3], v17, v31, v[0:3]
	ds_read2_b32 v[16:17], v220 offset0:176 offset1:180
	s_waitcnt vmcnt(4) lgkmcnt(0)
	v_mfma_f32_16x16x4_f32 v[4:7], v16, v32, v[4:7]
	v_mfma_f32_16x16x4_f32 v[8:11], v16, v33, v[8:11]
	v_lshl_add_u64 v[32:33], s[18:19], 0, v[112:113]
	v_add_co_u32_e32 v44, vcc, s17, v32
	s_nop 1
	v_addc_co_u32_e32 v45, vcc, 0, v33, vcc
	v_mfma_f32_16x16x4_f32 v[12:15], v16, v34, v[12:15]
	v_mfma_f32_16x16x4_f32 v[0:3], v16, v35, v[0:3]
	s_waitcnt vmcnt(3)
	v_mfma_f32_16x16x4_f32 v[4:7], v17, v36, v[4:7]
	v_mfma_f32_16x16x4_f32 v[8:11], v17, v37, v[8:11]
	v_mfma_f32_16x16x4_f32 v[12:15], v17, v38, v[12:15]
	v_mfma_f32_16x16x4_f32 v[0:3], v17, v39, v[0:3]
	global_load_dwordx4 v[16:19], v112, s[18:19]
	global_load_dwordx4 v[24:27], v112, s[18:19] offset:2048
	global_load_dwordx4 v[28:31], v112, s[18:19] offset:3072
	v_mov_b32_e32 v112, v228
	s_waitcnt vmcnt(5)
	v_mfma_f32_16x16x4_f32 v[4:7], v52, v40, v[4:7]
	v_mfma_f32_16x16x4_f32 v[8:11], v52, v41, v[8:11]
	v_mfma_f32_16x16x4_f32 v[12:15], v52, v42, v[12:15]
	v_mfma_f32_16x16x4_f32 v[0:3], v52, v43, v[0:3]
	global_load_dwordx4 v[32:35], v[44:45], off
	global_load_dwordx4 v[36:39], v[44:45], off offset:1024
	global_load_dwordx4 v[40:43], v[44:45], off offset:2048
	s_nop 0
	global_load_dwordx4 v[44:47], v[44:45], off offset:3072
	s_waitcnt vmcnt(8)
	v_mfma_f32_16x16x4_f32 v[4:7], v53, v48, v[4:7]
	v_mfma_f32_16x16x4_f32 v[8:11], v53, v49, v[8:11]
	ds_read2_b32 v[48:49], v220 offset0:192 offset1:196
	v_mfma_f32_16x16x4_f32 v[12:15], v53, v50, v[12:15]
	v_mfma_f32_16x16x4_f32 v[0:3], v53, v51, v[0:3]
	s_waitcnt vmcnt(6) lgkmcnt(0)
	v_mfma_f32_16x16x4_f32 v[4:7], v48, v16, v[4:7]
	v_mfma_f32_16x16x4_f32 v[8:11], v48, v17, v[8:11]
	ds_read2_b32 v[16:17], v220 offset0:200 offset1:204
	v_mfma_f32_16x16x4_f32 v[12:15], v48, v18, v[12:15]
	v_mfma_f32_16x16x4_f32 v[0:3], v48, v19, v[0:3]
	v_mfma_f32_16x16x4_f32 v[4:7], v49, v20, v[4:7]
	v_mfma_f32_16x16x4_f32 v[8:11], v49, v21, v[8:11]
	v_mfma_f32_16x16x4_f32 v[12:15], v49, v22, v[12:15]
	v_mfma_f32_16x16x4_f32 v[0:3], v49, v23, v[0:3]
	global_load_dwordx4 v[20:23], v112, s[18:19] offset:1024
	s_waitcnt vmcnt(6) lgkmcnt(0)
	v_mfma_f32_16x16x4_f32 v[4:7], v16, v24, v[4:7]
	v_mfma_f32_16x16x4_f32 v[8:11], v16, v25, v[8:11]
	ds_read2_b32 v[24:25], v220 offset0:216 offset1:220
	v_mfma_f32_16x16x4_f32 v[12:15], v16, v26, v[12:15]
	v_mfma_f32_16x16x4_f32 v[0:3], v16, v27, v[0:3]
	s_waitcnt vmcnt(5)
	v_mfma_f32_16x16x4_f32 v[4:7], v17, v28, v[4:7]
	v_mfma_f32_16x16x4_f32 v[8:11], v17, v29, v[8:11]
	ds_read2_b32 v[28:29], v220 offset0:224 offset1:228
	v_mfma_f32_16x16x4_f32 v[12:15], v17, v30, v[12:15]
	v_mfma_f32_16x16x4_f32 v[0:3], v17, v31, v[0:3]
	ds_read2_b32 v[16:17], v220 offset0:208 offset1:212
	s_waitcnt vmcnt(4) lgkmcnt(0)
	v_mfma_f32_16x16x4_f32 v[4:7], v16, v32, v[4:7]
	v_mfma_f32_16x16x4_f32 v[8:11], v16, v33, v[8:11]
	v_mfma_f32_16x16x4_f32 v[12:15], v16, v34, v[12:15]
	v_mfma_f32_16x16x4_f32 v[0:3], v16, v35, v[0:3]
	s_waitcnt vmcnt(3)
	v_mfma_f32_16x16x4_f32 v[4:7], v17, v36, v[4:7]
	v_mfma_f32_16x16x4_f32 v[8:11], v17, v37, v[8:11]
	v_mfma_f32_16x16x4_f32 v[12:15], v17, v38, v[12:15]
	v_mfma_f32_16x16x4_f32 v[0:3], v17, v39, v[0:3]
	global_load_dwordx4 v[16:19], v112, s[18:19]
	s_waitcnt vmcnt(3)
	v_mfma_f32_16x16x4_f32 v[4:7], v24, v40, v[4:7]
	v_mfma_f32_16x16x4_f32 v[8:11], v24, v41, v[8:11]
	v_mfma_f32_16x16x4_f32 v[12:15], v24, v42, v[12:15]
	v_mfma_f32_16x16x4_f32 v[0:3], v24, v43, v[0:3]
	s_waitcnt vmcnt(2)
	v_mfma_f32_16x16x4_f32 v[4:7], v25, v44, v[4:7]
	v_mfma_f32_16x16x4_f32 v[8:11], v25, v45, v[8:11]
	v_mfma_f32_16x16x4_f32 v[12:15], v25, v46, v[12:15]
	v_mfma_f32_16x16x4_f32 v[0:3], v25, v47, v[0:3]
	global_load_dwordx4 v[24:27], v112, s[18:19] offset:3072
	s_waitcnt vmcnt(1)
	v_mfma_f32_16x16x4_f32 v[4:7], v28, v16, v[4:7]
	v_mfma_f32_16x16x4_f32 v[8:11], v28, v17, v[8:11]
	v_mfma_f32_16x16x4_f32 v[12:15], v28, v18, v[12:15]
	v_mfma_f32_16x16x4_f32 v[0:3], v28, v19, v[0:3]
	global_load_dwordx4 v[16:19], v112, s[18:19] offset:2048
	v_mfma_f32_16x16x4_f32 v[4:7], v29, v20, v[4:7]
	v_mfma_f32_16x16x4_f32 v[8:11], v29, v21, v[8:11]
	v_mfma_f32_16x16x4_f32 v[12:15], v29, v22, v[12:15]
	v_mfma_f32_16x16x4_f32 v[0:3], v29, v23, v[0:3]
	ds_read2_b32 v[28:29], v220 offset0:232 offset1:236
	s_waitcnt vmcnt(0) lgkmcnt(0)
	v_mfma_f32_16x16x4_f32 v[4:7], v28, v16, v[4:7]
	v_mfma_f32_16x16x4_f32 v[8:11], v28, v17, v[8:11]
	v_lshl_add_u64 v[16:17], s[18:19], 0, v[112:113]
	s_mov_b64 s[18:19], -1
	v_mfma_f32_16x16x4_f32 v[4:7], v29, v24, v[4:7]
	v_add_co_u32_e32 v24, vcc, s17, v16
	v_mfma_f32_16x16x4_f32 v[8:11], v29, v25, v[8:11]
	s_nop 0
	v_addc_co_u32_e32 v25, vcc, 0, v17, vcc
	global_load_dwordx4 v[20:23], v[24:25], off offset:1024
	v_mfma_f32_16x16x4_f32 v[12:15], v28, v18, v[12:15]
	v_mfma_f32_16x16x4_f32 v[0:3], v28, v19, v[0:3]
	global_load_dwordx4 v[16:19], v[24:25], off
	v_mfma_f32_16x16x4_f32 v[12:15], v29, v26, v[12:15]
	v_mfma_f32_16x16x4_f32 v[0:3], v29, v27, v[0:3]
	ds_read2_b32 v[28:29], v220 offset0:240 offset1:244
	s_waitcnt vmcnt(0) lgkmcnt(0)
	v_mfma_f32_16x16x4_f32 v[4:7], v28, v16, v[4:7]
	v_mfma_f32_16x16x4_f32 v[8:11], v28, v17, v[8:11]
	v_mfma_f32_16x16x4_f32 v[12:15], v28, v18, v[12:15]
	v_mfma_f32_16x16x4_f32 v[0:3], v28, v19, v[0:3]
	global_load_dwordx4 v[16:19], v[24:25], off offset:2048
	s_nop 0
	global_load_dwordx4 v[24:27], v[24:25], off offset:3072
	v_mfma_f32_16x16x4_f32 v[4:7], v29, v20, v[4:7]
	v_mfma_f32_16x16x4_f32 v[8:11], v29, v21, v[8:11]
	ds_read2_b32 v[20:21], v220 offset0:248 offset1:252
	s_waitcnt lgkmcnt(0)
	s_barrier
	v_mfma_f32_16x16x4_f32 v[12:15], v29, v22, v[12:15]
	v_mfma_f32_16x16x4_f32 v[0:3], v29, v23, v[0:3]
	s_waitcnt vmcnt(1)
	v_mfma_f32_16x16x4_f32 v[4:7], v20, v16, v[4:7]
	v_mfma_f32_16x16x4_f32 v[8:11], v20, v17, v[8:11]
	v_mfma_f32_16x16x4_f32 v[12:15], v20, v18, v[12:15]
	v_mfma_f32_16x16x4_f32 v[0:3], v20, v19, v[0:3]
	s_waitcnt vmcnt(0)
	v_mfma_f32_16x16x4_f32 v[4:7], v21, v24, v[4:7]
	v_mfma_f32_16x16x4_f32 v[8:11], v21, v25, v[8:11]
	s_nop 8
	v_mov_b32_e32 v16, v4
	v_mfma_f32_16x16x4_f32 v[12:15], v21, v26, v[12:15]
	v_mov_b32_e32 v17, v8
	v_mfma_f32_16x16x4_f32 v[0:3], v21, v27, v[0:3]
	s_nop 7
	v_mov_b32_e32 v18, v12
	s_nop 0
	v_mov_b32_e32 v19, v0
	ds_write_b128 v230, v[16:19]
	v_mov_b32_e32 v16, v5
	v_mov_b32_e32 v17, v9
	v_mov_b32_e32 v18, v13
	v_mov_b32_e32 v19, v1
	ds_write_b128 v230, v[16:19] offset:256
	v_mov_b32_e32 v16, v6
	v_mov_b32_e32 v17, v10
	v_mov_b32_e32 v18, v14
	v_mov_b32_e32 v19, v2
	v_mov_b32_e32 v0, v7
	v_mov_b32_e32 v1, v11
	v_mov_b32_e32 v2, v15
	ds_write_b128 v230, v[16:19] offset:512
	ds_write_b128 v230, v[0:3] offset:768
	s_waitcnt lgkmcnt(0)
	s_barrier
	s_branch .LBB0_1196

.LBB0_1546:
	s_ashr_i32 s28, s0, 31
	s_lshr_b32 s28, s28, 20
	s_add_i32 s28, s0, s28
	s_ashr_i32 s28, s28, 12
	v_lshl_add_u64 v[0:1], s[2:3], 0, v[102:103]
	s_mul_i32 s36, s28, 6
	v_add_co_u32_e32 v18, vcc, s5, v0
	s_ashr_i32 s37, s36, 31
	v_lshl_add_u64 v[104:105], s[2:3], 0, v[100:101]
	v_addc_co_u32_e32 v19, vcc, 0, v1, vcc
	s_add_u32 s46, s2, s29
	global_load_dwordx4 v[2:5], v[104:105], off offset:-2048
	global_load_dwordx4 v[6:9], v[104:105], off offset:-1024
	global_load_dwordx4 v[10:13], v[104:105], off
	v_add_co_u32_e32 v114, vcc, s45, v0
	s_addc_u32 s47, s3, s17
	global_load_dwordx4 v[14:17], v[104:105], off offset:1024
	v_addc_co_u32_e32 v115, vcc, 0, v1, vcc
	global_load_dwordx2 v[0:1], v[18:19], off offset:512
	global_load_dwordx2 v[26:27], v[18:19], off offset:1024
	global_load_dwordx2 v[28:29], v[18:19], off offset:1536
	global_load_dwordx2 v[30:31], v[18:19], off offset:2048
	s_nop 0
	global_load_dwordx4 v[18:21], v148, s[46:47] offset:512
	global_load_dwordx4 v[22:25], v149, s[46:47] offset:512
	s_add_u32 s48, s46, 0x19a200
	s_addc_u32 s49, s47, 0
	global_load_dwordx2 v[32:33], v97, s[48:49] offset:16
	s_add_u32 s46, s46, 0x13a200
	s_addc_u32 s47, s47, 0
	global_load_dwordx2 v[34:35], v97, s[46:47] offset:16
	s_lshl_b64 s[36:37], s[36:37], 13
	v_mov_b32_e32 v152, 0
	v_mov_b32_e32 v153, 0
	v_mov_b32_e32 v154, 0
	v_mov_b32_e32 v155, 0
	v_mov_b32_e32 v106, 0
	v_mov_b32_e32 v107, 0
	v_mov_b32_e32 v108, 0
	v_mov_b32_e32 v109, 0
	v_mov_b32_e32 v110, 0
	v_mov_b32_e32 v111, 0
	v_mov_b32_e32 v112, 0
	v_mov_b32_e32 v113, 0
	v_lshl_add_u64 v[100:101], v[100:101], 0, s[6:7]
	v_lshl_add_u64 v[102:103], v[102:103], 0, s[8:9]
	s_waitcnt vmcnt(11)
	v_lshlrev_b32_e32 v116, 16, v5
	v_and_b32_e32 v117, 0xffff0000, v5
	v_lshlrev_b32_e32 v118, 16, v4
	v_and_b32_e32 v119, 0xffff0000, v4
	v_lshlrev_b32_e32 v122, 16, v3
	v_and_b32_e32 v123, 0xffff0000, v3
	v_lshlrev_b32_e32 v128, 16, v2
	v_and_b32_e32 v129, 0xffff0000, v2
	s_waitcnt vmcnt(10)
	v_lshlrev_b32_e32 v130, 16, v7
	v_and_b32_e32 v131, 0xffff0000, v7
	v_lshlrev_b32_e32 v136, 16, v6
	v_and_b32_e32 v137, 0xffff0000, v6
	s_waitcnt vmcnt(7)
	v_cvt_pk_f32_fp8_e32 v[2:3], v0
	v_cvt_pk_f32_fp8_sdwa v[4:5], v0 src0_sel:WORD_1
	v_cvt_pk_f32_fp8_e32 v[6:7], v1
	v_cvt_pk_f32_fp8_sdwa v[0:1], v1 src0_sel:WORD_1
	s_waitcnt vmcnt(3)
	v_readfirstlane_b32 s46, v18
	v_readfirstlane_b32 s48, v19
	v_readfirstlane_b32 s50, v20
	v_readfirstlane_b32 s52, v21
	s_ashr_i32 s47, s46, 31
	s_ashr_i32 s49, s48, 31
	s_ashr_i32 s51, s50, 31
	s_ashr_i32 s53, s52, 31
	s_lshl_b64 s[46:47], s[46:47], 11
	v_pk_add_f32 v[156:157], v[0:1], 0 op_sel_hi:[1,0]
	s_lshl_b64 s[48:49], s[48:49], 11
	s_lshl_b64 s[50:51], s[50:51], 11
	s_lshl_b64 s[52:53], s[52:53], 11
	v_lshl_add_u64 v[0:1], v[98:99], 0, s[46:47]
	v_pk_add_f32 v[158:159], v[6:7], 0 op_sel_hi:[1,0]
	v_pk_add_f32 v[160:161], v[4:5], 0 op_sel_hi:[1,0]
	v_pk_add_f32 v[162:163], v[2:3], 0 op_sel_hi:[1,0]
	v_lshl_add_u64 v[2:3], v[98:99], 0, s[48:49]
	v_lshl_add_u64 v[4:5], v[98:99], 0, s[50:51]
	v_lshl_add_u64 v[6:7], v[98:99], 0, s[52:53]
	global_load_dwordx2 v[188:189], v[0:1], off
	global_load_dwordx2 v[190:191], v[0:1], off offset:512
	global_load_dwordx2 v[192:193], v[0:1], off offset:1024
	global_load_dwordx2 v[194:195], v[0:1], off offset:1536
	global_load_dwordx2 v[196:197], v[2:3], off
	global_load_dwordx2 v[198:199], v[2:3], off offset:512
	global_load_dwordx2 v[200:201], v[2:3], off offset:1024
	global_load_dwordx2 v[202:203], v[2:3], off offset:1536
	global_load_dwordx2 v[204:205], v[4:5], off
	global_load_dwordx2 v[206:207], v[4:5], off offset:512
	global_load_dwordx2 v[208:209], v[4:5], off offset:1024
	global_load_dwordx2 v[210:211], v[4:5], off offset:1536
	global_load_dwordx2 v[212:213], v[6:7], off
	global_load_dwordx2 v[214:215], v[6:7], off offset:512
	global_load_dwordx2 v[216:217], v[6:7], off offset:1024
	global_load_dwordx2 v[218:219], v[6:7], off offset:1536
	s_waitcnt vmcnt(17)
	v_readfirstlane_b32 s54, v32
	v_readfirstlane_b32 s56, v33
	s_ashr_i32 s55, s54, 31
	s_ashr_i32 s57, s56, 31
	s_lshl_b64 s[46:47], s[54:55], 11
	s_lshl_b64 s[48:49], s[56:57], 11
	v_lshl_add_u64 v[0:1], v[98:99], 0, s[46:47]
	v_lshl_add_u64 v[2:3], v[98:99], 0, s[48:49]
	global_load_dwordx2 v[220:221], v[0:1], off
	global_load_dwordx2 v[222:223], v[0:1], off offset:512
	global_load_dwordx2 v[224:225], v[0:1], off offset:1024
	global_load_dwordx2 v[226:227], v[0:1], off offset:1536
	global_load_dwordx2 v[228:229], v[2:3], off
	global_load_dwordx2 v[230:231], v[2:3], off offset:512
	global_load_dwordx2 v[232:233], v[2:3], off offset:1024
	global_load_dwordx2 v[234:235], v[2:3], off offset:1536
	s_add_u32 s46, s2, s36
	s_addc_u32 s47, s3, s37
	v_lshl_add_u64 v[0:1], s[46:47], 0, v[96:97]
	v_lshl_add_u64 v[2:3], v[0:1], 0, s[10:11]
	v_add_co_u32_e32 v4, vcc, s39, v0
	v_lshl_add_u64 v[6:7], v[0:1], 0, s[12:13]
	s_nop 0
	v_addc_co_u32_e32 v5, vcc, 0, v1, vcc
	v_lshl_add_u64 v[0:1], v[0:1], 0, s[14:15]
	global_load_dwordx4 v[84:87], v[2:3], off offset:16
	global_load_dwordx4 v[80:83], v[2:3], off offset:2048
	global_load_dwordx4 v[92:95], v[4:5], off offset:-4096
	global_load_dwordx4 v[72:75], v[4:5], off
	global_load_dwordx4 v[88:91], v[2:3], off offset:2064
	global_load_dwordx4 v[76:79], v[6:7], off offset:16
	global_load_dwordx4 v[68:71], v[4:5], off offset:2048
	global_load_dwordx4 v[64:67], v[0:1], off offset:16
	v_lshlrev_b32_e32 v126, 16, v13
	v_and_b32_e32 v127, 0xffff0000, v13
	v_lshlrev_b32_e32 v132, 16, v12
	v_and_b32_e32 v133, 0xffff0000, v12
	v_lshlrev_b32_e32 v138, 16, v11
	v_and_b32_e32 v139, 0xffff0000, v11
	v_lshlrev_b32_e32 v142, 16, v10
	v_and_b32_e32 v143, 0xffff0000, v10
	v_lshlrev_b32_e32 v144, 16, v15
	v_and_b32_e32 v145, 0xffff0000, v15
	v_lshlrev_b32_e32 v146, 16, v14
	v_and_b32_e32 v147, 0xffff0000, v14
	v_cvt_pk_f32_fp8_sdwa v[10:11], v26 src0_sel:WORD_1
	v_cvt_pk_f32_fp8_e32 v[12:13], v27
	v_cvt_pk_f32_fp8_sdwa v[14:15], v27 src0_sel:WORD_1
	v_lshlrev_b32_e32 v120, 16, v9
	v_and_b32_e32 v121, 0xffff0000, v9
	v_lshlrev_b32_e32 v124, 16, v8
	v_and_b32_e32 v125, 0xffff0000, v8
	v_lshlrev_b32_e32 v134, 16, v17
	v_and_b32_e32 v135, 0xffff0000, v17
	v_lshlrev_b32_e32 v140, 16, v16
	v_and_b32_e32 v141, 0xffff0000, v16
	v_cvt_pk_f32_fp8_e32 v[8:9], v26
	v_cvt_pk_f32_fp8_e32 v[16:17], v28
	v_cvt_pk_f32_fp8_sdwa v[26:27], v28 src0_sel:WORD_1
	v_cvt_pk_f32_fp8_e32 v[36:37], v29
	v_cvt_pk_f32_fp8_sdwa v[28:29], v29 src0_sel:WORD_1
	v_cvt_pk_f32_fp8_e32 v[38:39], v30
	v_cvt_pk_f32_fp8_sdwa v[40:41], v30 src0_sel:WORD_1
	v_cvt_pk_f32_fp8_e32 v[42:43], v31
	v_cvt_pk_f32_fp8_sdwa v[30:31], v31 src0_sel:WORD_1
	v_readfirstlane_b32 s42, v22
	v_pk_add_f32 v[164:165], v[14:15], 0 op_sel_hi:[1,0]
	v_pk_add_f32 v[166:167], v[12:13], 0 op_sel_hi:[1,0]
	v_pk_add_f32 v[168:169], v[10:11], 0 op_sel_hi:[1,0]
	v_pk_add_f32 v[170:171], v[8:9], 0 op_sel_hi:[1,0]
	v_pk_add_f32 v[172:173], v[28:29], 0 op_sel_hi:[1,0]
	v_pk_add_f32 v[174:175], v[36:37], 0 op_sel_hi:[1,0]
	v_pk_add_f32 v[176:177], v[26:27], 0 op_sel_hi:[1,0]
	v_pk_add_f32 v[178:179], v[16:17], 0 op_sel_hi:[1,0]
	v_pk_add_f32 v[180:181], v[30:31], 0 op_sel_hi:[1,0]
	v_pk_add_f32 v[182:183], v[42:43], 0 op_sel_hi:[1,0]
	v_readfirstlane_b32 s40, v23
	s_waitcnt vmcnt(31)
	v_cvt_pk_f32_fp8_e32 v[236:237], v188
	v_cvt_pk_f32_fp8_sdwa v[238:239], v188 src0_sel:WORD_1
	v_cvt_pk_f32_fp8_e32 v[240:241], v189
	v_cvt_pk_f32_fp8_sdwa v[188:189], v189 src0_sel:WORD_1
	s_waitcnt vmcnt(30)
	v_cvt_pk_f32_fp8_e32 v[242:243], v190
	v_cvt_pk_f32_fp8_sdwa v[244:245], v190 src0_sel:WORD_1
	v_cvt_pk_f32_fp8_e32 v[246:247], v191
	v_cvt_pk_f32_fp8_sdwa v[190:191], v191 src0_sel:WORD_1
	s_waitcnt vmcnt(29)
	v_cvt_pk_f32_fp8_e32 v[248:249], v192
	v_cvt_pk_f32_fp8_sdwa v[250:251], v192 src0_sel:WORD_1
	v_pk_fma_f32 v[156:157], v[188:189], s[42:43], v[156:157] op_sel_hi:[1,0,1]
	v_cvt_pk_f32_fp8_e32 v[188:189], v193
	v_cvt_pk_f32_fp8_sdwa v[192:193], v193 src0_sel:WORD_1
	v_pk_fma_f32 v[158:159], v[240:241], s[42:43], v[158:159] op_sel_hi:[1,0,1]
	s_waitcnt vmcnt(28)
	v_cvt_pk_f32_fp8_e32 v[240:241], v194
	v_pk_fma_f32 v[160:161], v[238:239], s[42:43], v[160:161] op_sel_hi:[1,0,1]
	v_cvt_pk_f32_fp8_sdwa v[238:239], v194 src0_sel:WORD_1
	v_pk_fma_f32 v[162:163], v[236:237], s[42:43], v[162:163] op_sel_hi:[1,0,1]
	v_cvt_pk_f32_fp8_e32 v[236:237], v195
	v_cvt_pk_f32_fp8_sdwa v[194:195], v195 src0_sel:WORD_1
	v_pk_fma_f32 v[164:165], v[190:191], s[42:43], v[164:165] op_sel_hi:[1,0,1]
	s_waitcnt vmcnt(27)
	v_cvt_pk_f32_fp8_e32 v[190:191], v196
	v_pk_fma_f32 v[166:167], v[246:247], s[42:43], v[166:167] op_sel_hi:[1,0,1]
	v_cvt_pk_f32_fp8_sdwa v[246:247], v196 src0_sel:WORD_1
	v_pk_fma_f32 v[168:169], v[244:245], s[42:43], v[168:169] op_sel_hi:[1,0,1]
	v_cvt_pk_f32_fp8_e32 v[244:245], v197
	v_cvt_pk_f32_fp8_sdwa v[196:197], v197 src0_sel:WORD_1
	v_pk_fma_f32 v[170:171], v[242:243], s[42:43], v[170:171] op_sel_hi:[1,0,1]
	s_waitcnt vmcnt(26)
	v_cvt_pk_f32_fp8_e32 v[242:243], v198
	v_pk_fma_f32 v[172:173], v[192:193], s[42:43], v[172:173] op_sel_hi:[1,0,1]
	v_cvt_pk_f32_fp8_sdwa v[192:193], v198 src0_sel:WORD_1
	v_pk_fma_f32 v[174:175], v[188:189], s[42:43], v[174:175] op_sel_hi:[1,0,1]
	v_cvt_pk_f32_fp8_e32 v[188:189], v199
	v_cvt_pk_f32_fp8_sdwa v[198:199], v199 src0_sel:WORD_1
	v_pk_fma_f32 v[176:177], v[250:251], s[42:43], v[176:177] op_sel_hi:[1,0,1]
	s_waitcnt vmcnt(25)
	v_cvt_pk_f32_fp8_e32 v[250:251], v200
	v_pk_fma_f32 v[178:179], v[248:249], s[42:43], v[178:179] op_sel_hi:[1,0,1]
	v_cvt_pk_f32_fp8_sdwa v[248:249], v200 src0_sel:WORD_1
	v_pk_fma_f32 v[180:181], v[194:195], s[42:43], v[180:181] op_sel_hi:[1,0,1]
	v_cvt_pk_f32_fp8_e32 v[194:195], v201
	v_cvt_pk_f32_fp8_sdwa v[200:201], v201 src0_sel:WORD_1
	v_pk_fma_f32 v[182:183], v[236:237], s[42:43], v[182:183] op_sel_hi:[1,0,1]
	s_waitcnt vmcnt(24)
	v_cvt_pk_f32_fp8_e32 v[236:237], v202
	v_pk_fma_f32 v[156:157], v[196:197], s[40:41], v[156:157] op_sel_hi:[1,0,1]
	s_waitcnt vmcnt(23)
	v_cvt_pk_f32_fp8_e32 v[196:197], v204
	v_pk_fma_f32 v[158:159], v[244:245], s[40:41], v[158:159] op_sel_hi:[1,0,1]
	v_cvt_pk_f32_fp8_sdwa v[244:245], v204 src0_sel:WORD_1
	v_pk_fma_f32 v[160:161], v[246:247], s[40:41], v[160:161] op_sel_hi:[1,0,1]
	v_cvt_pk_f32_fp8_e32 v[246:247], v205
	v_cvt_pk_f32_fp8_sdwa v[204:205], v205 src0_sel:WORD_1
	v_pk_add_f32 v[184:185], v[40:41], 0 op_sel_hi:[1,0]
	v_pk_add_f32 v[186:187], v[38:39], 0 op_sel_hi:[1,0]
	v_pk_fma_f32 v[184:185], v[238:239], s[42:43], v[184:185] op_sel_hi:[1,0,1]
	v_cvt_pk_f32_fp8_sdwa v[238:239], v202 src0_sel:WORD_1
	v_pk_fma_f32 v[186:187], v[240:241], s[42:43], v[186:187] op_sel_hi:[1,0,1]
	v_cvt_pk_f32_fp8_e32 v[240:241], v203
	v_cvt_pk_f32_fp8_sdwa v[202:203], v203 src0_sel:WORD_1
	v_readfirstlane_b32 s34, v24
	v_pk_fma_f32 v[162:163], v[190:191], s[40:41], v[162:163] op_sel_hi:[1,0,1]
	s_waitcnt vmcnt(22)
	v_cvt_pk_f32_fp8_e32 v[190:191], v206
	v_pk_fma_f32 v[164:165], v[198:199], s[40:41], v[164:165] op_sel_hi:[1,0,1]
	v_cvt_pk_f32_fp8_sdwa v[198:199], v206 src0_sel:WORD_1
	v_pk_fma_f32 v[166:167], v[188:189], s[40:41], v[166:167] op_sel_hi:[1,0,1]
	v_cvt_pk_f32_fp8_e32 v[188:189], v207
	v_cvt_pk_f32_fp8_sdwa v[206:207], v207 src0_sel:WORD_1
	v_pk_fma_f32 v[168:169], v[192:193], s[40:41], v[168:169] op_sel_hi:[1,0,1]
	s_waitcnt vmcnt(21)
	v_cvt_pk_f32_fp8_e32 v[192:193], v208
	v_pk_fma_f32 v[170:171], v[242:243], s[40:41], v[170:171] op_sel_hi:[1,0,1]
	v_cvt_pk_f32_fp8_sdwa v[242:243], v208 src0_sel:WORD_1
	v_pk_fma_f32 v[172:173], v[200:201], s[40:41], v[172:173] op_sel_hi:[1,0,1]
	v_cvt_pk_f32_fp8_e32 v[200:201], v209
	v_cvt_pk_f32_fp8_sdwa v[208:209], v209 src0_sel:WORD_1
	v_pk_fma_f32 v[186:187], v[236:237], s[40:41], v[186:187] op_sel_hi:[1,0,1]
	s_waitcnt vmcnt(18)
	v_cvt_pk_f32_fp8_e32 v[236:237], v214
	v_pk_fma_f32 v[156:157], v[204:205], s[34:35], v[156:157] op_sel_hi:[1,0,1]
	v_cvt_pk_f32_fp8_sdwa v[204:205], v214 src0_sel:WORD_1
	v_pk_fma_f32 v[158:159], v[246:247], s[34:35], v[158:159] op_sel_hi:[1,0,1]
	v_cvt_pk_f32_fp8_e32 v[246:247], v215
	v_cvt_pk_f32_fp8_sdwa v[214:215], v215 src0_sel:WORD_1
	s_add_u32 s36, s1, s36
	v_pk_fma_f32 v[174:175], v[194:195], s[40:41], v[174:175] op_sel_hi:[1,0,1]
	v_cvt_pk_f32_fp8_e32 v[194:195], v210
	s_addc_u32 s37, s16, s37
	s_add_i32 s0, s0, s4
	v_pk_fma_f32 v[180:181], v[202:203], s[40:41], v[180:181] op_sel_hi:[1,0,1]
	v_cvt_pk_f32_fp8_e32 v[202:203], v212
	v_readfirstlane_b32 s28, v25
	s_add_u32 s29, s29, s33
	v_pk_fma_f32 v[178:179], v[250:251], s[40:41], v[178:179] op_sel_hi:[1,0,1]
	v_cvt_pk_f32_fp8_e32 v[250:251], v211
	v_pk_fma_f32 v[182:183], v[240:241], s[40:41], v[182:183] op_sel_hi:[1,0,1]
	v_cvt_pk_f32_fp8_sdwa v[240:241], v212 src0_sel:WORD_1
	v_pk_fma_f32 v[184:185], v[238:239], s[40:41], v[184:185] op_sel_hi:[1,0,1]
	v_cvt_pk_f32_fp8_e32 v[238:239], v213
	v_pk_fma_f32 v[164:165], v[206:207], s[34:35], v[164:165] op_sel_hi:[1,0,1]
	v_pk_fma_f32 v[172:173], v[208:209], s[34:35], v[172:173] op_sel_hi:[1,0,1]
	s_waitcnt vmcnt(15)
	v_cvt_pk_f32_fp8_e32 v[208:209], v220
	v_pk_fma_f32 v[162:163], v[196:197], s[34:35], v[162:163] op_sel_hi:[1,0,1]
	v_cvt_pk_f32_fp8_sdwa v[196:197], v216 src0_sel:WORD_1
	v_pk_fma_f32 v[166:167], v[188:189], s[34:35], v[166:167] op_sel_hi:[1,0,1]
	v_pk_fma_f32 v[170:171], v[190:191], s[34:35], v[170:171] op_sel_hi:[1,0,1]
	v_cvt_pk_f32_fp8_e32 v[190:191], v219
	v_pk_fma_f32 v[174:175], v[200:201], s[34:35], v[174:175] op_sel_hi:[1,0,1]
	v_cvt_pk_f32_fp8_sdwa v[200:201], v220 src0_sel:WORD_1
	v_pk_fma_f32 v[164:165], v[214:215], s[28:29], v[164:165] op_sel_hi:[1,0,1]
	s_waitcnt vmcnt(11)
	v_cvt_pk_f32_fp8_e32 v[214:215], v228
	v_pk_fma_f32 v[176:177], v[248:249], s[40:41], v[176:177] op_sel_hi:[1,0,1]
	v_pk_fma_f32 v[186:187], v[194:195], s[34:35], v[186:187] op_sel_hi:[1,0,1]
	v_cvt_pk_f32_fp8_sdwa v[194:195], v224 src0_sel:WORD_1
	v_pk_fma_f32 v[166:167], v[246:247], s[28:29], v[166:167] op_sel_hi:[1,0,1]
	v_cvt_pk_f32_fp8_sdwa v[246:247], v228 src0_sel:WORD_1
	v_readfirstlane_b32 s38, v34
	v_pk_fma_f32 v[160:161], v[244:245], s[34:35], v[160:161] op_sel_hi:[1,0,1]
	v_cvt_pk_f32_fp8_e32 v[188:189], v218
	v_pk_fma_f32 v[168:169], v[198:199], s[34:35], v[168:169] op_sel_hi:[1,0,1]
	v_pk_fma_f32 v[176:177], v[242:243], s[34:35], v[176:177] op_sel_hi:[1,0,1]
	v_cvt_pk_f32_fp8_e32 v[242:243], v221
	v_pk_fma_f32 v[178:179], v[192:193], s[34:35], v[178:179] op_sel_hi:[1,0,1]
	v_cvt_pk_f32_fp8_e32 v[192:193], v222
	v_pk_fma_f32 v[162:163], v[202:203], s[28:29], v[162:163] op_sel_hi:[1,0,1]
	v_lshl_add_u64 v[0:1], s[36:37], 0, v[96:97]
	v_readfirstlane_b32 s36, v35
	v_cvt_pk_f32_fp8_sdwa v[212:213], v213 src0_sel:WORD_1
	v_pk_fma_f32 v[182:183], v[250:251], s[34:35], v[182:183] op_sel_hi:[1,0,1]
	v_pk_fma_f32 v[158:159], v[238:239], s[28:29], v[158:159] op_sel_hi:[1,0,1]
	v_cvt_pk_f32_fp8_e32 v[238:239], v226
	v_pk_fma_f32 v[160:161], v[240:241], s[28:29], v[160:161] op_sel_hi:[1,0,1]
	v_pk_fma_f32 v[168:169], v[204:205], s[28:29], v[168:169] op_sel_hi:[1,0,1]
	v_cvt_pk_f32_fp8_e32 v[204:205], v229
	v_pk_fma_f32 v[162:163], v[208:209], s[38:39], v[162:163] op_sel_hi:[1,0,1]
	v_cvt_pk_f32_fp8_sdwa v[248:249], v210 src0_sel:WORD_1
	v_cvt_pk_f32_fp8_sdwa v[210:211], v211 src0_sel:WORD_1
	v_cvt_pk_f32_fp8_sdwa v[220:221], v221 src0_sel:WORD_1
	v_pk_fma_f32 v[176:177], v[196:197], s[28:29], v[176:177] op_sel_hi:[1,0,1]
	v_pk_fma_f32 v[182:183], v[190:191], s[28:29], v[182:183] op_sel_hi:[1,0,1]
	s_waitcnt vmcnt(8)
	v_cvt_pk_f32_fp8_e32 v[190:191], v234
	v_pk_fma_f32 v[160:161], v[200:201], s[38:39], v[160:161] op_sel_hi:[1,0,1]
	v_pk_fma_f32 v[162:163], v[214:215], s[36:37], v[162:163] op_sel_hi:[1,0,1]
	v_cvt_pk_f32_fp8_e32 v[244:245], v216
	v_cvt_pk_f32_fp8_e32 v[206:207], v217
	v_cvt_pk_f32_fp8_sdwa v[216:217], v217 src0_sel:WORD_1
	v_cvt_pk_f32_fp8_e32 v[202:203], v227
	v_cvt_pk_f32_fp8_sdwa v[228:229], v229 src0_sel:WORD_1
	v_pk_fma_f32 v[170:171], v[236:237], s[28:29], v[170:171] op_sel_hi:[1,0,1]
	v_pk_fma_f32 v[176:177], v[194:195], s[38:39], v[176:177] op_sel_hi:[1,0,1]
	v_pk_fma_f32 v[160:161], v[246:247], s[36:37], v[160:161] op_sel_hi:[1,0,1]
	v_pk_mul_f32 v[194:195], v[162:163], v[162:163]
	v_pk_fma_f32 v[186:187], v[188:189], s[28:29], v[186:187] op_sel_hi:[1,0,1]
	v_cvt_pk_f32_fp8_e32 v[188:189], v235
	v_pk_fma_f32 v[158:159], v[242:243], s[38:39], v[158:159] op_sel_hi:[1,0,1]
	v_pk_fma_f32 v[170:171], v[192:193], s[38:39], v[170:171] op_sel_hi:[1,0,1]
	v_pk_mul_f32 v[192:193], v[160:161], v[160:161]
	v_add_f32_e32 v194, v194, v195
	v_pk_fma_f32 v[156:157], v[212:213], s[28:29], v[156:157] op_sel_hi:[1,0,1]
	v_cvt_pk_f32_fp8_e32 v[236:237], v230
	v_pk_fma_f32 v[186:187], v[238:239], s[38:39], v[186:187] op_sel_hi:[1,0,1]
	v_pk_fma_f32 v[158:159], v[204:205], s[36:37], v[158:159] op_sel_hi:[1,0,1]
	v_add_f32_e32 v192, v194, v192
	v_cvt_pk_f32_fp8_sdwa v[198:199], v218 src0_sel:WORD_1
	v_pk_fma_f32 v[180:181], v[210:211], s[34:35], v[180:181] op_sel_hi:[1,0,1]
	v_cvt_pk_f32_fp8_sdwa v[210:211], v222 src0_sel:WORD_1
	v_pk_fma_f32 v[156:157], v[220:221], s[38:39], v[156:157] op_sel_hi:[1,0,1]
	v_pk_fma_f32 v[186:187], v[190:191], s[36:37], v[186:187] op_sel_hi:[1,0,1]
	v_pk_mul_f32 v[190:191], v[158:159], v[158:159]
	v_add_f32_e32 v192, v193, v192
	v_pk_fma_f32 v[172:173], v[216:217], s[28:29], v[172:173] op_sel_hi:[1,0,1]
	v_cvt_pk_f32_fp8_sdwa v[216:217], v230 src0_sel:WORD_1
	v_pk_fma_f32 v[182:183], v[202:203], s[38:39], v[182:183] op_sel_hi:[1,0,1]
	v_pk_fma_f32 v[156:157], v[228:229], s[36:37], v[156:157] op_sel_hi:[1,0,1]
	v_add_f32_e32 v190, v190, v192
	v_cvt_pk_f32_fp8_e32 v[250:251], v223
	v_pk_fma_f32 v[182:183], v[188:189], s[36:37], v[182:183] op_sel_hi:[1,0,1]
	v_pk_mul_f32 v[188:189], v[156:157], v[156:157]
	v_add_f32_e32 v190, v191, v190
	v_pk_fma_f32 v[184:185], v[248:249], s[34:35], v[184:185] op_sel_hi:[1,0,1]
	v_cvt_pk_f32_fp8_sdwa v[240:241], v226 src0_sel:WORD_1
	v_pk_fma_f32 v[174:175], v[206:207], s[28:29], v[174:175] op_sel_hi:[1,0,1]
	v_cvt_pk_f32_fp8_e32 v[206:207], v231
	v_pk_fma_f32 v[170:171], v[236:237], s[36:37], v[170:171] op_sel_hi:[1,0,1]
	v_add_f32_e32 v188, v188, v190
	v_cvt_pk_f32_fp8_sdwa v[222:223], v223 src0_sel:WORD_1
	v_pk_fma_f32 v[184:185], v[198:199], s[28:29], v[184:185] op_sel_hi:[1,0,1]
	v_cvt_pk_f32_fp8_sdwa v[198:199], v234 src0_sel:WORD_1
	v_pk_fma_f32 v[168:169], v[210:211], s[38:39], v[168:169] op_sel_hi:[1,0,1]
	v_pk_mul_f32 v[202:203], v[170:171], v[170:171]
	v_add_f32_e32 v188, v189, v188
	v_cvt_pk_f32_fp8_e32 v[248:249], v224
	v_cvt_pk_f32_fp8_sdwa v[230:231], v231 src0_sel:WORD_1
	v_pk_fma_f32 v[168:169], v[216:217], s[36:37], v[168:169] op_sel_hi:[1,0,1]
	v_add_f32_e32 v188, v202, v188
	v_cvt_pk_f32_fp8_e32 v[196:197], v232
	v_pk_fma_f32 v[166:167], v[250:251], s[38:39], v[166:167] op_sel_hi:[1,0,1]
	v_pk_mul_f32 v[200:201], v[168:169], v[168:169]
	v_add_f32_e32 v188, v203, v188
	v_cvt_pk_f32_fp8_sdwa v[218:219], v219 src0_sel:WORD_1
	v_pk_fma_f32 v[184:185], v[240:241], s[38:39], v[184:185] op_sel_hi:[1,0,1]
	v_pk_fma_f32 v[166:167], v[206:207], s[36:37], v[166:167] op_sel_hi:[1,0,1]
	v_add_f32_e32 v188, v200, v188
	v_pk_fma_f32 v[178:179], v[244:245], s[28:29], v[178:179] op_sel_hi:[1,0,1]
	v_pk_fma_f32 v[164:165], v[222:223], s[38:39], v[164:165] op_sel_hi:[1,0,1]
	v_pk_fma_f32 v[184:185], v[198:199], s[36:37], v[184:185] op_sel_hi:[1,0,1]
	v_pk_mul_f32 v[198:199], v[166:167], v[166:167]
	v_add_f32_e32 v188, v201, v188
	v_cvt_pk_f32_fp8_sdwa v[244:245], v232 src0_sel:WORD_1
	v_pk_fma_f32 v[178:179], v[248:249], s[38:39], v[178:179] op_sel_hi:[1,0,1]
	v_pk_fma_f32 v[164:165], v[230:231], s[36:37], v[164:165] op_sel_hi:[1,0,1]
	v_add_f32_e32 v188, v198, v188
	v_cvt_pk_f32_fp8_e32 v[212:213], v225
	v_pk_fma_f32 v[178:179], v[196:197], s[36:37], v[178:179] op_sel_hi:[1,0,1]
	v_pk_mul_f32 v[196:197], v[164:165], v[164:165]
	v_add_f32_e32 v188, v199, v188
	v_pk_fma_f32 v[180:181], v[218:219], s[28:29], v[180:181] op_sel_hi:[1,0,1]
	v_cvt_pk_f32_fp8_e32 v[218:219], v233
	v_add_f32_e32 v188, v196, v188
	v_cvt_pk_f32_fp8_sdwa v[224:225], v225 src0_sel:WORD_1
	v_pk_mul_f32 v[210:211], v[178:179], v[178:179]
	v_add_f32_e32 v188, v197, v188
	v_cvt_pk_f32_fp8_sdwa v[232:233], v233 src0_sel:WORD_1
	v_pk_fma_f32 v[176:177], v[244:245], s[36:37], v[176:177] op_sel_hi:[1,0,1]
	v_add_f32_e32 v188, v210, v188
	v_pk_fma_f32 v[174:175], v[212:213], s[38:39], v[174:175] op_sel_hi:[1,0,1]
	v_pk_mul_f32 v[208:209], v[176:177], v[176:177]
	v_add_f32_e32 v188, v211, v188
	v_pk_fma_f32 v[174:175], v[218:219], s[36:37], v[174:175] op_sel_hi:[1,0,1]
	v_add_f32_e32 v188, v208, v188
	v_pk_fma_f32 v[172:173], v[224:225], s[38:39], v[172:173] op_sel_hi:[1,0,1]
	v_pk_mul_f32 v[206:207], v[174:175], v[174:175]
	v_add_f32_e32 v188, v209, v188
	v_pk_fma_f32 v[172:173], v[232:233], s[36:37], v[172:173] op_sel_hi:[1,0,1]
	v_add_f32_e32 v188, v206, v188
	v_pk_mul_f32 v[204:205], v[172:173], v[172:173]
	v_add_f32_e32 v188, v207, v188
	v_add_co_u32_e32 v20, vcc, s43, v0
	v_add_f32_e32 v188, v204, v188
	s_nop 0
	v_addc_co_u32_e32 v21, vcc, 0, v1, vcc
	v_cvt_pk_f32_fp8_sdwa v[226:227], v227 src0_sel:WORD_1
	v_pk_mul_f32 v[218:219], v[186:187], v[186:187]
	v_add_f32_e32 v188, v205, v188
	v_add_co_u32_e32 v28, vcc, s44, v0
	v_cvt_pk_f32_fp8_sdwa v[234:235], v235 src0_sel:WORD_1
	v_add_f32_e32 v188, v218, v188
	v_lshl_add_u64 v[4:5], v[0:1], 0, s[18:19]
	v_lshl_add_u64 v[8:9], v[0:1], 0, s[20:21]
	v_addc_co_u32_e32 v29, vcc, 0, v1, vcc
	v_lshl_add_u64 v[16:17], v[0:1], 0, s[22:23]
	v_lshl_add_u64 v[22:23], v[0:1], 0, s[24:25]
	v_lshl_add_u64 v[30:31], v[0:1], 0, s[26:27]
	v_lshl_add_u64 v[0:1], v[0:1], 0, s[30:31]
	v_pk_mul_f32 v[216:217], v[184:185], v[184:185]
	v_add_f32_e32 v188, v219, v188
	global_load_dwordx4 v[0:3], v[0:1], off offset:16
	s_nop 0
	global_load_dwordx4 v[60:63], v[20:21], off offset:-4096
	global_load_dwordx4 v[56:59], v[4:5], off offset:16
	global_load_dwordx4 v[44:47], v[4:5], off offset:2064
	global_load_dwordx4 v[52:55], v[4:5], off offset:2048
	s_nop 0
	global_load_dwordx4 v[4:7], v[8:9], off offset:16
	global_load_dwordx4 v[12:15], v[8:9], off offset:2048
	s_nop 0
	global_load_dwordx4 v[8:11], v[8:9], off offset:2064
	s_nop 0
	global_load_dwordx4 v[36:39], v[16:17], off offset:16
	global_load_dwordx4 v[24:27], v[28:29], off offset:-4096
	s_nop 0
	global_load_dwordx4 v[16:19], v[28:29], off
	global_load_dwordx4 v[48:51], v[20:21], off
	global_load_dwordx4 v[40:43], v[20:21], off offset:2048
	s_nop 0
	global_load_dwordx4 v[20:23], v[22:23], off offset:16
	s_nop 0
	global_load_dwordx4 v[32:35], v[30:31], off offset:16
	s_nop 0
	global_load_dwordx4 v[28:31], v[28:29], off offset:2048
	v_add_f32_e32 v188, v216, v188
	v_pk_fma_f32 v[180:181], v[226:227], s[38:39], v[180:181] op_sel_hi:[1,0,1]
	v_pk_mul_f32 v[214:215], v[182:183], v[182:183]
	v_add_f32_e32 v188, v217, v188
	v_pk_fma_f32 v[180:181], v[234:235], s[36:37], v[180:181] op_sel_hi:[1,0,1]
	v_add_f32_e32 v188, v214, v188
	v_pk_mul_f32 v[212:213], v[180:181], v[180:181]
	v_add_f32_e32 v188, v215, v188
	v_add_f32_e32 v188, v212, v188
	v_add_f32_e32 v188, v213, v188
	s_addc_u32 s17, s17, s35
	s_cmpk_lt_i32 s0, 0x4000
	v_add_f32_dpp v188, v188, v188 quad_perm:[1,0,3,2] row_mask:0xf bank_mask:0xf bound_ctrl:1
	s_nop 1
	v_add_f32_dpp v188, v188, v188 quad_perm:[2,3,0,1] row_mask:0xf bank_mask:0xf bound_ctrl:1
	s_nop 1
	v_add_f32_dpp v188, v188, v188 row_half_mirror row_mask:0xf bank_mask:0xf bound_ctrl:1
	s_nop 1
	v_add_f32_dpp v188, v188, v188 row_mirror row_mask:0xf bank_mask:0xf bound_ctrl:1
	s_nop 1
	v_mov_b32_dpp v152, v188 row_bcast:15 row_mask:0xa bank_mask:0xf
	v_add_f32_e32 v152, v188, v152
	s_nop 1
	v_mov_b32_dpp v153, v152 row_bcast:31 row_mask:0xc bank_mask:0xf
	v_add_f32_e32 v152, v152, v153
	s_nop 0
	v_readlane_b32 s28, v152, 63
	s_nop 1
	v_fma_f32 v152, s28, v151, v150
	v_mul_f32_e32 v153, 0x4b800000, v152
	v_cmp_gt_f32_e32 vcc, s41, v152
	s_nop 1
	v_cndmask_b32_e32 v152, v152, v153, vcc
	v_rsq_f32_e32 v152, v152
	s_nop 0
	v_mul_f32_e32 v153, 0x45800000, v152
	v_cndmask_b32_e32 v152, v152, v153, vcc
	v_pk_mul_f32 v[162:163], v[162:163], v[152:153] op_sel_hi:[1,0]
	v_pk_mul_f32 v[160:161], v[160:161], v[152:153] op_sel_hi:[1,0]
	v_pk_mul_f32 v[158:159], v[158:159], v[152:153] op_sel_hi:[1,0]
	v_pk_mul_f32 v[156:157], v[156:157], v[152:153] op_sel_hi:[1,0]
	v_pk_mul_f32 v[164:165], v[164:165], v[152:153] op_sel_hi:[1,0]
	v_pk_mul_f32 v[174:175], v[174:175], v[152:153] op_sel_hi:[1,0]
	s_waitcnt vmcnt(21)
	v_pk_fma_f32 v[92:93], v[92:93], v[162:163], v[128:129]
	v_pk_mul_f32 v[170:171], v[170:171], v[152:153] op_sel_hi:[1,0]
	v_pk_mul_f32 v[168:169], v[168:169], v[152:153] op_sel_hi:[1,0]
	v_pk_mul_f32 v[166:167], v[166:167], v[152:153] op_sel_hi:[1,0]
	v_pk_mul_f32 v[178:179], v[178:179], v[152:153] op_sel_hi:[1,0]
	v_pk_mul_f32 v[176:177], v[176:177], v[152:153] op_sel_hi:[1,0]
	v_pk_mul_f32 v[172:173], v[172:173], v[152:153] op_sel_hi:[1,0]
	v_pk_mul_f32 v[186:187], v[186:187], v[152:153] op_sel_hi:[1,0]
	v_pk_mul_f32 v[184:185], v[184:185], v[152:153] op_sel_hi:[1,0]
	v_pk_mul_f32 v[182:183], v[182:183], v[152:153] op_sel_hi:[1,0]
	v_pk_mul_f32 v[152:153], v[180:181], v[152:153] op_sel_hi:[1,0]
	v_pk_fma_f32 v[94:95], v[94:95], v[160:161], v[122:123]
	v_pk_fma_f32 v[84:85], v[84:85], v[158:159], v[118:119]
	v_pk_fma_f32 v[86:87], v[86:87], v[156:157], v[116:117]
	s_waitcnt vmcnt(19)
	v_pk_fma_f32 v[90:91], v[90:91], v[164:165], v[120:121]
	s_waitcnt vmcnt(18)
	v_pk_fma_f32 v[120:121], v[76:77], v[174:175], v[132:133]
	v_pk_mul_f32 v[132:133], v[92:93], v[92:93]
	v_pk_fma_f32 v[80:81], v[80:81], v[170:171], v[136:137]
	v_pk_fma_f32 v[82:83], v[82:83], v[168:169], v[130:131]
	v_pk_fma_f32 v[88:89], v[88:89], v[166:167], v[124:125]
	v_pk_fma_f32 v[116:117], v[72:73], v[178:179], v[142:143]
	v_pk_fma_f32 v[118:119], v[74:75], v[176:177], v[138:139]
	v_pk_fma_f32 v[122:123], v[78:79], v[172:173], v[126:127]
	s_waitcnt vmcnt(17)
	v_pk_fma_f32 v[124:125], v[68:69], v[186:187], v[146:147]
	v_pk_fma_f32 v[126:127], v[70:71], v[184:185], v[144:145]
	s_waitcnt vmcnt(16)
	v_pk_fma_f32 v[128:129], v[64:65], v[182:183], v[140:141]
	v_pk_fma_f32 v[130:131], v[66:67], v[152:153], v[134:135]
	v_pk_mul_f32 v[134:135], v[94:95], v[94:95]
	v_cvt_pk_bf16_f32 v64, v92, v93
	v_cvt_pk_bf16_f32 v65, v94, v95
	v_cvt_pk_bf16_f32 v66, v84, v85
	v_cvt_pk_bf16_f32 v67, v86, v87
	v_add_f32_e32 v132, v132, v133
	v_cvt_pk_bf16_f32 v68, v80, v81
	v_cvt_pk_bf16_f32 v69, v82, v83
	v_cvt_pk_bf16_f32 v70, v88, v89
	v_cvt_pk_bf16_f32 v71, v90, v91
	v_cvt_pk_bf16_f32 v72, v116, v117
	v_cvt_pk_bf16_f32 v73, v118, v119
	v_cvt_pk_bf16_f32 v74, v120, v121
	v_cvt_pk_bf16_f32 v75, v122, v123
	v_cvt_pk_bf16_f32 v76, v124, v125
	v_cvt_pk_bf16_f32 v77, v126, v127
	v_cvt_pk_bf16_f32 v78, v128, v129
	v_cvt_pk_bf16_f32 v79, v130, v131
	global_store_dwordx4 v[104:105], v[64:67], off offset:-2048 nt
	global_store_dwordx4 v[104:105], v[68:71], off offset:-1024 nt
	global_store_dwordx4 v[104:105], v[72:75], off nt
	global_store_dwordx4 v[104:105], v[76:79], off offset:1024 nt
	v_add_f32_e32 v64, v134, v132
	v_pk_mul_f32 v[136:137], v[84:85], v[84:85]
	v_add_f32_e32 v64, v135, v64
	v_add_f32_e32 v64, v136, v64
	v_pk_mul_f32 v[138:139], v[86:87], v[86:87]
	v_add_f32_e32 v64, v137, v64
	v_add_f32_e32 v64, v138, v64
	v_pk_mul_f32 v[140:141], v[80:81], v[80:81]
	v_add_f32_e32 v64, v139, v64
	v_add_f32_e32 v64, v140, v64
	v_pk_mul_f32 v[142:143], v[82:83], v[82:83]
	v_add_f32_e32 v64, v141, v64
	v_add_f32_e32 v64, v142, v64
	v_pk_mul_f32 v[144:145], v[88:89], v[88:89]
	v_add_f32_e32 v64, v143, v64
	v_add_f32_e32 v64, v144, v64
	v_pk_mul_f32 v[146:147], v[90:91], v[90:91]
	v_add_f32_e32 v64, v145, v64
	v_add_f32_e32 v64, v146, v64
	v_pk_mul_f32 v[152:153], v[116:117], v[116:117]
	v_add_f32_e32 v64, v147, v64
	v_add_f32_e32 v64, v152, v64
	v_pk_mul_f32 v[156:157], v[118:119], v[118:119]
	v_add_f32_e32 v64, v153, v64
	v_add_f32_e32 v64, v156, v64
	v_pk_mul_f32 v[158:159], v[120:121], v[120:121]
	v_add_f32_e32 v64, v157, v64
	v_add_f32_e32 v64, v158, v64
	v_pk_mul_f32 v[160:161], v[122:123], v[122:123]
	v_add_f32_e32 v64, v159, v64
	v_add_f32_e32 v64, v160, v64
	v_pk_mul_f32 v[162:163], v[124:125], v[124:125]
	v_add_f32_e32 v64, v161, v64
	v_add_f32_e32 v64, v162, v64
	v_pk_mul_f32 v[164:165], v[126:127], v[126:127]
	v_add_f32_e32 v64, v163, v64
	v_add_f32_e32 v64, v164, v64
	v_pk_mul_f32 v[166:167], v[128:129], v[128:129]
	v_add_f32_e32 v64, v165, v64
	v_add_f32_e32 v64, v166, v64
	v_pk_mul_f32 v[168:169], v[130:131], v[130:131]
	v_add_f32_e32 v64, v167, v64
	v_add_f32_e32 v64, v168, v64
	v_add_f32_e32 v64, v169, v64
	s_nop 1
	v_add_f32_dpp v64, v64, v64 quad_perm:[1,0,3,2] row_mask:0xf bank_mask:0xf bound_ctrl:1
	s_nop 1
	v_add_f32_dpp v64, v64, v64 quad_perm:[2,3,0,1] row_mask:0xf bank_mask:0xf bound_ctrl:1
	s_nop 1
	v_add_f32_dpp v64, v64, v64 row_half_mirror row_mask:0xf bank_mask:0xf bound_ctrl:1
	s_nop 1
	v_add_f32_dpp v64, v64, v64 row_mirror row_mask:0xf bank_mask:0xf bound_ctrl:1
	s_nop 1
	v_mov_b32_dpp v154, v64 row_bcast:15 row_mask:0xa bank_mask:0xf
	v_add_f32_e32 v64, v64, v154
	s_nop 1
	v_mov_b32_dpp v155, v64 row_bcast:31 row_mask:0xc bank_mask:0xf
	v_add_f32_e32 v64, v64, v155
	s_nop 0
	v_readlane_b32 s28, v64, 63
	s_nop 1
	v_fma_f32 v64, s28, v151, v150
	v_mul_f32_e32 v65, 0x4b800000, v64
	v_cmp_gt_f32_e32 vcc, s41, v64
	s_nop 1
	v_cndmask_b32_e32 v64, v64, v65, vcc
	v_rsq_f32_e32 v64, v64
	s_nop 0
	v_mul_f32_e32 v65, 0x45800000, v64
	v_cndmask_b32_e32 v64, v64, v65, vcc
	v_mul_f32_e32 v65, v92, v64
	v_mul_f32_e32 v66, v93, v64
	v_mul_f32_e32 v69, v84, v64
	v_mul_f32_e32 v70, v85, v64
	v_mul_f32_e32 v73, v80, v64
	v_mul_f32_e32 v74, v81, v64
	v_mul_f32_e32 v77, v88, v64
	v_mul_f32_e32 v78, v89, v64
	s_waitcnt vmcnt(10)
	v_fma_f32 v24, v60, v65, v24
	v_fma_f32 v25, v61, v66, v25
	v_fma_f32 v4, v56, v69, v4
	v_fma_f32 v5, v57, v70, v5
	v_mul_f32_e32 v71, v86, v64
	v_mul_f32_e32 v75, v82, v64
	v_mul_f32_e32 v81, v116, v64
	v_mul_f32_e32 v82, v117, v64
	v_mul_f32_e32 v85, v120, v64
	v_mul_f32_e32 v86, v121, v64
	v_fma_f32 v12, v52, v73, v12
	v_fma_f32 v13, v53, v74, v13
	v_fma_f32 v8, v44, v77, v8
	v_fma_f32 v9, v45, v78, v9
	v_cvt_pk_fp8_f32 v106, v24, v25
	v_cvt_pk_fp8_f32 v107, v4, v5
	v_mul_f32_e32 v67, v94, v64
	v_mul_f32_e32 v79, v90, v64
	v_mul_f32_e32 v89, v124, v64
	v_mul_f32_e32 v90, v125, v64
	v_mul_f32_e32 v93, v128, v64
	v_mul_f32_e32 v94, v129, v64
	s_waitcnt vmcnt(8)
	v_fma_f32 v16, v48, v81, v16
	v_fma_f32 v17, v49, v82, v17
	s_waitcnt vmcnt(6)
	v_fma_f32 v20, v36, v85, v20
	v_fma_f32 v21, v37, v86, v21
	v_cvt_pk_fp8_f32 v108, v12, v13
	v_cvt_pk_fp8_f32 v109, v8, v9
	v_mul_f32_e32 v68, v95, v64
	v_mul_f32_e32 v72, v87, v64
	s_waitcnt vmcnt(4)
	v_fma_f32 v28, v40, v89, v28
	v_fma_f32 v29, v41, v90, v29
	v_fma_f32 v0, v32, v93, v0
	v_fma_f32 v1, v33, v94, v1
	v_cvt_pk_fp8_f32 v110, v16, v17
	v_cvt_pk_fp8_f32 v111, v20, v21
	v_mul_f32_e32 v76, v83, v64
	v_mul_f32_e32 v80, v91, v64
	v_fma_f32 v26, v62, v67, v26
	v_fmac_f32_e32 v27, v63, v68
	v_fma_f32 v6, v58, v71, v6
	v_fmac_f32_e32 v7, v59, v72
	v_cvt_pk_fp8_f32 v112, v28, v29
	v_cvt_pk_fp8_f32 v113, v0, v1
	v_mul_f32_e32 v83, v118, v64
	v_mul_f32_e32 v84, v119, v64
	v_mul_f32_e32 v87, v122, v64
	v_mul_f32_e32 v88, v123, v64
	v_fma_f32 v14, v54, v75, v14
	v_fmac_f32_e32 v15, v55, v76
	v_fma_f32 v10, v46, v79, v10
	v_fmac_f32_e32 v11, v47, v80
	v_cvt_pk_fp8_f32 v106, v26, v27 op_sel:[0,0,1]
	v_cvt_pk_fp8_f32 v107, v6, v7 op_sel:[0,0,1]
	v_mul_f32_e32 v91, v126, v64
	v_mul_f32_e32 v92, v127, v64
	v_mul_f32_e32 v95, v130, v64
	v_mul_f32_e32 v64, v131, v64
	v_fma_f32 v18, v50, v83, v18
	v_fmac_f32_e32 v19, v51, v84
	v_fma_f32 v22, v38, v87, v22
	v_fmac_f32_e32 v23, v39, v88
	v_cvt_pk_fp8_f32 v108, v14, v15 op_sel:[0,0,1]
	v_cvt_pk_fp8_f32 v109, v10, v11 op_sel:[0,0,1]
	v_fma_f32 v30, v42, v91, v30
	v_fmac_f32_e32 v31, v43, v92
	v_fma_f32 v2, v34, v95, v2
	v_fmac_f32_e32 v3, v35, v64
	v_cvt_pk_fp8_f32 v110, v18, v19 op_sel:[0,0,1]
	v_cvt_pk_fp8_f32 v111, v22, v23 op_sel:[0,0,1]
	v_cvt_pk_fp8_f32 v112, v30, v31 op_sel:[0,0,1]
	v_cvt_pk_fp8_f32 v113, v2, v3 op_sel:[0,0,1]
	global_store_dwordx2 v[114:115], v[106:107], off offset:512
	global_store_dwordx2 v[114:115], v[108:109], off offset:1024
	global_store_dwordx2 v[114:115], v[110:111], off offset:1536
	global_store_dwordx2 v[114:115], v[112:113], off offset:2048
	s_cbranch_scc1 .LBB0_1546

.LBB0_2471:
	s_lshl_b32 s56, s55, 4
	v_add_u32_e32 v82, s56, v208
	v_or_b32_e32 v80, 1, v82
	v_ashrrev_i32_e32 v83, 31, v82
	v_ashrrev_i32_e32 v81, 31, v80
	v_lshlrev_b64 v[0:1], 12, v[82:83]
	v_lshlrev_b64 v[2:3], 12, v[80:81]
	v_lshl_add_u64 v[86:87], v[72:73], 0, v[0:1]
	v_lshl_add_u64 v[0:1], v[70:71], 0, v[0:1]
	v_lshl_add_u64 v[84:85], v[72:73], 0, v[2:3]
	v_lshl_add_u64 v[2:3], v[70:71], 0, v[2:3]
	global_load_dwordx4 v[54:57], v[86:87], off
	global_load_dwordx4 v[58:61], v[0:1], off
	global_load_dwordx4 v[112:115], v[84:85], off
	global_load_dwordx4 v[116:119], v[2:3], off
	global_load_dwordx4 v[130:133], v[86:87], off offset:1024
	global_load_dwordx4 v[134:137], v[0:1], off offset:1024
	global_load_dwordx4 v[162:165], v[0:1], off offset:2048
	global_load_dwordx4 v[44:47], v[0:1], off offset:3072
	global_load_dwordx4 v[166:169], v[86:87], off offset:2048
	global_load_dwordx4 v[36:39], v[86:87], off offset:3072
	global_load_dwordx4 v[140:143], v[2:3], off offset:1024
	global_load_dwordx4 v[48:51], v[2:3], off offset:2048
	global_load_dwordx4 v[40:43], v[2:3], off offset:3072
	global_load_dwordx4 v[144:147], v[84:85], off offset:1024
	global_load_dwordx4 v[180:183], v[84:85], off offset:2048
	global_load_dwordx4 v[32:35], v[84:85], off offset:3072
	v_lshrrev_b32_e32 v4, 20, v83
	v_add_u32_e32 v4, v82, v4
	v_ashrrev_i32_e32 v4, 12, v4
	v_mul_i32_i24_e32 v0, 6, v4
	v_ashrrev_i32_e32 v1, 31, v0
	v_lshlrev_b64 v[0:1], 13, v[0:1]
	v_lshl_add_u64 v[0:1], s[22:23], 0, v[0:1]
	v_lshl_add_u64 v[88:89], v[0:1], 0, v[78:79]
	global_load_dwordx4 v[24:27], v[88:89], off offset:16
	global_load_dwordx4 v[28:31], v[88:89], off
	global_load_dwordx4 v[8:11], v[88:89], off offset:2064
	global_load_dwordx4 v[16:19], v[88:89], off offset:2048
	v_add_co_u32_e32 v2, vcc, s48, v88
	v_lshl_add_u64 v[0:1], v[88:89], 0, s[30:31]
	s_nop 0
	v_addc_co_u32_e32 v3, vcc, 0, v89, vcc
	v_add_co_u32_e32 v52, vcc, s33, v88
	v_lshl_add_u64 v[62:63], v[88:89], 0, s[34:35]
	s_nop 0
	v_addc_co_u32_e32 v53, vcc, 0, v89, vcc
	global_load_dwordx4 v[20:23], v[52:53], off offset:-4096
	global_load_dwordx4 v[12:15], v[0:1], off offset:16
	global_load_dwordx4 v[4:7], v[2:3], off offset:2048
	s_nop 0
	global_load_dwordx4 v[0:3], v[62:63], off offset:16
	v_lshlrev_b64 v[80:81], 11, v[80:81]
	s_mov_b32 s28, 0
	s_waitcnt vmcnt(13)
	v_lshlrev_b32_e32 v122, 16, v142
	v_lshlrev_b32_e32 v106, 16, v59
	v_and_b32_e32 v205, 0xffff0000, v45
	v_and_b32_e32 v207, 0xffff0000, v44
	v_and_b32_e32 v107, 0xffff0000, v59
	v_lshlrev_b32_e32 v110, 16, v58
	v_and_b32_e32 v111, 0xffff0000, v58
	v_lshlrev_b32_e32 v62, 16, v113
	v_and_b32_e32 v63, 0xffff0000, v113
	v_lshlrev_b32_e32 v98, 16, v117
	v_and_b32_e32 v99, 0xffff0000, v117
	v_lshlrev_b32_e32 v102, 16, v112
	v_and_b32_e32 v103, 0xffff0000, v112
	v_lshlrev_b32_e32 v104, 16, v116
	v_and_b32_e32 v105, 0xffff0000, v116
	v_lshlrev_b32_e32 v234, 16, v131
	v_and_b32_e32 v235, 0xffff0000, v131
	v_lshlrev_b32_e32 v236, 16, v135
	v_and_b32_e32 v237, 0xffff0000, v135
	v_lshlrev_b32_e32 v240, 16, v130
	v_and_b32_e32 v241, 0xffff0000, v130
	v_lshlrev_b32_e32 v242, 16, v134
	v_and_b32_e32 v243, 0xffff0000, v134
	s_waitcnt vmcnt(10)
	v_lshlrev_b32_e32 v112, 16, v147
	v_and_b32_e32 v113, 0xffff0000, v147
	v_lshlrev_b32_e32 v116, 16, v146
	v_and_b32_e32 v117, 0xffff0000, v146
	v_lshlrev_b32_e32 v130, 16, v141
	v_and_b32_e32 v131, 0xffff0000, v141
	v_lshlrev_b32_e32 v134, 16, v140
	v_and_b32_e32 v135, 0xffff0000, v140
	v_lshlrev_b32_e32 v146, 16, v169
	v_and_b32_e32 v147, 0xffff0000, v169
	v_lshlrev_b32_e32 v154, 16, v168
	v_and_b32_e32 v155, 0xffff0000, v168
	v_lshlrev_b32_e32 v168, 16, v163
	v_and_b32_e32 v169, 0xffff0000, v163
	v_lshlrev_b32_e32 v252, 16, v162
	v_and_b32_e32 v253, 0xffff0000, v162
	v_lshlrev_b32_e32 v140, 16, v51
	v_and_b32_e32 v141, 0xffff0000, v51
	v_lshlrev_b32_e32 v148, 16, v50
	v_and_b32_e32 v149, 0xffff0000, v50
	s_waitcnt vmcnt(9)
	v_lshlrev_b32_e32 v50, 16, v181
	v_and_b32_e32 v51, 0xffff0000, v181
	v_lshlrev_b32_e32 v162, 16, v180
	v_and_b32_e32 v163, 0xffff0000, v180
	v_lshlrev_b32_e32 v204, 16, v45
	v_lshlrev_b32_e32 v206, 16, v44
	v_mov_b32_e32 v180, v205
	v_mov_b32_e32 v181, v207
	v_lshlrev_b32_e32 v96, 16, v60
	v_and_b32_e32 v97, 0xffff0000, v60
	v_pk_mul_f32 v[188:189], v[106:107], v[106:107]
	v_pk_mul_f32 v[190:191], v[110:111], v[110:111]
	v_and_b32_e32 v199, 0xffff0000, v47
	v_and_b32_e32 v203, 0xffff0000, v46
	v_mov_b32_e32 v44, v204
	v_mov_b32_e32 v45, v206
	v_pk_mul_f32 v[180:181], v[180:181], v[180:181]
	v_lshlrev_b32_e32 v92, 16, v61
	v_and_b32_e32 v93, 0xffff0000, v61
	v_pk_mul_f32 v[186:187], v[96:97], v[96:97]
	v_lshlrev_b32_e32 v198, 16, v47
	v_lshlrev_b32_e32 v202, 16, v46
	v_mov_b32_e32 v46, v199
	v_mov_b32_e32 v47, v203
	v_pk_fma_f32 v[44:45], v[44:45], v[44:45], v[180:181]
	v_add_f32_e32 v68, v188, v189
	v_add_f32_e32 v180, v190, v191
	v_pk_mul_f32 v[184:185], v[92:93], v[92:93]
	v_lshlrev_b32_e32 v196, 16, v39
	v_and_b32_e32 v197, 0xffff0000, v39
	v_lshlrev_b32_e32 v200, 16, v38
	v_and_b32_e32 v201, 0xffff0000, v38
	v_mov_b32_e32 v38, v198
	v_mov_b32_e32 v39, v202
	v_pk_mul_f32 v[46:47], v[46:47], v[46:47]
	v_add_f32_e32 v68, v180, v68
	v_add_f32_e32 v180, v186, v187
	v_pk_mul_f32 v[244:245], v[242:243], v[242:243]
	v_pk_fma_f32 v[38:39], v[38:39], v[38:39], v[46:47]
	v_add_f32_e32 v47, v184, v185
	v_add_f32_e32 v68, v180, v68
	v_lshlrev_b32_e32 v230, 16, v136
	v_and_b32_e32 v231, 0xffff0000, v136
	v_pk_mul_f32 v[238:239], v[236:237], v[236:237]
	v_add_f32_e32 v47, v47, v68
	v_add_f32_e32 v68, v244, v245
	v_lshlrev_b32_e32 v194, 16, v137
	v_and_b32_e32 v195, 0xffff0000, v137
	v_pk_mul_f32 v[232:233], v[230:231], v[230:231]
	v_add_f32_e32 v47, v68, v47
	v_add_f32_e32 v68, v238, v239
	v_pk_mul_f32 v[228:229], v[194:195], v[194:195]
	v_add_f32_e32 v47, v68, v47
	v_add_f32_e32 v68, v232, v233
	v_pk_mul_f32 v[214:215], v[252:253], v[252:253]
	v_add_f32_e32 v47, v68, v47
	v_add_f32_e32 v68, v228, v229
	v_lshlrev_b32_e32 v156, 16, v164
	v_and_b32_e32 v157, 0xffff0000, v164
	v_pk_mul_f32 v[250:251], v[168:169], v[168:169]
	v_add_f32_e32 v47, v68, v47
	v_add_f32_e32 v68, v214, v215
	v_lshlrev_b32_e32 v152, 16, v165
	v_and_b32_e32 v153, 0xffff0000, v165
	v_pk_mul_f32 v[248:249], v[156:157], v[156:157]
	v_add_f32_e32 v47, v68, v47
	v_add_f32_e32 v68, v250, v251
	v_pk_mul_f32 v[246:247], v[152:153], v[152:153]
	v_add_f32_e32 v47, v68, v47
	v_add_f32_e32 v68, v248, v249
	v_add_f32_e32 v47, v68, v47
	v_add_f32_e32 v68, v246, v247
	v_add_f32_e32 v47, v68, v47
	v_add_f32_e32 v45, v45, v47
	v_add_f32_e32 v44, v44, v45
	v_add_f32_e32 v39, v39, v44
	v_add_f32_e32 v38, v38, v39
	v_mov_b32_e32 v39, 0
	v_lshlrev_b32_e32 v44, 16, v36
	v_add_f32_dpp v38, v38, v38 quad_perm:[1,0,3,2] row_mask:0xf bank_mask:0xf bound_ctrl:1
	v_and_b32_e32 v45, 0xffff0000, v36
	v_lshlrev_b32_e32 v108, 16, v54
	v_add_f32_dpp v38, v38, v38 quad_perm:[2,3,0,1] row_mask:0xf bank_mask:0xf bound_ctrl:1
	v_and_b32_e32 v109, 0xffff0000, v54
	v_lshlrev_b32_e32 v46, 16, v37
	v_add_f32_dpp v38, v38, v38 row_half_mirror row_mask:0xf bank_mask:0xf bound_ctrl:1
	v_and_b32_e32 v47, 0xffff0000, v37
	v_lshlrev_b32_e32 v100, 16, v55
	v_add_f32_dpp v38, v38, v38 row_mirror row_mask:0xf bank_mask:0xf bound_ctrl:1
	v_and_b32_e32 v101, 0xffff0000, v55
	v_lshlrev_b32_e32 v94, 16, v56
	v_mov_b32_dpp v39, v38 row_bcast:15 row_mask:0xa bank_mask:0xf
	v_add_f32_e32 v38, v38, v39
	v_mov_b32_e32 v39, 0
	v_and_b32_e32 v95, 0xffff0000, v56
	v_lshlrev_b32_e32 v90, 16, v57
	v_mov_b32_dpp v39, v38 row_bcast:31 row_mask:0xc bank_mask:0xf
	v_add_f32_e32 v38, v38, v39
	v_and_b32_e32 v91, 0xffff0000, v57
	v_readlane_b32 s18, v38, 63
	v_lshlrev_b32_e32 v192, 16, v132
	v_and_b32_e32 v193, 0xffff0000, v132
	v_fma_f32 v38, s18, v224, v221
	v_mul_f32_e32 v39, 0x4b800000, v38
	v_cmp_gt_f32_e32 vcc, s49, v38
	v_lshlrev_b32_e32 v172, 16, v133
	v_and_b32_e32 v173, 0xffff0000, v133
	v_cndmask_b32_e32 v38, v38, v39, vcc
	v_rsq_f32_e32 v38, v38
	v_lshlrev_b32_e32 v164, 16, v167
	v_and_b32_e32 v165, 0xffff0000, v167
	v_lshlrev_b32_e32 v170, 16, v166
	v_mul_f32_e32 v36, 0x45800000, v38
	v_cndmask_b32_e32 v68, v38, v36, vcc
	v_pk_mul_f32 v[36:37], v[68:69], v[110:111] op_sel_hi:[0,1]
	s_waitcnt vmcnt(6)
	v_pk_fma_f32 v[108:109], v[28:29], v[36:37], v[108:109]
	v_pk_mul_f32 v[36:37], v[68:69], v[106:107] op_sel_hi:[0,1]
	v_pk_fma_f32 v[110:111], v[30:31], v[36:37], v[100:101]
	v_pk_mul_f32 v[36:37], v[68:69], v[96:97] op_sel_hi:[0,1]
	v_pk_fma_f32 v[106:107], v[24:25], v[36:37], v[94:95]
	v_pk_mul_f32 v[36:37], v[68:69], v[92:93] op_sel_hi:[0,1]
	v_pk_fma_f32 v[100:101], v[26:27], v[36:37], v[90:91]
	v_pk_mul_f32 v[36:37], v[68:69], v[242:243] op_sel_hi:[0,1]
	s_waitcnt vmcnt(4)
	v_pk_fma_f32 v[94:95], v[16:17], v[36:37], v[240:241]
	v_pk_mul_f32 v[36:37], v[68:69], v[236:237] op_sel_hi:[0,1]
	v_pk_fma_f32 v[96:97], v[18:19], v[36:37], v[234:235]
	v_pk_mul_f32 v[36:37], v[68:69], v[230:231] op_sel_hi:[0,1]
	v_pk_fma_f32 v[92:93], v[8:9], v[36:37], v[192:193]
	v_pk_mul_f32 v[36:37], v[68:69], v[194:195] op_sel_hi:[0,1]
	v_and_b32_e32 v171, 0xffff0000, v166
	v_pk_fma_f32 v[90:91], v[10:11], v[36:37], v[172:173]
	v_pk_mul_f32 v[172:173], v[68:69], v[252:253] op_sel_hi:[0,1]
	v_pk_mul_f32 v[168:169], v[68:69], v[168:169] op_sel_hi:[0,1]
	v_pk_mul_f32 v[152:153], v[68:69], v[152:153] op_sel_hi:[0,1]
	v_lshlrev_b32_e32 v56, 16, v119
	v_and_b32_e32 v57, 0xffff0000, v119
	s_waitcnt vmcnt(3)
	v_pk_fma_f32 v[170:171], v[20:21], v[172:173], v[170:171]
	v_pk_fma_f32 v[172:173], v[22:23], v[168:169], v[164:165]
	s_waitcnt vmcnt(2)
	v_pk_fma_f32 v[164:165], v[14:15], v[152:153], v[146:147]
	v_pk_mul_f32 v[146:147], v[68:69], v[206:207] op_sel_hi:[0,1]
	v_lshlrev_b32_e32 v60, 16, v118
	v_and_b32_e32 v61, 0xffff0000, v118
	v_pk_mul_f32 v[120:121], v[56:57], v[56:57]
	v_pk_mul_f32 v[124:125], v[98:99], v[98:99]
	v_pk_mul_f32 v[128:129], v[104:105], v[104:105]
	v_pk_mul_f32 v[156:157], v[68:69], v[156:157] op_sel_hi:[0,1]
	s_waitcnt vmcnt(1)
	v_pk_fma_f32 v[152:153], v[4:5], v[146:147], v[44:45]
	v_pk_mul_f32 v[146:147], v[68:69], v[202:203] op_sel_hi:[0,1]
	v_pk_mul_f32 v[118:119], v[60:61], v[60:61]
	v_pk_fma_f32 v[168:169], v[12:13], v[156:157], v[154:155]
	v_pk_mul_f32 v[44:45], v[68:69], v[204:205] op_sel_hi:[0,1]
	s_waitcnt vmcnt(0)
	v_pk_fma_f32 v[154:155], v[0:1], v[146:147], v[200:201]
	v_pk_mul_f32 v[146:147], v[68:69], v[198:199] op_sel_hi:[0,1]
	v_add_f32_e32 v68, v120, v121
	v_add_f32_e32 v120, v124, v125
	v_add_f32_e32 v121, v128, v129
	v_add_f32_e32 v120, v121, v120
	v_add_f32_e32 v118, v118, v119
	v_pk_mul_f32 v[160:161], v[134:135], v[134:135]
	v_add_f32_e32 v118, v118, v120
	v_and_b32_e32 v123, 0xffff0000, v142
	v_pk_mul_f32 v[150:151], v[130:131], v[130:131]
	v_add_f32_e32 v68, v68, v118
	v_add_f32_e32 v118, v160, v161
	v_lshlrev_b32_e32 v54, 16, v115
	v_and_b32_e32 v55, 0xffff0000, v115
	v_lshlrev_b32_e32 v58, 16, v114
	v_and_b32_e32 v59, 0xffff0000, v114
	v_lshlrev_b32_e32 v114, 16, v143
	v_and_b32_e32 v115, 0xffff0000, v143
	v_pk_mul_f32 v[142:143], v[122:123], v[122:123]
	v_add_f32_e32 v68, v118, v68
	v_add_f32_e32 v118, v150, v151
	v_pk_mul_f32 v[138:139], v[114:115], v[114:115]
	v_lshlrev_b32_e32 v166, 16, v48
	v_and_b32_e32 v167, 0xffff0000, v48
	v_add_f32_e32 v68, v118, v68
	v_add_f32_e32 v118, v142, v143
	v_lshlrev_b32_e32 v158, 16, v49
	v_and_b32_e32 v159, 0xffff0000, v49
	v_pk_mul_f32 v[48:49], v[166:167], v[166:167]
	v_add_f32_e32 v68, v118, v68
	v_add_f32_e32 v118, v138, v139
	v_pk_mul_f32 v[178:179], v[158:159], v[158:159]
	v_add_f32_e32 v68, v118, v68
	v_add_f32_e32 v48, v48, v49
	v_pk_mul_f32 v[176:177], v[148:149], v[148:149]
	v_and_b32_e32 v239, 0xffff0000, v41
	v_and_b32_e32 v241, 0xffff0000, v40
	v_add_f32_e32 v48, v48, v68
	v_add_f32_e32 v49, v178, v179
	v_pk_mul_f32 v[174:175], v[140:141], v[140:141]
	v_lshlrev_b32_e32 v238, 16, v41
	v_lshlrev_b32_e32 v240, 16, v40
	v_mov_b32_e32 v242, v239
	v_mov_b32_e32 v243, v241
	v_add_f32_e32 v48, v49, v48
	v_add_f32_e32 v49, v176, v177
	v_pk_fma_f32 v[146:147], v[2:3], v[146:147], v[196:197]
	v_lshlrev_b32_e32 v196, 16, v35
	v_and_b32_e32 v197, 0xffff0000, v35
	v_and_b32_e32 v199, 0xffff0000, v43
	v_and_b32_e32 v35, 0xffff0000, v42
	v_mov_b32_e32 v40, v238
	v_mov_b32_e32 v41, v240
	v_pk_mul_f32 v[242:243], v[242:243], v[242:243]
	v_add_f32_e32 v48, v49, v48
	v_add_f32_e32 v49, v174, v175
	v_lshlrev_b32_e32 v198, 16, v43
	v_lshlrev_b32_e32 v234, 16, v34
	v_and_b32_e32 v235, 0xffff0000, v34
	v_lshlrev_b32_e32 v34, 16, v42
	v_mov_b32_e32 v236, v199
	v_mov_b32_e32 v237, v35
	v_pk_fma_f32 v[40:41], v[40:41], v[40:41], v[242:243]
	v_add_f32_e32 v48, v49, v48
	v_mov_b32_e32 v42, v198
	v_mov_b32_e32 v43, v34
	v_pk_mul_f32 v[236:237], v[236:237], v[236:237]
	v_add_f32_e32 v41, v41, v48
	v_pk_fma_f32 v[42:43], v[42:43], v[42:43], v[236:237]
	v_add_f32_e32 v40, v40, v41
	v_add_f32_e32 v40, v43, v40
	v_add_f32_e32 v40, v42, v40
	v_mov_b32_e32 v41, 0
	v_lshlrev_b32_e32 v132, 16, v144
	v_add_f32_dpp v40, v40, v40 quad_perm:[1,0,3,2] row_mask:0xf bank_mask:0xf bound_ctrl:1
	v_and_b32_e32 v133, 0xffff0000, v144
	v_lshlrev_b32_e32 v126, 16, v145
	v_add_f32_dpp v40, v40, v40 quad_perm:[2,3,0,1] row_mask:0xf bank_mask:0xf bound_ctrl:1
	v_and_b32_e32 v127, 0xffff0000, v145
	v_lshlrev_b32_e32 v144, 16, v182
	v_add_f32_dpp v40, v40, v40 row_half_mirror row_mask:0xf bank_mask:0xf bound_ctrl:1
	v_and_b32_e32 v145, 0xffff0000, v182
	v_lshlrev_b32_e32 v136, 16, v183
	v_add_f32_dpp v40, v40, v40 row_mirror row_mask:0xf bank_mask:0xf bound_ctrl:1
	v_and_b32_e32 v137, 0xffff0000, v183
	v_pk_mul_f32 v[180:181], v[108:109], v[108:109]
	v_mov_b32_dpp v41, v40 row_bcast:15 row_mask:0xa bank_mask:0xf
	v_add_f32_e32 v40, v40, v41
	v_mov_b32_e32 v41, 0
	v_pk_mul_f32 v[182:183], v[110:111], v[110:111]
	v_add_f32_e32 v68, v180, v181
	v_mov_b32_dpp v41, v40 row_bcast:31 row_mask:0xc bank_mask:0xf
	v_add_f32_e32 v40, v40, v41
	v_lshlrev_b32_e32 v236, 16, v33
	v_readlane_b32 s18, v40, 63
	v_and_b32_e32 v237, 0xffff0000, v33
	v_add_f32_e32 v68, v182, v68
	v_fma_f32 v40, s18, v224, v221
	v_mul_f32_e32 v41, 0x4b800000, v40
	v_cmp_gt_f32_e32 vcc, s49, v40
	v_pk_mul_f32 v[184:185], v[106:107], v[106:107]
	v_lshl_add_u64 v[36:37], v[88:89], 0, s[46:47]
	v_cndmask_b32_e32 v40, v40, v41, vcc
	v_rsq_f32_e32 v42, v40
	v_lshlrev_b32_e32 v40, 16, v32
	v_and_b32_e32 v41, 0xffff0000, v32
	v_lshl_add_u64 v[202:203], v[88:89], 0, s[36:37]
	v_mul_f32_e32 v32, 0x45800000, v42
	v_cndmask_b32_e32 v32, v42, v32, vcc
	v_pk_mul_f32 v[42:43], v[32:33], v[104:105] op_sel_hi:[0,1]
	v_pk_fma_f32 v[142:143], v[28:29], v[42:43], v[102:103]
	v_pk_mul_f32 v[28:29], v[32:33], v[98:99] op_sel_hi:[0,1]
	v_pk_fma_f32 v[150:151], v[30:31], v[28:29], v[62:63]
	v_pk_mul_f32 v[28:29], v[32:33], v[60:61] op_sel_hi:[0,1]
	v_pk_fma_f32 v[160:161], v[24:25], v[28:29], v[58:59]
	v_pk_mul_f32 v[24:25], v[32:33], v[56:57] op_sel_hi:[0,1]
	v_pk_fma_f32 v[138:139], v[26:27], v[24:25], v[54:55]
	v_pk_mul_f32 v[24:25], v[32:33], v[134:135] op_sel_hi:[0,1]
	v_pk_fma_f32 v[124:125], v[16:17], v[24:25], v[132:133]
	v_pk_mul_f32 v[16:17], v[32:33], v[130:131] op_sel_hi:[0,1]
	v_pk_fma_f32 v[126:127], v[18:19], v[16:17], v[126:127]
	v_pk_mul_f32 v[16:17], v[32:33], v[122:123] op_sel_hi:[0,1]
	v_pk_fma_f32 v[128:129], v[8:9], v[16:17], v[116:117]
	v_pk_mul_f32 v[8:9], v[32:33], v[114:115] op_sel_hi:[0,1]
	v_pk_fma_f32 v[122:123], v[10:11], v[8:9], v[112:113]
	v_pk_mul_f32 v[8:9], v[32:33], v[166:167] op_sel_hi:[0,1]
	v_pk_fma_f32 v[116:117], v[20:21], v[8:9], v[162:163]
	v_pk_mul_f32 v[8:9], v[32:33], v[158:159] op_sel_hi:[0,1]
	v_pk_fma_f32 v[118:119], v[22:23], v[8:9], v[50:51]
	v_pk_mul_f32 v[8:9], v[32:33], v[148:149] op_sel_hi:[0,1]
	v_pk_fma_f32 v[120:121], v[12:13], v[8:9], v[144:145]
	v_pk_mul_f32 v[8:9], v[32:33], v[140:141] op_sel_hi:[0,1]
	v_pk_fma_f32 v[114:115], v[14:15], v[8:9], v[136:137]
	v_pk_mul_f32 v[8:9], v[32:33], v[240:241] op_sel_hi:[0,1]
	v_pk_fma_f32 v[102:103], v[4:5], v[8:9], v[40:41]
	v_pk_mul_f32 v[4:5], v[32:33], v[238:239] op_sel_hi:[0,1]
	v_pk_fma_f32 v[104:105], v[6:7], v[4:5], v[236:237]
	v_pk_mul_f32 v[4:5], v[32:33], v[34:35] op_sel_hi:[0,1]
	v_add_f32_e32 v68, v183, v68
	global_load_dwordx4 v[36:39], v[36:37], off offset:16
	v_pk_fma_f32 v[156:157], v[6:7], v[44:45], v[46:47]
	global_load_dwordx4 v[44:47], v[202:203], off offset:16
	v_pk_fma_f32 v[112:113], v[0:1], v[4:5], v[234:235]
	v_pk_mul_f32 v[0:1], v[32:33], v[198:199] op_sel_hi:[0,1]
	v_add_co_u32_e32 v8, vcc, s51, v88
	v_add_f32_e32 v68, v184, v68
	v_pk_mul_f32 v[186:187], v[100:101], v[100:101]
	v_pk_fma_f32 v[98:99], v[2:3], v[0:1], v[196:197]
	v_lshl_add_u64 v[0:1], v[88:89], 0, s[38:39]
	v_addc_co_u32_e32 v9, vcc, 0, v89, vcc
	global_load_dwordx4 v[56:59], v[52:53], off
	global_load_dwordx4 v[60:63], v[8:9], off offset:-4096
	global_load_dwordx4 v[28:31], v[202:203], off offset:2064
	global_load_dwordx4 v[40:43], v[202:203], off offset:2048
	s_nop 0
	global_load_dwordx4 v[52:55], v[0:1], off offset:16
	global_load_dwordx4 v[48:51], v[0:1], off offset:2048
	v_add_f32_e32 v68, v185, v68
	v_lshl_add_u64 v[2:3], v[88:89], 0, s[40:41]
	global_load_dwordx4 v[32:35], v[0:1], off offset:2064
	global_load_dwordx4 v[12:15], v[2:3], off offset:16
	v_add_f32_e32 v68, v186, v68
	v_pk_mul_f32 v[188:189], v[94:95], v[94:95]
	v_add_f32_e32 v68, v187, v68
	v_add_f32_e32 v68, v188, v68
	v_pk_mul_f32 v[190:191], v[96:97], v[96:97]
	v_add_f32_e32 v68, v189, v68
	v_add_f32_e32 v68, v190, v68
	v_pk_mul_f32 v[192:193], v[92:93], v[92:93]
	v_add_f32_e32 v68, v191, v68
	v_add_f32_e32 v68, v192, v68
	v_pk_mul_f32 v[194:195], v[90:91], v[90:91]
	v_add_co_u32_e32 v4, vcc, s50, v88
	v_add_f32_e32 v68, v193, v68
	s_nop 0
	v_addc_co_u32_e32 v5, vcc, 0, v89, vcc
	v_lshl_add_u64 v[0:1], v[88:89], 0, s[42:43]
	v_lshl_add_u64 v[2:3], v[88:89], 0, s[44:45]
	v_add_f32_e32 v68, v194, v68
	v_pk_mul_f32 v[214:215], v[170:171], v[170:171]
	global_load_dwordx4 v[20:23], v[4:5], off
	s_nop 0
	global_load_dwordx4 v[4:7], v[4:5], off offset:2048
	s_nop 0
	global_load_dwordx4 v[16:19], v[0:1], off offset:16
	s_nop 0
	global_load_dwordx4 v[0:3], v[2:3], off offset:16
	s_nop 0
	global_load_dwordx4 v[24:27], v[8:9], off
	s_nop 0
	global_load_dwordx4 v[8:11], v[8:9], off offset:2048
	v_add_f32_e32 v68, v195, v68
	v_add_f32_e32 v68, v214, v68
	v_pk_mul_f32 v[228:229], v[172:173], v[172:173]
	v_add_f32_e32 v68, v215, v68
	v_add_f32_e32 v68, v228, v68
	v_pk_mul_f32 v[230:231], v[168:169], v[168:169]
	v_add_f32_e32 v68, v229, v68
	v_add_f32_e32 v68, v230, v68
	v_pk_mul_f32 v[232:233], v[164:165], v[164:165]
	v_add_f32_e32 v68, v231, v68
	v_add_f32_e32 v68, v232, v68
	v_pk_mul_f32 v[206:207], v[152:153], v[152:153]
	v_add_f32_e32 v68, v233, v68
	v_add_f32_e32 v68, v206, v68
	v_pk_mul_f32 v[204:205], v[156:157], v[156:157]
	v_add_f32_e32 v68, v207, v68
	v_add_f32_e32 v68, v204, v68
	v_pk_mul_f32 v[200:201], v[154:155], v[154:155]
	v_add_f32_e32 v68, v205, v68
	v_add_f32_e32 v68, v200, v68
	v_pk_mul_f32 v[130:131], v[146:147], v[146:147]
	v_add_f32_e32 v68, v201, v68
	v_add_f32_e32 v68, v130, v68
	v_add_f32_e32 v68, v131, v68
	v_cvt_pk_bf16_f32 v130, v108, v109
	v_cvt_pk_bf16_f32 v131, v110, v111
	v_cvt_pk_bf16_f32 v132, v106, v107
	v_cvt_pk_bf16_f32 v133, v100, v101
	global_store_dwordx4 v[86:87], v[130:133], off nt
	v_pk_mul_f32 v[174:175], v[142:143], v[142:143]
	v_pk_mul_f32 v[176:177], v[150:151], v[150:151]
	v_cvt_pk_bf16_f32 v130, v94, v95
	v_cvt_pk_bf16_f32 v131, v96, v97
	v_cvt_pk_bf16_f32 v132, v92, v93
	v_cvt_pk_bf16_f32 v133, v90, v91
	global_store_dwordx4 v[86:87], v[130:133], off offset:1024 nt
	v_pk_mul_f32 v[178:179], v[160:161], v[160:161]
	v_pk_mul_f32 v[242:243], v[138:139], v[138:139]
	v_cvt_pk_bf16_f32 v130, v170, v171
	v_cvt_pk_bf16_f32 v131, v172, v173
	v_cvt_pk_bf16_f32 v132, v168, v169
	v_cvt_pk_bf16_f32 v133, v164, v165
	global_store_dwordx4 v[86:87], v[130:133], off offset:2048 nt
	v_pk_mul_f32 v[134:135], v[124:125], v[124:125]
	v_pk_mul_f32 v[244:245], v[126:127], v[126:127]
	v_cvt_pk_bf16_f32 v130, v152, v153
	v_cvt_pk_bf16_f32 v131, v156, v157
	v_cvt_pk_bf16_f32 v132, v154, v155
	v_cvt_pk_bf16_f32 v133, v146, v147
	global_store_dwordx4 v[86:87], v[130:133], off offset:3072 nt
	v_pk_mul_f32 v[246:247], v[128:129], v[128:129]
	v_pk_mul_f32 v[248:249], v[122:123], v[122:123]
	v_add_f32_e32 v130, v174, v175
	v_add_f32_e32 v130, v176, v130
	v_add_f32_e32 v130, v177, v130
	v_add_f32_e32 v130, v178, v130
	v_add_f32_e32 v130, v179, v130
	v_add_f32_e32 v130, v242, v130
	v_add_f32_e32 v130, v243, v130
	v_add_f32_e32 v130, v134, v130
	v_add_f32_e32 v130, v135, v130
	v_add_f32_e32 v130, v244, v130
	v_add_f32_e32 v130, v245, v130
	v_add_f32_e32 v130, v246, v130
	v_add_f32_e32 v130, v247, v130
	v_add_f32_e32 v130, v248, v130
	v_pk_mul_f32 v[162:163], v[116:117], v[116:117]
	v_add_f32_e32 v130, v249, v130
	v_add_f32_e32 v130, v162, v130
	v_pk_mul_f32 v[158:159], v[118:119], v[118:119]
	v_add_f32_e32 v130, v163, v130
	v_add_f32_e32 v130, v158, v130
	v_pk_mul_f32 v[144:145], v[120:121], v[120:121]
	v_add_f32_e32 v130, v159, v130
	v_add_f32_e32 v130, v144, v130
	v_pk_mul_f32 v[136:137], v[114:115], v[114:115]
	v_add_f32_e32 v130, v145, v130
	v_add_f32_e32 v130, v136, v130
	v_pk_mul_f32 v[140:141], v[102:103], v[102:103]
	v_add_f32_e32 v130, v137, v130
	v_add_f32_e32 v130, v140, v130
	v_add_f32_dpp v68, v68, v68 quad_perm:[1,0,3,2] row_mask:0xf bank_mask:0xf bound_ctrl:1
	v_pk_mul_f32 v[148:149], v[104:105], v[104:105]
	v_add_f32_e32 v130, v141, v130
	v_add_f32_dpp v68, v68, v68 quad_perm:[2,3,0,1] row_mask:0xf bank_mask:0xf bound_ctrl:1
	v_add_f32_e32 v130, v148, v130
	v_pk_mul_f32 v[166:167], v[112:113], v[112:113]
	v_add_f32_dpp v68, v68, v68 row_half_mirror row_mask:0xf bank_mask:0xf bound_ctrl:1
	v_add_f32_e32 v130, v149, v130
	v_mov_b32_e32 v131, 0
	v_add_f32_dpp v68, v68, v68 row_mirror row_mask:0xf bank_mask:0xf bound_ctrl:1
	v_add_f32_e32 v130, v166, v130
	v_pk_mul_f32 v[196:197], v[98:99], v[98:99]
	v_mov_b32_dpp v131, v68 row_bcast:15 row_mask:0xa bank_mask:0xf
	v_add_f32_e32 v130, v167, v130
	v_add_f32_e32 v68, v68, v131
	v_mov_b32_e32 v131, 0
	v_add_f32_e32 v130, v196, v130
	v_add_f32_e32 v130, v197, v130
	v_mov_b32_dpp v131, v68 row_bcast:31 row_mask:0xc bank_mask:0xf
	v_add_f32_e32 v68, v68, v131
	v_cvt_pk_bf16_f32 v86, v142, v143
	v_readlane_b32 s18, v68, 63
	v_add_f32_dpp v68, v130, v130 quad_perm:[1,0,3,2] row_mask:0xf bank_mask:0xf bound_ctrl:1
	v_mov_b32_e32 v130, 0
	v_cvt_pk_bf16_f32 v87, v150, v151
	v_add_f32_dpp v68, v68, v68 quad_perm:[2,3,0,1] row_mask:0xf bank_mask:0xf bound_ctrl:1
	v_cvt_pk_bf16_f32 v88, v160, v161
	v_cvt_pk_bf16_f32 v89, v138, v139
	v_add_f32_dpp v68, v68, v68 row_half_mirror row_mask:0xf bank_mask:0xf bound_ctrl:1
	global_store_dwordx4 v[84:85], v[86:89], off nt
	v_lshlrev_b64 v[132:133], 11, v[82:83]
	v_add_f32_dpp v68, v68, v68 row_mirror row_mask:0xf bank_mask:0xf bound_ctrl:1
	v_cvt_pk_bf16_f32 v86, v124, v125
	v_cvt_pk_bf16_f32 v87, v126, v127
	v_mov_b32_dpp v130, v68 row_bcast:15 row_mask:0xa bank_mask:0xf
	v_add_f32_e32 v68, v68, v130
	v_mov_b32_e32 v130, 0
	v_cvt_pk_bf16_f32 v88, v128, v129
	v_cvt_pk_bf16_f32 v89, v122, v123
	v_mov_b32_dpp v130, v68 row_bcast:31 row_mask:0xc bank_mask:0xf
	v_add_f32_e32 v68, v68, v130
	global_store_dwordx4 v[84:85], v[86:89], off offset:1024 nt
	v_readlane_b32 s19, v68, 63
	v_fma_f32 v68, s18, v224, v221
	v_mul_f32_e32 v130, 0x4b800000, v68
	v_cmp_gt_f32_e32 vcc, s49, v68
	v_cvt_pk_bf16_f32 v86, v116, v117
	v_cvt_pk_bf16_f32 v87, v118, v119
	v_cndmask_b32_e32 v68, v68, v130, vcc
	v_fma_f32 v130, s19, v224, v221
	v_rsq_f32_e32 v68, v68
	v_mul_f32_e32 v131, 0x4b800000, v130
	v_cmp_gt_f32_e64 s[18:19], s49, v130
	v_cvt_pk_bf16_f32 v88, v120, v121
	v_cvt_pk_bf16_f32 v89, v114, v115
	v_cndmask_b32_e64 v130, v130, v131, s[18:19]
	v_rsq_f32_e32 v131, v130
	global_store_dwordx4 v[84:85], v[86:89], off offset:2048 nt
	s_nop 1
	v_cvt_pk_bf16_f32 v86, v102, v103
	v_cvt_pk_bf16_f32 v87, v104, v105
	v_cvt_pk_bf16_f32 v88, v112, v113
	v_cvt_pk_bf16_f32 v89, v98, v99
	global_store_dwordx4 v[84:85], v[86:89], off offset:3072 nt
	v_mul_f32_e32 v84, 0x45800000, v68
	v_cndmask_b32_e32 v130, v68, v84, vcc
	v_pk_mul_f32 v[82:83], v[108:109], v[130:131] op_sel_hi:[1,0]
	v_pk_mul_f32 v[86:87], v[106:107], v[130:131] op_sel_hi:[1,0]
	s_waitcnt vmcnt(20)
	v_pk_fma_f32 v[82:83], v[56:57], v[82:83], v[60:61]
	v_pk_mul_f32 v[84:85], v[110:111], v[130:131] op_sel_hi:[1,0]
	s_waitcnt vmcnt(17)
	v_pk_fma_f32 v[86:87], v[44:45], v[86:87], v[52:53]
	v_mov_b32_e32 v110, 0
	v_mov_b32_e32 v111, 0
	v_pk_mul_f32 v[94:95], v[94:95], v[130:131] op_sel_hi:[1,0]
	v_pk_mul_f32 v[92:93], v[92:93], v[130:131] op_sel_hi:[1,0]
	v_cvt_pk_fp8_f32 v110, v82, v83
	v_cvt_pk_fp8_f32 v111, v86, v87
	s_waitcnt vmcnt(16)
	v_pk_fma_f32 v[94:95], v[40:41], v[94:95], v[48:49]
	s_waitcnt vmcnt(15)
	v_pk_fma_f32 v[106:107], v[28:29], v[92:93], v[32:33]
	v_mov_b32_e32 v92, 0
	v_mov_b32_e32 v93, 0
	v_cvt_pk_fp8_f32 v92, v94, v95
	v_cvt_pk_fp8_f32 v93, v106, v107
	v_pk_mul_f32 v[88:89], v[100:101], v[130:131] op_sel_hi:[1,0]
	v_pk_fma_f32 v[84:85], v[58:59], v[84:85], v[62:63]
	v_pk_fma_f32 v[88:89], v[46:47], v[88:89], v[54:55]
	v_pk_mul_f32 v[96:97], v[96:97], v[130:131] op_sel_hi:[1,0]
	v_pk_mul_f32 v[90:91], v[90:91], v[130:131] op_sel_hi:[1,0]
	v_cvt_pk_fp8_f32 v110, v84, v85 op_sel:[0,0,1]
	v_cvt_pk_fp8_f32 v111, v88, v89 op_sel:[0,0,1]
	v_pk_fma_f32 v[96:97], v[42:43], v[96:97], v[50:51]
	v_pk_fma_f32 v[108:109], v[30:31], v[90:91], v[34:35]
	v_cvt_pk_fp8_f32 v92, v96, v97 op_sel:[0,0,1]
	v_cvt_pk_fp8_f32 v93, v108, v109 op_sel:[0,0,1]
	v_lshl_add_u64 v[100:101], v[76:77], 0, v[132:133]
	global_store_dwordx2 v[100:101], v[110:111], off
	ds_write_b128 v213, v[82:85]
	ds_write_b128 v213, v[86:89] offset:16
	v_pk_mul_f32 v[82:83], v[170:171], v[130:131] op_sel_hi:[1,0]
	v_pk_mul_f32 v[86:87], v[168:169], v[130:131] op_sel_hi:[1,0]
	global_store_dwordx2 v[100:101], v[92:93], off offset:512
	ds_write_b128 v213, v[94:97] offset:2048
	ds_write_b128 v213, v[106:109] offset:2064
	s_waitcnt vmcnt(11)
	v_pk_fma_f32 v[82:83], v[20:21], v[82:83], v[24:25]
	v_pk_fma_f32 v[86:87], v[12:13], v[86:87], v[16:17]
	v_mov_b32_e32 v106, 0
	v_mov_b32_e32 v107, 0
	v_cvt_pk_fp8_f32 v106, v82, v83
	v_cvt_pk_fp8_f32 v107, v86, v87
	v_pk_mul_f32 v[84:85], v[172:173], v[130:131] op_sel_hi:[1,0]
	v_pk_mul_f32 v[88:89], v[164:165], v[130:131] op_sel_hi:[1,0]
	v_pk_fma_f32 v[84:85], v[22:23], v[84:85], v[26:27]
	v_pk_fma_f32 v[88:89], v[14:15], v[88:89], v[18:19]
	v_cvt_pk_fp8_f32 v106, v84, v85 op_sel:[0,0,1]
	v_cvt_pk_fp8_f32 v107, v88, v89 op_sel:[0,0,1]
	v_mul_f32_e32 v68, 0x45800000, v131
	v_cndmask_b32_e64 v68, v131, v68, s[18:19]
	v_pk_mul_f32 v[90:91], v[152:153], v[130:131] op_sel_hi:[1,0]
	global_store_dwordx2 v[100:101], v[106:107], off offset:1024
	ds_write_b128 v213, v[82:85] offset:4096
	ds_write_b128 v213, v[86:89] offset:4112
	v_pk_mul_f32 v[82:83], v[142:143], v[68:69] op_sel_hi:[1,0]
	v_pk_mul_f32 v[94:95], v[154:155], v[130:131] op_sel_hi:[1,0]
	v_pk_fma_f32 v[56:57], v[56:57], v[82:83], v[60:61]
	v_pk_mul_f32 v[60:61], v[150:151], v[68:69] op_sel_hi:[1,0]
	s_waitcnt vmcnt(11)
	v_pk_fma_f32 v[90:91], v[4:5], v[90:91], v[8:9]
	v_pk_fma_f32 v[58:59], v[58:59], v[60:61], v[62:63]
	v_pk_mul_f32 v[60:61], v[160:161], v[68:69] op_sel_hi:[1,0]
	v_pk_fma_f32 v[94:95], v[0:1], v[94:95], v[36:37]
	v_pk_fma_f32 v[44:45], v[44:45], v[60:61], v[52:53]
	v_pk_mul_f32 v[60:61], v[138:139], v[68:69] op_sel_hi:[1,0]
	v_mov_b32_e32 v108, 0
	v_pk_fma_f32 v[46:47], v[46:47], v[60:61], v[54:55]
	v_pk_mul_f32 v[60:61], v[124:125], v[68:69] op_sel_hi:[1,0]
	v_mov_b32_e32 v109, 0
	v_pk_fma_f32 v[40:41], v[40:41], v[60:61], v[48:49]
	v_pk_mul_f32 v[48:49], v[126:127], v[68:69] op_sel_hi:[1,0]
	v_mov_b32_e32 v52, 0
	v_pk_fma_f32 v[42:43], v[42:43], v[48:49], v[50:51]
	v_pk_mul_f32 v[48:49], v[128:129], v[68:69] op_sel_hi:[1,0]
	v_mov_b32_e32 v53, 0
	v_pk_fma_f32 v[28:29], v[28:29], v[48:49], v[32:33]
	v_mov_b32_e32 v32, 0
	v_mov_b32_e32 v33, 0
	v_cvt_pk_fp8_f32 v108, v90, v91
	v_cvt_pk_fp8_f32 v109, v94, v95
	v_cvt_pk_fp8_f32 v52, v56, v57
	v_cvt_pk_fp8_f32 v53, v44, v45
	v_cvt_pk_fp8_f32 v32, v40, v41
	v_cvt_pk_fp8_f32 v33, v28, v29
	v_pk_mul_f32 v[92:93], v[156:157], v[130:131] op_sel_hi:[1,0]
	v_pk_mul_f32 v[96:97], v[146:147], v[130:131] op_sel_hi:[1,0]
	v_pk_mul_f32 v[48:49], v[122:123], v[68:69] op_sel_hi:[1,0]
	v_pk_fma_f32 v[92:93], v[6:7], v[92:93], v[10:11]
	v_pk_fma_f32 v[96:97], v[2:3], v[96:97], v[38:39]
	v_pk_fma_f32 v[30:31], v[30:31], v[48:49], v[34:35]
	v_cvt_pk_fp8_f32 v108, v92, v93 op_sel:[0,0,1]
	v_cvt_pk_fp8_f32 v109, v96, v97 op_sel:[0,0,1]
	v_cvt_pk_fp8_f32 v52, v58, v59 op_sel:[0,0,1]
	v_cvt_pk_fp8_f32 v53, v46, v47 op_sel:[0,0,1]
	v_cvt_pk_fp8_f32 v32, v42, v43 op_sel:[0,0,1]
	v_cvt_pk_fp8_f32 v33, v30, v31 op_sel:[0,0,1]
	v_lshl_add_u64 v[54:55], v[76:77], 0, v[80:81]
	global_store_dwordx2 v[100:101], v[108:109], off offset:1536
	ds_write_b128 v213, v[90:93] offset:6144
	ds_write_b128 v213, v[94:97] offset:6160
	global_store_dwordx2 v[54:55], v[52:53], off
	ds_write_b128 v213, v[56:59] offset:8208
	ds_write_b128 v213, v[44:47] offset:8224
	global_store_dwordx2 v[54:55], v[32:33], off offset:512
	ds_write_b128 v213, v[40:43] offset:10256
	ds_write_b128 v213, v[28:31] offset:10272
	v_pk_mul_f32 v[28:29], v[116:117], v[68:69] op_sel_hi:[1,0]
	v_readfirstlane_b32 s18, v65
	v_pk_fma_f32 v[20:21], v[20:21], v[28:29], v[24:25]
	v_pk_mul_f32 v[24:25], v[118:119], v[68:69] op_sel_hi:[1,0]
	s_ashr_i32 s19, s18, 31
	v_pk_fma_f32 v[22:23], v[22:23], v[24:25], v[26:27]
	v_pk_mul_f32 v[24:25], v[120:121], v[68:69] op_sel_hi:[1,0]
	s_lshl_b64 s[18:19], s[18:19], 16
	v_pk_fma_f32 v[12:13], v[12:13], v[24:25], v[16:17]
	v_pk_mul_f32 v[24:25], v[114:115], v[68:69] op_sel_hi:[1,0]
	v_mov_b32_e32 v16, 0
	v_pk_fma_f32 v[14:15], v[14:15], v[24:25], v[18:19]
	v_pk_mul_f32 v[18:19], v[102:103], v[68:69] op_sel_hi:[1,0]
	v_mov_b32_e32 v17, 0
	v_pk_fma_f32 v[4:5], v[4:5], v[18:19], v[8:9]
	v_pk_mul_f32 v[8:9], v[104:105], v[68:69] op_sel_hi:[1,0]
	v_cvt_pk_fp8_f32 v16, v20, v21
	v_pk_fma_f32 v[6:7], v[6:7], v[8:9], v[10:11]
	v_pk_mul_f32 v[8:9], v[112:113], v[68:69] op_sel_hi:[1,0]
	v_cvt_pk_fp8_f32 v17, v12, v13
	v_pk_fma_f32 v[0:1], v[0:1], v[8:9], v[36:37]
	v_mov_b32_e32 v8, 0
	v_mov_b32_e32 v9, 0
	v_cvt_pk_fp8_f32 v8, v4, v5
	v_cvt_pk_fp8_f32 v9, v0, v1
	v_pk_mul_f32 v[10:11], v[98:99], v[68:69] op_sel_hi:[1,0]
	v_cvt_pk_fp8_f32 v16, v22, v23 op_sel:[0,0,1]
	v_pk_fma_f32 v[2:3], v[2:3], v[10:11], v[38:39]
	v_cvt_pk_fp8_f32 v17, v14, v15 op_sel:[0,0,1]
	v_cvt_pk_fp8_f32 v8, v6, v7 op_sel:[0,0,1]
	v_cvt_pk_fp8_f32 v9, v2, v3 op_sel:[0,0,1]
	s_add_u32 s18, s16, s18
	v_mov_b32_e32 v68, v209
	global_store_dwordx2 v[54:55], v[16:17], off offset:1024
	ds_write_b128 v213, v[20:23] offset:12304
	ds_write_b128 v213, v[12:15] offset:12320
	global_store_dwordx2 v[54:55], v[8:9], off offset:1536
	ds_write_b128 v213, v[4:7] offset:14352
	ds_write_b128 v213, v[0:3] offset:14368
	s_addc_u32 s19, s17, s19
	global_load_dwordx4 v[0:3], v68, s[18:19]
	global_load_dwordx4 v[4:7], v68, s[18:19] offset:1024
	global_load_dwordx4 v[8:11], v68, s[18:19] offset:2048
	global_load_dwordx4 v[12:15], v68, s[18:19] offset:3072
	v_lshl_add_u64 v[16:17], s[18:19], 0, v[68:69]
	v_add_co_u32_e32 v28, vcc, s48, v16
	v_mov_b32_e32 v68, v210
	s_nop 0
	v_addc_co_u32_e32 v29, vcc, 0, v17, vcc
	global_load_dwordx4 v[16:19], v[28:29], off
	global_load_dwordx4 v[20:23], v[28:29], off offset:1024
	global_load_dwordx4 v[24:27], v[28:29], off offset:2048
	s_nop 0
	global_load_dwordx4 v[28:31], v[28:29], off offset:3072
	s_waitcnt lgkmcnt(0)
	s_barrier
	ds_read2_b32 v[44:45], v211 offset1:4
	s_waitcnt vmcnt(7) lgkmcnt(0)
	v_mfma_f32_16x16x4_f32 v[32:35], v44, v0, 0
	ds_read2_b32 v[52:53], v211 offset0:24 offset1:28
	v_mfma_f32_16x16x4_f32 v[36:39], v44, v1, 0
	v_mfma_f32_16x16x4_f32 v[40:43], v44, v2, 0
	v_mfma_f32_16x16x4_f32 v[0:3], v44, v3, 0
	s_waitcnt vmcnt(6)
	v_mfma_f32_16x16x4_f32 v[32:35], v45, v4, v[32:35]
	v_mfma_f32_16x16x4_f32 v[36:39], v45, v5, v[36:39]
	v_mfma_f32_16x16x4_f32 v[40:43], v45, v6, v[40:43]
	v_mfma_f32_16x16x4_f32 v[0:3], v45, v7, v[0:3]
	ds_read2_b32 v[44:45], v211 offset0:8 offset1:12
	s_waitcnt vmcnt(5) lgkmcnt(0)
	v_mfma_f32_16x16x4_f32 v[4:7], v44, v8, v[32:35]
	v_mfma_f32_16x16x4_f32 v[32:35], v44, v9, v[36:39]
	v_mfma_f32_16x16x4_f32 v[36:39], v44, v10, v[40:43]
	v_mfma_f32_16x16x4_f32 v[0:3], v44, v11, v[0:3]
	s_waitcnt vmcnt(4)
	v_mfma_f32_16x16x4_f32 v[8:11], v45, v13, v[32:35]
	v_mfma_f32_16x16x4_f32 v[32:35], v45, v14, v[36:39]
	s_nop 5
	ds_read2_b32 v[36:37], v211 offset0:16 offset1:20
	v_mfma_f32_16x16x4_f32 v[4:7], v45, v12, v[4:7]
	v_mfma_f32_16x16x4_f32 v[0:3], v45, v15, v[0:3]
	s_waitcnt vmcnt(3) lgkmcnt(0)
	v_mfma_f32_16x16x4_f32 v[4:7], v36, v16, v[4:7]
	v_mfma_f32_16x16x4_f32 v[8:11], v36, v17, v[8:11]
	v_mfma_f32_16x16x4_f32 v[12:15], v36, v18, v[32:35]
	v_mfma_f32_16x16x4_f32 v[0:3], v36, v19, v[0:3]
	global_load_dwordx4 v[16:19], v68, s[18:19]
	s_waitcnt vmcnt(3)
	v_mfma_f32_16x16x4_f32 v[4:7], v37, v20, v[4:7]
	v_mfma_f32_16x16x4_f32 v[8:11], v37, v21, v[8:11]
	v_mfma_f32_16x16x4_f32 v[12:15], v37, v22, v[12:15]
	v_mfma_f32_16x16x4_f32 v[0:3], v37, v23, v[0:3]
	global_load_dwordx4 v[20:23], v68, s[18:19] offset:1024
	s_waitcnt vmcnt(3)
	v_mfma_f32_16x16x4_f32 v[4:7], v52, v24, v[4:7]
	v_mfma_f32_16x16x4_f32 v[8:11], v52, v25, v[8:11]
	v_mfma_f32_16x16x4_f32 v[12:15], v52, v26, v[12:15]
	v_mfma_f32_16x16x4_f32 v[0:3], v52, v27, v[0:3]
	global_load_dwordx4 v[24:27], v68, s[18:19] offset:2048
	global_load_dwordx4 v[32:35], v68, s[18:19] offset:3072
	s_waitcnt vmcnt(4)
	v_mfma_f32_16x16x4_f32 v[4:7], v53, v28, v[4:7]
	v_mfma_f32_16x16x4_f32 v[8:11], v53, v29, v[8:11]
	v_lshl_add_u64 v[28:29], s[18:19], 0, v[68:69]
	v_add_co_u32_e32 v28, vcc, s48, v28
	v_mov_b32_e32 v68, v216
	s_nop 0
	v_addc_co_u32_e32 v29, vcc, 0, v29, vcc
	global_load_dwordx4 v[36:39], v[28:29], off
	global_load_dwordx4 v[40:43], v[28:29], off offset:1024
	global_load_dwordx4 v[44:47], v[28:29], off offset:2048
	global_load_dwordx4 v[48:51], v[28:29], off offset:3072
	ds_read2_b32 v[28:29], v211 offset0:32 offset1:36
	v_mfma_f32_16x16x4_f32 v[12:15], v53, v30, v[12:15]
	v_mfma_f32_16x16x4_f32 v[0:3], v53, v31, v[0:3]
	ds_read2_b32 v[52:53], v211 offset0:56 offset1:60
	s_waitcnt vmcnt(7) lgkmcnt(1)
	v_mfma_f32_16x16x4_f32 v[4:7], v28, v16, v[4:7]
	v_mfma_f32_16x16x4_f32 v[8:11], v28, v17, v[8:11]
	ds_read2_b32 v[16:17], v211 offset0:40 offset1:44
	v_mfma_f32_16x16x4_f32 v[12:15], v28, v18, v[12:15]
	v_mfma_f32_16x16x4_f32 v[0:3], v28, v19, v[0:3]
	s_waitcnt vmcnt(6)
	v_mfma_f32_16x16x4_f32 v[4:7], v29, v20, v[4:7]
	v_mfma_f32_16x16x4_f32 v[8:11], v29, v21, v[8:11]
	v_mfma_f32_16x16x4_f32 v[12:15], v29, v22, v[12:15]
	v_mfma_f32_16x16x4_f32 v[0:3], v29, v23, v[0:3]
	global_load_dwordx4 v[20:23], v68, s[18:19] offset:1024
	s_waitcnt vmcnt(6) lgkmcnt(0)
	v_mfma_f32_16x16x4_f32 v[4:7], v16, v24, v[4:7]
	v_mfma_f32_16x16x4_f32 v[8:11], v16, v25, v[8:11]
	v_mfma_f32_16x16x4_f32 v[12:15], v16, v26, v[12:15]
	v_mfma_f32_16x16x4_f32 v[0:3], v16, v27, v[0:3]
	s_waitcnt vmcnt(5)
	v_mfma_f32_16x16x4_f32 v[4:7], v17, v32, v[4:7]
	v_mfma_f32_16x16x4_f32 v[8:11], v17, v33, v[8:11]
	v_lshl_add_u64 v[32:33], s[18:19], 0, v[68:69]
	v_mfma_f32_16x16x4_f32 v[12:15], v17, v34, v[12:15]
	v_mfma_f32_16x16x4_f32 v[0:3], v17, v35, v[0:3]
	ds_read2_b32 v[16:17], v211 offset0:48 offset1:52
	s_waitcnt vmcnt(4) lgkmcnt(0)
	v_mfma_f32_16x16x4_f32 v[4:7], v16, v36, v[4:7]
	v_mfma_f32_16x16x4_f32 v[8:11], v16, v37, v[8:11]
	v_mfma_f32_16x16x4_f32 v[12:15], v16, v38, v[12:15]
	v_mfma_f32_16x16x4_f32 v[0:3], v16, v39, v[0:3]
	s_waitcnt vmcnt(3)
	v_mfma_f32_16x16x4_f32 v[4:7], v17, v40, v[4:7]
	v_mfma_f32_16x16x4_f32 v[8:11], v17, v41, v[8:11]
	v_mfma_f32_16x16x4_f32 v[12:15], v17, v42, v[12:15]
	v_mfma_f32_16x16x4_f32 v[0:3], v17, v43, v[0:3]
	global_load_dwordx4 v[16:19], v68, s[18:19]
	global_load_dwordx4 v[24:27], v68, s[18:19] offset:2048
	global_load_dwordx4 v[28:31], v68, s[18:19] offset:3072
	v_mov_b32_e32 v68, v227
	s_waitcnt vmcnt(5)
	v_mfma_f32_16x16x4_f32 v[4:7], v52, v44, v[4:7]
	v_add_co_u32_e32 v44, vcc, s48, v32
	v_mfma_f32_16x16x4_f32 v[8:11], v52, v45, v[8:11]
	s_nop 0
	v_addc_co_u32_e32 v45, vcc, 0, v33, vcc
	v_mfma_f32_16x16x4_f32 v[12:15], v52, v46, v[12:15]
	v_mfma_f32_16x16x4_f32 v[0:3], v52, v47, v[0:3]
	global_load_dwordx4 v[32:35], v[44:45], off
	global_load_dwordx4 v[36:39], v[44:45], off offset:1024
	global_load_dwordx4 v[40:43], v[44:45], off offset:2048
	s_nop 0
	global_load_dwordx4 v[44:47], v[44:45], off offset:3072
	s_waitcnt vmcnt(8)
	v_mfma_f32_16x16x4_f32 v[4:7], v53, v48, v[4:7]
	v_mfma_f32_16x16x4_f32 v[8:11], v53, v49, v[8:11]
	ds_read2_b32 v[48:49], v211 offset0:64 offset1:68
	v_mfma_f32_16x16x4_f32 v[12:15], v53, v50, v[12:15]
	v_mfma_f32_16x16x4_f32 v[0:3], v53, v51, v[0:3]
	ds_read2_b32 v[52:53], v211 offset0:88 offset1:92
	s_waitcnt vmcnt(6) lgkmcnt(1)
	v_mfma_f32_16x16x4_f32 v[4:7], v48, v16, v[4:7]
	v_mfma_f32_16x16x4_f32 v[8:11], v48, v17, v[8:11]
	ds_read2_b32 v[16:17], v211 offset0:72 offset1:76
	v_mfma_f32_16x16x4_f32 v[12:15], v48, v18, v[12:15]
	v_mfma_f32_16x16x4_f32 v[0:3], v48, v19, v[0:3]
	v_mfma_f32_16x16x4_f32 v[4:7], v49, v20, v[4:7]
	v_mfma_f32_16x16x4_f32 v[8:11], v49, v21, v[8:11]
	v_mfma_f32_16x16x4_f32 v[12:15], v49, v22, v[12:15]
	v_mfma_f32_16x16x4_f32 v[0:3], v49, v23, v[0:3]
	global_load_dwordx4 v[20:23], v68, s[18:19] offset:1024
	s_waitcnt vmcnt(6) lgkmcnt(0)
	v_mfma_f32_16x16x4_f32 v[4:7], v16, v24, v[4:7]
	v_mfma_f32_16x16x4_f32 v[8:11], v16, v25, v[8:11]
	v_mfma_f32_16x16x4_f32 v[12:15], v16, v26, v[12:15]
	v_mfma_f32_16x16x4_f32 v[0:3], v16, v27, v[0:3]
	s_waitcnt vmcnt(5)
	v_mfma_f32_16x16x4_f32 v[4:7], v17, v28, v[4:7]
	v_mfma_f32_16x16x4_f32 v[8:11], v17, v29, v[8:11]
	v_mfma_f32_16x16x4_f32 v[12:15], v17, v30, v[12:15]
	v_mfma_f32_16x16x4_f32 v[0:3], v17, v31, v[0:3]
	ds_read2_b32 v[16:17], v211 offset0:80 offset1:84
	s_waitcnt vmcnt(4) lgkmcnt(0)
	v_mfma_f32_16x16x4_f32 v[4:7], v16, v32, v[4:7]
	v_mfma_f32_16x16x4_f32 v[8:11], v16, v33, v[8:11]
	v_lshl_add_u64 v[32:33], s[18:19], 0, v[68:69]
	v_mfma_f32_16x16x4_f32 v[12:15], v16, v34, v[12:15]
	v_mfma_f32_16x16x4_f32 v[0:3], v16, v35, v[0:3]
	s_waitcnt vmcnt(3)
	v_mfma_f32_16x16x4_f32 v[4:7], v17, v36, v[4:7]
	v_mfma_f32_16x16x4_f32 v[8:11], v17, v37, v[8:11]
	v_mfma_f32_16x16x4_f32 v[12:15], v17, v38, v[12:15]
	v_mfma_f32_16x16x4_f32 v[0:3], v17, v39, v[0:3]
	global_load_dwordx4 v[16:19], v68, s[18:19]
	global_load_dwordx4 v[24:27], v68, s[18:19] offset:2048
	global_load_dwordx4 v[28:31], v68, s[18:19] offset:3072
	v_mov_b32_e32 v68, v217
	s_waitcnt vmcnt(5)
	v_mfma_f32_16x16x4_f32 v[4:7], v52, v40, v[4:7]
	v_mfma_f32_16x16x4_f32 v[8:11], v52, v41, v[8:11]
	s_waitcnt vmcnt(4)
	v_mfma_f32_16x16x4_f32 v[4:7], v53, v44, v[4:7]
	v_add_co_u32_e32 v44, vcc, s48, v32
	v_mfma_f32_16x16x4_f32 v[8:11], v53, v45, v[8:11]
	s_nop 0
	v_addc_co_u32_e32 v45, vcc, 0, v33, vcc
	v_mfma_f32_16x16x4_f32 v[12:15], v52, v42, v[12:15]
	v_mfma_f32_16x16x4_f32 v[0:3], v52, v43, v[0:3]
	global_load_dwordx4 v[32:35], v[44:45], off
	global_load_dwordx4 v[36:39], v[44:45], off offset:1024
	global_load_dwordx4 v[40:43], v[44:45], off offset:2048
	global_load_dwordx4 v[48:51], v[44:45], off offset:3072
	ds_read2_b32 v[44:45], v211 offset0:96 offset1:100
	v_mfma_f32_16x16x4_f32 v[12:15], v53, v46, v[12:15]
	v_mfma_f32_16x16x4_f32 v[0:3], v53, v47, v[0:3]
	ds_read2_b32 v[52:53], v211 offset0:120 offset1:124
	s_waitcnt vmcnt(6) lgkmcnt(1)
	v_mfma_f32_16x16x4_f32 v[4:7], v44, v16, v[4:7]
	v_mfma_f32_16x16x4_f32 v[8:11], v44, v17, v[8:11]
	ds_read2_b32 v[16:17], v211 offset0:104 offset1:108
	v_mfma_f32_16x16x4_f32 v[12:15], v44, v18, v[12:15]
	v_mfma_f32_16x16x4_f32 v[0:3], v44, v19, v[0:3]
	v_mfma_f32_16x16x4_f32 v[4:7], v45, v20, v[4:7]
	v_mfma_f32_16x16x4_f32 v[8:11], v45, v21, v[8:11]
	v_mfma_f32_16x16x4_f32 v[12:15], v45, v22, v[12:15]
	v_mfma_f32_16x16x4_f32 v[0:3], v45, v23, v[0:3]
	global_load_dwordx4 v[20:23], v68, s[18:19] offset:1024
	s_waitcnt vmcnt(6) lgkmcnt(0)
	v_mfma_f32_16x16x4_f32 v[4:7], v16, v24, v[4:7]
	v_mfma_f32_16x16x4_f32 v[8:11], v16, v25, v[8:11]
	v_mfma_f32_16x16x4_f32 v[12:15], v16, v26, v[12:15]
	v_mfma_f32_16x16x4_f32 v[0:3], v16, v27, v[0:3]
	s_waitcnt vmcnt(5)
	v_mfma_f32_16x16x4_f32 v[4:7], v17, v28, v[4:7]
	v_mfma_f32_16x16x4_f32 v[8:11], v17, v29, v[8:11]
	v_mfma_f32_16x16x4_f32 v[12:15], v17, v30, v[12:15]
	v_mfma_f32_16x16x4_f32 v[0:3], v17, v31, v[0:3]
	ds_read2_b32 v[16:17], v211 offset0:112 offset1:116
	s_waitcnt vmcnt(4) lgkmcnt(0)
	v_mfma_f32_16x16x4_f32 v[4:7], v16, v32, v[4:7]
	v_mfma_f32_16x16x4_f32 v[8:11], v16, v33, v[8:11]
	v_lshl_add_u64 v[32:33], s[18:19], 0, v[68:69]
	v_add_co_u32_e32 v44, vcc, s48, v32
	s_nop 1
	v_addc_co_u32_e32 v45, vcc, 0, v33, vcc
	v_mfma_f32_16x16x4_f32 v[12:15], v16, v34, v[12:15]
	v_mfma_f32_16x16x4_f32 v[0:3], v16, v35, v[0:3]
	s_waitcnt vmcnt(3)
	v_mfma_f32_16x16x4_f32 v[4:7], v17, v36, v[4:7]
	v_mfma_f32_16x16x4_f32 v[8:11], v17, v37, v[8:11]
	v_mfma_f32_16x16x4_f32 v[12:15], v17, v38, v[12:15]
	v_mfma_f32_16x16x4_f32 v[0:3], v17, v39, v[0:3]
	global_load_dwordx4 v[16:19], v68, s[18:19]
	global_load_dwordx4 v[24:27], v68, s[18:19] offset:2048
	global_load_dwordx4 v[28:31], v68, s[18:19] offset:3072
	v_mov_b32_e32 v68, v218
	s_waitcnt vmcnt(5)
	v_mfma_f32_16x16x4_f32 v[4:7], v52, v40, v[4:7]
	v_mfma_f32_16x16x4_f32 v[8:11], v52, v41, v[8:11]
	v_mfma_f32_16x16x4_f32 v[12:15], v52, v42, v[12:15]
	v_mfma_f32_16x16x4_f32 v[0:3], v52, v43, v[0:3]
	global_load_dwordx4 v[32:35], v[44:45], off
	global_load_dwordx4 v[36:39], v[44:45], off offset:1024
	global_load_dwordx4 v[40:43], v[44:45], off offset:2048
	s_nop 0
	global_load_dwordx4 v[44:47], v[44:45], off offset:3072
	s_waitcnt vmcnt(8)
	v_mfma_f32_16x16x4_f32 v[4:7], v53, v48, v[4:7]
	v_mfma_f32_16x16x4_f32 v[8:11], v53, v49, v[8:11]
	ds_read2_b32 v[48:49], v211 offset0:128 offset1:132
	v_mfma_f32_16x16x4_f32 v[12:15], v53, v50, v[12:15]
	v_mfma_f32_16x16x4_f32 v[0:3], v53, v51, v[0:3]
	ds_read2_b32 v[52:53], v211 offset0:152 offset1:156
	s_waitcnt vmcnt(6) lgkmcnt(1)
	v_mfma_f32_16x16x4_f32 v[4:7], v48, v16, v[4:7]
	v_mfma_f32_16x16x4_f32 v[8:11], v48, v17, v[8:11]
	ds_read2_b32 v[16:17], v211 offset0:136 offset1:140
	v_mfma_f32_16x16x4_f32 v[12:15], v48, v18, v[12:15]
	v_mfma_f32_16x16x4_f32 v[0:3], v48, v19, v[0:3]
	v_mfma_f32_16x16x4_f32 v[4:7], v49, v20, v[4:7]
	v_mfma_f32_16x16x4_f32 v[8:11], v49, v21, v[8:11]
	v_mfma_f32_16x16x4_f32 v[12:15], v49, v22, v[12:15]
	v_mfma_f32_16x16x4_f32 v[0:3], v49, v23, v[0:3]
	global_load_dwordx4 v[20:23], v68, s[18:19] offset:1024
	s_waitcnt vmcnt(6) lgkmcnt(0)
	v_mfma_f32_16x16x4_f32 v[4:7], v16, v24, v[4:7]
	v_mfma_f32_16x16x4_f32 v[8:11], v16, v25, v[8:11]
	v_mfma_f32_16x16x4_f32 v[12:15], v16, v26, v[12:15]
	v_mfma_f32_16x16x4_f32 v[0:3], v16, v27, v[0:3]
	s_waitcnt vmcnt(5)
	v_mfma_f32_16x16x4_f32 v[4:7], v17, v28, v[4:7]
	v_mfma_f32_16x16x4_f32 v[8:11], v17, v29, v[8:11]
	v_mfma_f32_16x16x4_f32 v[12:15], v17, v30, v[12:15]
	v_mfma_f32_16x16x4_f32 v[0:3], v17, v31, v[0:3]
	ds_read2_b32 v[16:17], v211 offset0:144 offset1:148
	s_waitcnt vmcnt(4) lgkmcnt(0)
	v_mfma_f32_16x16x4_f32 v[4:7], v16, v32, v[4:7]
	v_mfma_f32_16x16x4_f32 v[8:11], v16, v33, v[8:11]
	v_lshl_add_u64 v[32:33], s[18:19], 0, v[68:69]
	v_mfma_f32_16x16x4_f32 v[12:15], v16, v34, v[12:15]
	v_mfma_f32_16x16x4_f32 v[0:3], v16, v35, v[0:3]
	s_waitcnt vmcnt(3)
	v_mfma_f32_16x16x4_f32 v[4:7], v17, v36, v[4:7]
	v_mfma_f32_16x16x4_f32 v[8:11], v17, v37, v[8:11]
	v_mfma_f32_16x16x4_f32 v[12:15], v17, v38, v[12:15]
	v_mfma_f32_16x16x4_f32 v[0:3], v17, v39, v[0:3]
	global_load_dwordx4 v[16:19], v68, s[18:19]
	global_load_dwordx4 v[24:27], v68, s[18:19] offset:2048
	global_load_dwordx4 v[28:31], v68, s[18:19] offset:3072
	v_mov_b32_e32 v68, v219
	s_waitcnt vmcnt(5)
	v_mfma_f32_16x16x4_f32 v[4:7], v52, v40, v[4:7]
	v_mfma_f32_16x16x4_f32 v[8:11], v52, v41, v[8:11]
	s_waitcnt vmcnt(4)
	v_mfma_f32_16x16x4_f32 v[4:7], v53, v44, v[4:7]
	v_add_co_u32_e32 v44, vcc, s48, v32
	v_mfma_f32_16x16x4_f32 v[8:11], v53, v45, v[8:11]
	s_nop 0
	v_addc_co_u32_e32 v45, vcc, 0, v33, vcc
	v_mfma_f32_16x16x4_f32 v[12:15], v52, v42, v[12:15]
	v_mfma_f32_16x16x4_f32 v[0:3], v52, v43, v[0:3]
	global_load_dwordx4 v[32:35], v[44:45], off
	global_load_dwordx4 v[36:39], v[44:45], off offset:1024
	global_load_dwordx4 v[40:43], v[44:45], off offset:2048
	global_load_dwordx4 v[48:51], v[44:45], off offset:3072
	ds_read2_b32 v[44:45], v211 offset0:160 offset1:164
	v_mfma_f32_16x16x4_f32 v[12:15], v53, v46, v[12:15]
	v_mfma_f32_16x16x4_f32 v[0:3], v53, v47, v[0:3]
	ds_read2_b32 v[52:53], v211 offset0:184 offset1:188
	s_waitcnt vmcnt(6) lgkmcnt(1)
	v_mfma_f32_16x16x4_f32 v[4:7], v44, v16, v[4:7]
	v_mfma_f32_16x16x4_f32 v[8:11], v44, v17, v[8:11]
	ds_read2_b32 v[16:17], v211 offset0:168 offset1:172
	v_mfma_f32_16x16x4_f32 v[12:15], v44, v18, v[12:15]
	v_mfma_f32_16x16x4_f32 v[0:3], v44, v19, v[0:3]
	v_mfma_f32_16x16x4_f32 v[4:7], v45, v20, v[4:7]
	v_mfma_f32_16x16x4_f32 v[8:11], v45, v21, v[8:11]
	v_mfma_f32_16x16x4_f32 v[12:15], v45, v22, v[12:15]
	v_mfma_f32_16x16x4_f32 v[0:3], v45, v23, v[0:3]
	global_load_dwordx4 v[20:23], v68, s[18:19] offset:1024
	s_waitcnt vmcnt(6) lgkmcnt(0)
	v_mfma_f32_16x16x4_f32 v[4:7], v16, v24, v[4:7]
	v_mfma_f32_16x16x4_f32 v[8:11], v16, v25, v[8:11]
	v_mfma_f32_16x16x4_f32 v[12:15], v16, v26, v[12:15]
	v_mfma_f32_16x16x4_f32 v[0:3], v16, v27, v[0:3]
	s_waitcnt vmcnt(5)
	v_mfma_f32_16x16x4_f32 v[4:7], v17, v28, v[4:7]
	v_mfma_f32_16x16x4_f32 v[8:11], v17, v29, v[8:11]
	v_mfma_f32_16x16x4_f32 v[12:15], v17, v30, v[12:15]
	v_mfma_f32_16x16x4_f32 v[0:3], v17, v31, v[0:3]
	ds_read2_b32 v[16:17], v211 offset0:176 offset1:180
	s_waitcnt vmcnt(4) lgkmcnt(0)
	v_mfma_f32_16x16x4_f32 v[4:7], v16, v32, v[4:7]
	v_mfma_f32_16x16x4_f32 v[8:11], v16, v33, v[8:11]
	v_lshl_add_u64 v[32:33], s[18:19], 0, v[68:69]
	v_add_co_u32_e32 v44, vcc, s48, v32
	s_nop 1
	v_addc_co_u32_e32 v45, vcc, 0, v33, vcc
	v_mfma_f32_16x16x4_f32 v[12:15], v16, v34, v[12:15]
	v_mfma_f32_16x16x4_f32 v[0:3], v16, v35, v[0:3]
	s_waitcnt vmcnt(3)
	v_mfma_f32_16x16x4_f32 v[4:7], v17, v36, v[4:7]
	v_mfma_f32_16x16x4_f32 v[8:11], v17, v37, v[8:11]
	v_mfma_f32_16x16x4_f32 v[12:15], v17, v38, v[12:15]
	v_mfma_f32_16x16x4_f32 v[0:3], v17, v39, v[0:3]
	global_load_dwordx4 v[16:19], v68, s[18:19]
	global_load_dwordx4 v[24:27], v68, s[18:19] offset:2048
	global_load_dwordx4 v[28:31], v68, s[18:19] offset:3072
	v_mov_b32_e32 v68, v220
	s_waitcnt vmcnt(5)
	v_mfma_f32_16x16x4_f32 v[4:7], v52, v40, v[4:7]
	v_mfma_f32_16x16x4_f32 v[8:11], v52, v41, v[8:11]
	v_mfma_f32_16x16x4_f32 v[12:15], v52, v42, v[12:15]
	v_mfma_f32_16x16x4_f32 v[0:3], v52, v43, v[0:3]
	global_load_dwordx4 v[32:35], v[44:45], off
	global_load_dwordx4 v[36:39], v[44:45], off offset:1024
	global_load_dwordx4 v[40:43], v[44:45], off offset:2048
	s_nop 0
	global_load_dwordx4 v[44:47], v[44:45], off offset:3072
	s_waitcnt vmcnt(8)
	v_mfma_f32_16x16x4_f32 v[4:7], v53, v48, v[4:7]
	v_mfma_f32_16x16x4_f32 v[8:11], v53, v49, v[8:11]
	ds_read2_b32 v[48:49], v211 offset0:192 offset1:196
	v_mfma_f32_16x16x4_f32 v[12:15], v53, v50, v[12:15]
	v_mfma_f32_16x16x4_f32 v[0:3], v53, v51, v[0:3]
	s_waitcnt vmcnt(6) lgkmcnt(0)
	v_mfma_f32_16x16x4_f32 v[4:7], v48, v16, v[4:7]
	v_mfma_f32_16x16x4_f32 v[8:11], v48, v17, v[8:11]
	ds_read2_b32 v[16:17], v211 offset0:200 offset1:204
	v_mfma_f32_16x16x4_f32 v[12:15], v48, v18, v[12:15]
	v_mfma_f32_16x16x4_f32 v[0:3], v48, v19, v[0:3]
	v_mfma_f32_16x16x4_f32 v[4:7], v49, v20, v[4:7]
	v_mfma_f32_16x16x4_f32 v[8:11], v49, v21, v[8:11]
	v_mfma_f32_16x16x4_f32 v[12:15], v49, v22, v[12:15]
	v_mfma_f32_16x16x4_f32 v[0:3], v49, v23, v[0:3]
	global_load_dwordx4 v[20:23], v68, s[18:19] offset:1024
	s_waitcnt vmcnt(6) lgkmcnt(0)
	v_mfma_f32_16x16x4_f32 v[4:7], v16, v24, v[4:7]
	v_mfma_f32_16x16x4_f32 v[8:11], v16, v25, v[8:11]
	ds_read2_b32 v[24:25], v211 offset0:216 offset1:220
	v_mfma_f32_16x16x4_f32 v[12:15], v16, v26, v[12:15]
	v_mfma_f32_16x16x4_f32 v[0:3], v16, v27, v[0:3]
	s_waitcnt vmcnt(5)
	v_mfma_f32_16x16x4_f32 v[4:7], v17, v28, v[4:7]
	v_mfma_f32_16x16x4_f32 v[8:11], v17, v29, v[8:11]
	ds_read2_b32 v[28:29], v211 offset0:224 offset1:228
	v_mfma_f32_16x16x4_f32 v[12:15], v17, v30, v[12:15]
	v_mfma_f32_16x16x4_f32 v[0:3], v17, v31, v[0:3]
	ds_read2_b32 v[16:17], v211 offset0:208 offset1:212
	s_waitcnt vmcnt(4) lgkmcnt(0)
	v_mfma_f32_16x16x4_f32 v[4:7], v16, v32, v[4:7]
	v_mfma_f32_16x16x4_f32 v[8:11], v16, v33, v[8:11]
	v_mfma_f32_16x16x4_f32 v[12:15], v16, v34, v[12:15]
	v_mfma_f32_16x16x4_f32 v[0:3], v16, v35, v[0:3]
	s_waitcnt vmcnt(3)
	v_mfma_f32_16x16x4_f32 v[4:7], v17, v36, v[4:7]
	v_mfma_f32_16x16x4_f32 v[8:11], v17, v37, v[8:11]
	v_mfma_f32_16x16x4_f32 v[12:15], v17, v38, v[12:15]
	v_mfma_f32_16x16x4_f32 v[0:3], v17, v39, v[0:3]
	global_load_dwordx4 v[16:19], v68, s[18:19]
	s_waitcnt vmcnt(3)
	v_mfma_f32_16x16x4_f32 v[4:7], v24, v40, v[4:7]
	v_mfma_f32_16x16x4_f32 v[8:11], v24, v41, v[8:11]
	v_mfma_f32_16x16x4_f32 v[12:15], v24, v42, v[12:15]
	v_mfma_f32_16x16x4_f32 v[0:3], v24, v43, v[0:3]
	s_waitcnt vmcnt(2)
	v_mfma_f32_16x16x4_f32 v[4:7], v25, v44, v[4:7]
	v_mfma_f32_16x16x4_f32 v[8:11], v25, v45, v[8:11]
	v_mfma_f32_16x16x4_f32 v[12:15], v25, v46, v[12:15]
	v_mfma_f32_16x16x4_f32 v[0:3], v25, v47, v[0:3]
	global_load_dwordx4 v[24:27], v68, s[18:19] offset:3072
	s_waitcnt vmcnt(1)
	v_mfma_f32_16x16x4_f32 v[4:7], v28, v16, v[4:7]
	v_mfma_f32_16x16x4_f32 v[8:11], v28, v17, v[8:11]
	v_mfma_f32_16x16x4_f32 v[12:15], v28, v18, v[12:15]
	v_mfma_f32_16x16x4_f32 v[0:3], v28, v19, v[0:3]
	global_load_dwordx4 v[16:19], v68, s[18:19] offset:2048
	v_mfma_f32_16x16x4_f32 v[4:7], v29, v20, v[4:7]
	v_mfma_f32_16x16x4_f32 v[8:11], v29, v21, v[8:11]
	v_mfma_f32_16x16x4_f32 v[12:15], v29, v22, v[12:15]
	v_mfma_f32_16x16x4_f32 v[0:3], v29, v23, v[0:3]
	ds_read2_b32 v[28:29], v211 offset0:232 offset1:236
	s_waitcnt vmcnt(0) lgkmcnt(0)
	v_mfma_f32_16x16x4_f32 v[4:7], v28, v16, v[4:7]
	v_mfma_f32_16x16x4_f32 v[8:11], v28, v17, v[8:11]
	v_lshl_add_u64 v[16:17], s[18:19], 0, v[68:69]
	v_add_co_u32_e32 v30, vcc, s48, v16
	s_mov_b64 s[18:19], -1
	s_nop 0
	v_addc_co_u32_e32 v31, vcc, 0, v17, vcc
	global_load_dwordx4 v[20:23], v[30:31], off offset:1024
	v_mfma_f32_16x16x4_f32 v[12:15], v28, v18, v[12:15]
	v_mfma_f32_16x16x4_f32 v[0:3], v28, v19, v[0:3]
	global_load_dwordx4 v[16:19], v[30:31], off
	v_mfma_f32_16x16x4_f32 v[4:7], v29, v24, v[4:7]
	v_mfma_f32_16x16x4_f32 v[8:11], v29, v25, v[8:11]
	v_mfma_f32_16x16x4_f32 v[12:15], v29, v26, v[12:15]
	v_mfma_f32_16x16x4_f32 v[0:3], v29, v27, v[0:3]
	ds_read2_b32 v[28:29], v211 offset0:240 offset1:244
	global_load_dwordx4 v[24:27], v[30:31], off offset:3072
	s_waitcnt vmcnt(1) lgkmcnt(0)
	v_mfma_f32_16x16x4_f32 v[4:7], v28, v16, v[4:7]
	v_mfma_f32_16x16x4_f32 v[8:11], v28, v17, v[8:11]
	v_mfma_f32_16x16x4_f32 v[12:15], v28, v18, v[12:15]
	v_mfma_f32_16x16x4_f32 v[0:3], v28, v19, v[0:3]
	global_load_dwordx4 v[16:19], v[30:31], off offset:2048
	v_mfma_f32_16x16x4_f32 v[4:7], v29, v20, v[4:7]
	v_mfma_f32_16x16x4_f32 v[8:11], v29, v21, v[8:11]
	ds_read2_b32 v[20:21], v211 offset0:248 offset1:252
	s_waitcnt lgkmcnt(0)
	s_barrier
	v_mfma_f32_16x16x4_f32 v[12:15], v29, v22, v[12:15]
	v_mfma_f32_16x16x4_f32 v[0:3], v29, v23, v[0:3]
	s_waitcnt vmcnt(0)
	v_mfma_f32_16x16x4_f32 v[4:7], v20, v16, v[4:7]
	v_mfma_f32_16x16x4_f32 v[8:11], v20, v17, v[8:11]
	v_mfma_f32_16x16x4_f32 v[12:15], v20, v18, v[12:15]
	v_mfma_f32_16x16x4_f32 v[0:3], v20, v19, v[0:3]
	v_mfma_f32_16x16x4_f32 v[4:7], v21, v24, v[4:7]
	v_mfma_f32_16x16x4_f32 v[8:11], v21, v25, v[8:11]
	s_nop 8
	v_mov_b32_e32 v16, v4
	v_mfma_f32_16x16x4_f32 v[12:15], v21, v26, v[12:15]
	v_mov_b32_e32 v17, v8
	v_mfma_f32_16x16x4_f32 v[0:3], v21, v27, v[0:3]
	s_nop 7
	v_mov_b32_e32 v18, v12
	s_nop 0
	v_mov_b32_e32 v19, v0
	ds_write_b128 v222, v[16:19]
	v_mov_b32_e32 v16, v5
	v_mov_b32_e32 v17, v9
	v_mov_b32_e32 v18, v13
	v_mov_b32_e32 v19, v1
	ds_write_b128 v222, v[16:19] offset:256
	v_mov_b32_e32 v16, v6
	v_mov_b32_e32 v17, v10
	v_mov_b32_e32 v18, v14
	v_mov_b32_e32 v19, v2
	v_mov_b32_e32 v0, v7
	v_mov_b32_e32 v1, v11
	v_mov_b32_e32 v2, v15
	ds_write_b128 v222, v[16:19] offset:512
	ds_write_b128 v222, v[0:3] offset:768
	s_waitcnt lgkmcnt(0)
	s_barrier
	s_branch .LBB0_2473
